# SGU unit: norm gain loaded once per unit (kept in v160-167) instead of a global load + wait per token row
# baseline (speedup 1.0000x reference)
; #define LAS __attribute__((address_space(3)))
; __device__ __forceinline__ unsigned cvt_pk_bf16(float lo, float hi) { const f32x2 v = {lo, hi}; const bf16x2_t b = __builtin_convertvector(v, bf16x2_t); return __builtin_bit_cast(unsigned, b); }
; __device__ __forceinline__ void sgu_unit(const Params& p, int l, int un, LAS unsigned char* lds) {
;     ...
;     const float* Wg = p.in[I_SGUW] + ((size_t)l * 4 + h) * 128 * 128;
;     f32x4 wq[8]; u32x4 vv[16];
; #pragma unroll
;     for (int i = 0; i < 8; ++i) wq[i] = *(const f32x4*)(Wg + (i * 512 + tid) * 4);
; #pragma unroll
;     for (int qi = 0; qi < 16; ++qi) vv[qi] = *(const u32x4*)(P + (size_t)(row0 + wave * 16 + qi) * INP + C_SGU_V + lane * 8);
; #pragma unroll
;     for (int i = 0; i < 8; ++i) { const int e4 = (i * 512 + tid) * 4, r = e4 >> 7, c = e4 & 127; const f32x4 v = wq[i];
;         u32x2 w; w.x = cvt_pk_bf16(v[0], v[1]); w.y = cvt_pk_bf16(v[2], v[3]); *(LAS u32x2*)(Wl + r * 136 + c) = w; }
; __device__ __forceinline__ void ph_rowsplit(const Params& p, int l, LAS unsigned char* lds) {
;     ...
;         if (k < nmine) it = B_ROWITEMS + c_ + k * G_;
;         else { if (rit >= rend) break; it = rit; rit += rstride; }
;         if (it < B_ROWITEMS) {
;             const int row = it * 8 + wave;
;             if (gridDim.x == 256) b_row<true, false>(p, ws, l, row, lane); else b_row<true, true>(p, ws, l, row, lane);
;         } else if (it < B_ROWITEMS + B_SGU) {
;             sgu_unit(p, l, it - B_ROWITEMS, lds);
.LBB0_474:
	s_and_b64 vcc, exec, s[2:3]
	s_cbranch_vccz .LBB0_539
	s_cmpk_gt_i32 s31, 0x47f
	s_cbranch_scc0 .LBB0_511
	s_cmpk_gt_u32 s31, 0x59f
	s_cbranch_scc1 .LBB0_510
	v_mov_b32_e32 v64, v0
	s_mov_b64 s[0:1], 0
	s_add_u32 s42, s84, s0
	s_addc_u32 s43, s85, s1
	s_add_u32 s14, s42, 0x1f1b8000
	s_addc_u32 s15, s43, 0
	s_and_b32 s0, s31, 3
	v_readlane_b32 s44, v251, 16
	s_lshl_b32 s19, s0, 7
	v_readlane_b32 s45, v251, 17
	v_readlane_b32 s46, v251, 18
	v_readlane_b32 s47, v251, 19
	v_readlane_b32 s48, v251, 20
	v_readlane_b32 s49, v251, 21
	v_readlane_b32 s50, v251, 22
	v_readlane_b32 s51, v251, 23
	s_lshl_b32 s1, s31, 5
	s_or_b32 s4, s19, s18
	v_readlane_b32 s52, v251, 24
	v_readlane_b32 s53, v251, 25
	v_readlane_b32 s54, v251, 26
	v_readlane_b32 s55, v251, 27
	s_mov_b64 s[44:45], s[48:49]
	s_add_i32 s1, s1, 0x7fff7000
	s_lshl_b64 s[2:3], s[4:5], 9
	s_mov_b64 s[46:47], s[50:51]
	s_add_u32 s2, s46, s2
	v_lshlrev_b32_e32 v2, 2, v64
	s_addc_u32 s3, s47, s3
	v_ashrrev_i32_e32 v3, 31, v2
	v_add_u32_e32 v62, 0x800, v2
	v_lshl_add_u64 v[4:5], v[2:3], 2, s[2:3]
	v_ashrrev_i32_e32 v63, 31, v62
	v_lshl_add_u64 v[6:7], v[62:63], 2, s[2:3]
	global_load_dwordx4 v[66:69], v[4:5], off
	global_load_dwordx4 v[70:73], v[6:7], off
	v_add_u32_e32 v126, 0x1000, v2
	v_ashrrev_i32_e32 v127, 31, v126
	v_add_u32_e32 v128, 0x1800, v2
	v_lshl_add_u64 v[4:5], v[126:127], 2, s[2:3]
	v_ashrrev_i32_e32 v129, 31, v128
	v_lshl_add_u64 v[6:7], v[128:129], 2, s[2:3]
	global_load_dwordx4 v[98:101], v[4:5], off
	global_load_dwordx4 v[102:105], v[6:7], off
	v_add_u32_e32 v130, 0x2000, v2
	v_ashrrev_i32_e32 v131, 31, v130
	v_add_u32_e32 v132, 0x2800, v2
	v_lshl_add_u64 v[4:5], v[130:131], 2, s[2:3]
	v_ashrrev_i32_e32 v133, 31, v132
	v_lshl_add_u64 v[6:7], v[132:133], 2, s[2:3]
	global_load_dwordx4 v[106:109], v[4:5], off
	global_load_dwordx4 v[110:113], v[6:7], off
	v_add_u32_e32 v134, 0x3000, v2
	v_add_u32_e32 v136, 0x3800, v2
	v_ashrrev_i32_e32 v135, 31, v134
	v_ashrrev_i32_e32 v137, 31, v136
	v_ashrrev_i32_e32 v127, 6, v64
	v_lshl_add_u64 v[4:5], v[134:135], 2, s[2:3]
	v_lshl_add_u64 v[2:3], v[136:137], 2, s[2:3]
	s_and_b32 s60, s1, 0x7fffff80
	v_lshlrev_b32_e32 v65, 4, v127
	v_and_b32_e32 v8, 63, v64
	global_load_dwordx4 v[114:117], v[4:5], off
	global_load_dwordx4 v[118:121], v[2:3], off
	v_add_u32_e32 v9, s60, v65
	v_mov_b64_e32 v[2:3], s[14:15]
	s_movk_i32 s1, 0x1e00
	v_mad_i64_i32 v[4:5], s[2:3], v9, s1, v[2:3]
	v_lshlrev_b32_e32 v206, 4, v8
	v_or_b32_e32 v6, 1, v9
	v_lshl_add_u64 v[4:5], v[4:5], 0, v[206:207]
	v_mad_i64_i32 v[6:7], s[2:3], v6, s1, v[2:3]
	v_lshl_add_u64 v[6:7], v[6:7], 0, v[206:207]
	global_load_dwordx4 v[122:125], v[4:5], off offset:1024
	global_load_dwordx4 v[58:61], v[6:7], off offset:1024
	v_or_b32_e32 v4, 2, v9
	v_or_b32_e32 v6, 3, v9
	v_mad_i64_i32 v[4:5], s[2:3], v4, s1, v[2:3]
	v_mad_i64_i32 v[6:7], s[2:3], v6, s1, v[2:3]
	v_lshl_add_u64 v[4:5], v[4:5], 0, v[206:207]
	v_lshl_add_u64 v[6:7], v[6:7], 0, v[206:207]
	global_load_dwordx4 v[54:57], v[4:5], off offset:1024
	global_load_dwordx4 v[50:53], v[6:7], off offset:1024
	v_or_b32_e32 v4, 4, v9
	v_or_b32_e32 v6, 5, v9
	v_mad_i64_i32 v[4:5], s[2:3], v4, s1, v[2:3]
	v_mad_i64_i32 v[6:7], s[2:3], v6, s1, v[2:3]
	v_lshl_add_u64 v[4:5], v[4:5], 0, v[206:207]
	v_lshl_add_u64 v[6:7], v[6:7], 0, v[206:207]
	global_load_dwordx4 v[46:49], v[4:5], off offset:1024
	global_load_dwordx4 v[42:45], v[6:7], off offset:1024
	v_or_b32_e32 v4, 6, v9
	v_or_b32_e32 v6, 7, v9
	v_mad_i64_i32 v[4:5], s[2:3], v4, s1, v[2:3]
	v_mad_i64_i32 v[6:7], s[2:3], v6, s1, v[2:3]
	v_lshl_add_u64 v[4:5], v[4:5], 0, v[206:207]
	v_lshl_add_u64 v[6:7], v[6:7], 0, v[206:207]
	global_load_dwordx4 v[38:41], v[4:5], off offset:1024
	global_load_dwordx4 v[34:37], v[6:7], off offset:1024
	v_or_b32_e32 v4, 8, v9
	v_or_b32_e32 v6, 9, v9
	v_mad_i64_i32 v[4:5], s[2:3], v4, s1, v[2:3]
	v_mad_i64_i32 v[6:7], s[2:3], v6, s1, v[2:3]
	v_lshl_add_u64 v[4:5], v[4:5], 0, v[206:207]
	v_lshl_add_u64 v[6:7], v[6:7], 0, v[206:207]
	global_load_dwordx4 v[30:33], v[4:5], off offset:1024
	global_load_dwordx4 v[26:29], v[6:7], off offset:1024
	v_or_b32_e32 v4, 10, v9
	v_or_b32_e32 v6, 11, v9
	v_mad_i64_i32 v[4:5], s[2:3], v4, s1, v[2:3]
	v_mad_i64_i32 v[6:7], s[2:3], v6, s1, v[2:3]
	v_lshl_add_u64 v[4:5], v[4:5], 0, v[206:207]
	v_lshl_add_u64 v[6:7], v[6:7], 0, v[206:207]
	global_load_dwordx4 v[22:25], v[4:5], off offset:1024
	global_load_dwordx4 v[18:21], v[6:7], off offset:1024
	v_or_b32_e32 v4, 12, v9
	v_or_b32_e32 v6, 13, v9
	v_mad_i64_i32 v[4:5], s[2:3], v4, s1, v[2:3]
	v_mad_i64_i32 v[6:7], s[2:3], v6, s1, v[2:3]
	v_lshl_add_u64 v[4:5], v[4:5], 0, v[206:207]
	v_lshl_add_u64 v[6:7], v[6:7], 0, v[206:207]
	v_lshlrev_b32_e32 v129, 3, v64
	global_load_dwordx4 v[14:17], v[4:5], off offset:1024
	global_load_dwordx4 v[10:13], v[6:7], off offset:1024
	v_or_b32_e32 v4, 14, v9
	v_or_b32_e32 v6, 15, v9
	v_and_b32_e32 v63, 0xf8, v129
	v_mad_i64_i32 v[4:5], s[2:3], v4, s1, v[2:3]
	v_mad_i64_i32 v[2:3], s[2:3], v6, s1, v[2:3]
	v_add_u32_e32 v138, 0, v63
	v_bfe_i32 v63, v64, 5, 25
	s_movk_i32 s44, 0x110
	v_lshl_add_u64 v[4:5], v[4:5], 0, v[206:207]
	v_lshl_add_u64 v[2:3], v[2:3], 0, v[206:207]
	s_waitcnt vmcnt(21)
	v_cvt_pk_bf16_f32 v66, v66, v67
	v_cvt_pk_bf16_f32 v67, v68, v69
	v_mad_u64_u32 v[68:69], s[2:3], v63, s44, v[138:139]
	global_load_dwordx4 v[6:9], v[4:5], off offset:1024
	s_nop 0
	global_load_dwordx4 v[2:5], v[2:3], off offset:1024
	ds_write_b64 v68, v[66:67]
	v_ashrrev_i32_e32 v66, 7, v62
	s_waitcnt vmcnt(22)
	v_cvt_pk_bf16_f32 v62, v70, v71
	v_cvt_pk_bf16_f32 v63, v72, v73
	v_mad_u64_u32 v[66:67], s[2:3], v66, s44, v[138:139]
	ds_write_b64 v66, v[62:63]
	v_ashrrev_i32_e32 v66, 7, v126
	s_waitcnt vmcnt(21)
; #define LAS __attribute__((address_space(3)))
; __device__ __forceinline__ unsigned cvt_pk_bf16(float lo, float hi) { const f32x2 v = {lo, hi}; const bf16x2_t b = __builtin_convertvector(v, bf16x2_t); return __builtin_bit_cast(unsigned, b); }
; __device__ __forceinline__ float bflo(unsigned w) { return __uint_as_float(w << 16); }
; __device__ __forceinline__ float bfhi(unsigned w) { return __uint_as_float(w & 0xffff0000u); }
; __device__ __forceinline__ unsigned short f2bf(float f) { return (unsigned short)(cvt_pk_bf16(f, 0.f) & 0xffffu); }
; __device__ __forceinline__ void sgu_unit(const Params& p, int l, int un, LAS unsigned char* lds) {
;     ...
;     for (int i = 0; i < 8; ++i) { const int e4 = (i * 512 + tid) * 4, r = e4 >> 7, c = e4 & 127; const f32x4 v = wq[i];
;         u32x2 w; w.x = cvt_pk_bf16(v[0], v[1]); w.y = cvt_pk_bf16(v[2], v[3]); *(LAS u32x2*)(Wl + r * 136 + c) = w; }
; #pragma unroll
;     for (int qi = 0; qi < 16; ++qi) { const int q = wave * 16 + qi;
;         const u32x4 v = vv[qi]; float f[8] = {bflo(v.x), bfhi(v.x), bflo(v.y), bfhi(v.y), bflo(v.z), bfhi(v.z), bflo(v.w), bfhi(v.w)}; float ss = 0.f;
; #pragma unroll
;         for (int j = 0; j < 8; ++j) { f[j] = gelu_tanh(f[j]); ss += f[j] * f[j]; }
;         ss = wave_sum(ss); const float rinv = rsqrtf(ss * (1.0f / 512.0f) + EPS);
;         if ((lane >> 4) == h) { const int c0 = (lane & 15) * 8; const float* g = p.in[I_SGUNG] + l * 512 + h * 128 + c0;
; #pragma unroll
;             for (int j = 0; j < 8; ++j) Vl[(c0 + j) * 136 + q] = f2bf(f[j] * rinv * g[j]); } }
	v_cvt_pk_bf16_f32 v62, v98, v99
	v_cvt_pk_bf16_f32 v63, v100, v101
	v_mad_u64_u32 v[66:67], s[2:3], v66, s44, v[138:139]
	ds_write_b64 v66, v[62:63]
	v_ashrrev_i32_e32 v66, 7, v128
	s_waitcnt vmcnt(20)
	v_cvt_pk_bf16_f32 v62, v102, v103
	v_cvt_pk_bf16_f32 v63, v104, v105
	v_mad_u64_u32 v[66:67], s[2:3], v66, s44, v[138:139]
	ds_write_b64 v66, v[62:63]
	v_ashrrev_i32_e32 v66, 7, v130
	s_waitcnt vmcnt(19)
	v_cvt_pk_bf16_f32 v62, v106, v107
	v_cvt_pk_bf16_f32 v63, v108, v109
	v_mad_u64_u32 v[66:67], s[2:3], v66, s44, v[138:139]
	ds_write_b64 v66, v[62:63]
	v_ashrrev_i32_e32 v66, 7, v132
	s_waitcnt vmcnt(18)
	v_cvt_pk_bf16_f32 v62, v110, v111
	v_cvt_pk_bf16_f32 v63, v112, v113
	v_mad_u64_u32 v[66:67], s[2:3], v66, s44, v[138:139]
	ds_write_b64 v66, v[62:63]
	v_ashrrev_i32_e32 v66, 7, v134
	s_waitcnt vmcnt(17)
	v_cvt_pk_bf16_f32 v62, v114, v115
	v_cvt_pk_bf16_f32 v63, v116, v117
	v_mad_u64_u32 v[66:67], s[2:3], v66, s44, v[138:139]
	ds_write_b64 v66, v[62:63]
	v_ashrrev_i32_e32 v66, 7, v136
	v_mad_u64_u32 v[66:67], s[2:3], v66, s44, v[138:139]
	s_waitcnt vmcnt(15)
	v_and_b32_e32 v67, 0xffff0000, v122
	v_mul_f32_e32 v77, 0x3dd2d3e8, v67
	v_fma_f32 v77, -v77, v67, s33
	v_mul_f32_e32 v77, v77, v67
	v_exp_f32_e32 v77, v77
	v_cvt_pk_bf16_f32 v62, v118, v119
	v_cvt_pk_bf16_f32 v63, v120, v121
	ds_write_b64 v66, v[62:63]
	v_lshlrev_b32_e32 v66, 16, v122
	v_add_f32_e32 v77, 1.0, v77
	v_mul_f32_e32 v73, 0x3dd2d3e8, v66
	v_rcp_f32_e32 v77, v77
	v_fma_f32 v73, -v73, v66, s33
	v_mul_f32_e32 v73, v73, v66
	v_lshlrev_b32_e32 v70, 16, v123
	v_exp_f32_e32 v73, v73
	v_mul_f32_e32 v102, v77, v67
	v_mul_f32_e32 v67, 0x3dd2d3e8, v70
	v_fma_f32 v67, -v67, v70, s33
	v_mul_f32_e32 v67, v67, v70
	v_add_f32_e32 v73, 1.0, v73
	v_exp_f32_e32 v67, v67
	v_rcp_f32_e32 v73, v73
	v_lshlrev_b32_e32 v72, 16, v124
	v_and_b32_e32 v71, 0xffff0000, v123
	v_add_f32_e32 v67, 1.0, v67
	v_mul_f32_e32 v77, 0x3dd2d3e8, v72
	v_mul_f32_e32 v104, v73, v66
	v_mul_f32_e32 v73, 0x3dd2d3e8, v71
	v_rcp_f32_e32 v67, v67
	v_fma_f32 v77, -v77, v72, s33
	v_fma_f32 v73, -v73, v71, s33
	v_mul_f32_e32 v77, v77, v72
	v_mul_f32_e32 v73, v73, v71
	v_exp_f32_e32 v77, v77
	v_and_b32_e32 v98, 0xffff0000, v124
	v_exp_f32_e32 v73, v73
	v_mul_f32_e32 v103, v67, v70
	v_mul_f32_e32 v70, 0x3dd2d3e8, v98
	v_fma_f32 v70, -v70, v98, s33
	v_add_f32_e32 v67, 1.0, v77
	v_mul_f32_e32 v70, v70, v98
	v_add_f32_e32 v73, 1.0, v73
	v_rcp_f32_e32 v67, v67
	v_exp_f32_e32 v70, v70
	v_rcp_f32_e32 v73, v73
	v_lshlrev_b32_e32 v105, 16, v125
	v_and_b32_e32 v106, 0xffff0000, v125
	v_mul_f32_e32 v99, v67, v72
	v_add_f32_e32 v67, 1.0, v70
	v_mul_f32_e32 v70, 0x3dd2d3e8, v105
	v_mul_f32_e32 v101, v73, v71
	v_fma_f32 v70, -v70, v105, s33
	v_mul_f32_e32 v71, 0x3dd2d3e8, v106
	v_mul_f32_e32 v70, v70, v105
	v_fma_f32 v71, -v71, v106, s33
	v_rcp_f32_e32 v67, v67
	v_exp_f32_e32 v70, v70
	v_mul_f32_e32 v71, v71, v106
	v_exp_f32_e32 v71, v71
	v_mul_f32_e32 v66, v102, v102
	v_mul_f32_e32 v100, v67, v98
	v_add_f32_e32 v67, 1.0, v70
	v_fmac_f32_e32 v66, v104, v104
	v_rcp_f32_e32 v67, v67
	v_add_f32_e32 v70, 1.0, v71
	v_fmac_f32_e32 v66, v103, v103
	v_rcp_f32_e32 v70, v70
	v_and_b32_e32 v62, 64, v249
	v_fmac_f32_e32 v66, v101, v101
	v_add_u32_e32 v62, 64, v62
	v_xor_b32_e32 v63, 32, v249
	v_fmac_f32_e32 v66, v99, v99
	v_cmp_lt_i32_e32 vcc, v63, v62
	v_fmac_f32_e32 v66, v100, v100
	v_mul_f32_e32 v98, v67, v105
	v_cndmask_b32_e32 v63, v249, v63, vcc
	v_fmac_f32_e32 v66, v98, v98
	v_mul_f32_e32 v77, v70, v106
	v_lshlrev_b32_e32 v68, 2, v63
	v_fmac_f32_e32 v66, v77, v77
	v_mov_b32_e32 v67, v66
	s_nop 1
	v_permlane32_swap_b32_e32 v67, v66
	v_xor_b32_e32 v63, 16, v249
	v_cmp_lt_i32_e32 vcc, v63, v62
	v_lshl_add_u32 v107, v127, 5, 0
	v_readlane_b32 s56, v251, 28
	v_cndmask_b32_e32 v63, v249, v63, vcc
	v_lshlrev_b32_e32 v69, 2, v63
	s_waitcnt lgkmcnt(0)
	v_add_f32_e32 v66, v66, v67
	v_mov_b32_e32 v67, v66
	s_nop 1
	v_permlane16_swap_b32_e32 v67, v66
	v_xor_b32_e32 v63, 8, v249
	v_cmp_lt_i32_e32 vcc, v63, v62
	v_readlane_b32 s57, v251, 29
	v_readlane_b32 s58, v251, 30
	v_cndmask_b32_e32 v63, v249, v63, vcc
	v_lshlrev_b32_e32 v70, 2, v63
	s_waitcnt lgkmcnt(0)
	v_add_f32_e32 v66, v66, v67
	s_nop 1
	v_mov_b32_dpp v67, v66 row_ror:8 row_mask:0xf bank_mask:0xf
	v_xor_b32_e32 v63, 4, v249
	v_cmp_lt_i32_e32 vcc, v63, v62
	v_readlane_b32 s59, v251, 31
	s_mov_b64 s[48:49], s[52:53]
	v_cndmask_b32_e32 v63, v249, v63, vcc
	v_lshlrev_b32_e32 v71, 2, v63
	v_xor_b32_e32 v63, 2, v249
	s_waitcnt lgkmcnt(0)
	v_add_f32_e32 v67, v66, v67
	v_cmp_lt_i32_e32 vcc, v63, v62
	s_nop 1
	v_mov_b32_dpp v105, v67 row_shl:4 row_mask:0xf bank_mask:0x5
	v_mov_b32_dpp v105, v67 row_shr:4 row_mask:0xf bank_mask:0xa
	v_bfe_u32 v66, v64, 4, 2
	v_cndmask_b32_e32 v63, v249, v63, vcc
	v_lshlrev_b32_e32 v72, 2, v63
	v_xor_b32_e32 v63, 1, v249
	v_cmp_lt_i32_e32 vcc, v63, v62
	s_mov_b64 s[50:51], s[54:55]
	s_nop 0
	v_cndmask_b32_e32 v62, v249, v63, vcc
	v_lshlrev_b32_e32 v73, 2, v62
	s_waitcnt lgkmcnt(0)
	v_add_f32_e32 v62, v67, v105
	s_nop 1
	v_mov_b32_dpp v63, v62 quad_perm:[2,3,0,1] row_mask:0xf bank_mask:0xf
	v_cmp_eq_u32_e32 vcc, s0, v66
	s_lshl_b32 s0, s0, 9
	v_and_b32_e32 v67, 0x78, v129
	s_add_u32 s0, s25, s0
	s_waitcnt lgkmcnt(0)
	v_add_f32_e32 v105, v62, v63
	s_nop 1
	v_mov_b32_dpp v106, v105 quad_perm:[1,0,3,2] row_mask:0xf bank_mask:0xf
	s_addc_u32 s1, s26, 0
	v_lshlrev_b32_e32 v206, 2, v67
	v_lshl_add_u64 v[62:63], s[0:1], 0, v[206:207]
	v_mad_u32_u24 v67, v67, s44, v107
	s_and_saveexec_b64 s[0:1], vcc
	s_cbranch_execz .LBB0_479
; __device__ __forceinline__ float bflo(unsigned w) { return __uint_as_float(w << 16); }
; __device__ __forceinline__ float bfhi(unsigned w) { return __uint_as_float(w & 0xffff0000u); }
; __device__ __forceinline__ unsigned short f2bf(float f) { return (unsigned short)(cvt_pk_bf16(f, 0.f) & 0xffffu); }
; __device__ __forceinline__ void sgu_unit(const Params& p, int l, int un, LAS unsigned char* lds) {
;     ...
;     for (int qi = 0; qi < 16; ++qi) { const int q = wave * 16 + qi;
;         const u32x4 v = vv[qi]; float f[8] = {bflo(v.x), bfhi(v.x), bflo(v.y), bfhi(v.y), bflo(v.z), bfhi(v.z), bflo(v.w), bfhi(v.w)}; float ss = 0.f;
; #pragma unroll
;         for (int j = 0; j < 8; ++j) { f[j] = gelu_tanh(f[j]); ss += f[j] * f[j]; }
;         ss = wave_sum(ss); const float rinv = rsqrtf(ss * (1.0f / 512.0f) + EPS);
;         if ((lane >> 4) == h) { const int c0 = (lane & 15) * 8; const float* g = p.in[I_SGUNG] + l * 512 + h * 128 + c0;
; #pragma unroll
;             for (int j = 0; j < 8; ++j) Vl[(c0 + j) * 136 + q] = f2bf(f[j] * rinv * g[j]); } }
	s_waitcnt lgkmcnt(0)
	v_add_f32_e32 v105, v105, v106
	v_fmamk_f32 v105, v105, 0x3b000000, v246
	s_mov_b32 s2, 0x800000
	v_cmp_gt_f32_e64 s[2:3], s2, v105
	v_mul_f32_e32 v106, 0x4b800000, v105
	s_nop 0
	v_cndmask_b32_e64 v105, v105, v106, s[2:3]
	v_rsq_f32_e32 v105, v105
	s_nop 0
	v_mul_f32_e32 v106, 0x45800000, v105
	v_cndmask_b32_e64 v112, v105, v106, s[2:3]
	v_mul_f32_e32 v113, v104, v112
	global_load_dwordx4 v[104:107], v[62:63], off offset:16
	global_load_dwordx4 v[108:111], v[62:63], off
	v_mul_f32_e32 v102, v102, v112
	v_mul_f32_e32 v99, v99, v112
	v_mul_f32_e32 v101, v101, v112
	v_mul_f32_e32 v98, v98, v112
	v_mul_f32_e32 v77, v77, v112
	s_waitcnt vmcnt(1)
	v_mul_f32_e32 v99, v99, v104
	s_waitcnt vmcnt(0)
	v_mov_b32_e32 v160, v108
	v_mov_b32_e32 v161, v109
	v_mov_b32_e32 v162, v110
	v_mov_b32_e32 v163, v111
	v_mov_b32_e32 v164, v104
	v_mov_b32_e32 v165, v105
	v_mov_b32_e32 v166, v106
	v_mov_b32_e32 v167, v107
	v_mul_f32_e32 v102, v102, v109
	v_cvt_pk_bf16_f32 v102, v102, s0
	v_cvt_pk_bf16_f32 v99, v99, s0
	ds_write_b16 v67, v102 offset:35088
	v_mul_f32_e32 v102, v103, v112
	ds_write_b16 v67, v99 offset:35904
	v_mul_f32_e32 v99, v100, v112
	v_mul_f32_e32 v108, v113, v108
	v_mul_f32_e32 v102, v102, v110
	v_mul_f32_e32 v101, v101, v111
	v_mul_f32_e32 v99, v99, v105
	v_mul_f32_e32 v98, v98, v106
	v_mul_f32_e32 v77, v77, v107
	v_cvt_pk_bf16_f32 v108, v108, s0
	v_cvt_pk_bf16_f32 v102, v102, s0
	v_cvt_pk_bf16_f32 v101, v101, s0
	v_cvt_pk_bf16_f32 v99, v99, s0
	v_cvt_pk_bf16_f32 v98, v98, s0
	v_cvt_pk_bf16_f32 v77, v77, s0
	ds_write_b16 v67, v108 offset:34816
	ds_write_b16 v67, v102 offset:35360
	ds_write_b16 v67, v101 offset:35632
	ds_write_b16 v67, v99 offset:36176
	ds_write_b16 v67, v98 offset:36448
	ds_write_b16 v67, v77 offset:36720
.LBB0_479:
	s_or_b64 exec, exec, s[0:1]
	s_waitcnt vmcnt(14)
	v_lshlrev_b32_e32 v77, 16, v58
	v_lshlrev_b32_e32 v98, 16, v59
	v_and_b32_e32 v100, 0xffff0000, v59
	v_mul_f32_e32 v59, 0x3dd2d3e8, v77
	v_fma_f32 v59, -v59, v77, s33
	v_mul_f32_e32 v59, v59, v77
	v_exp_f32_e32 v59, v59
	v_and_b32_e32 v58, 0xffff0000, v58
	v_lshlrev_b32_e32 v101, 16, v60
	v_and_b32_e32 v102, 0xffff0000, v60
	v_add_f32_e32 v59, 1.0, v59
	v_rcp_f32_e32 v59, v59
	v_mul_f32_e32 v60, 0x3dd2d3e8, v100
	v_fma_f32 v60, -v60, v100, s33
	v_mul_f32_e32 v60, v60, v100
	v_mul_f32_e32 v99, v59, v77
	v_mul_f32_e32 v59, 0x3dd2d3e8, v58
	v_fma_f32 v59, -v59, v58, s33
	v_mul_f32_e32 v59, v59, v58
	v_exp_f32_e32 v59, v59
	v_exp_f32_e32 v60, v60
	v_lshlrev_b32_e32 v103, 16, v61
	v_and_b32_e32 v104, 0xffff0000, v61
	v_add_f32_e32 v59, 1.0, v59
	v_rcp_f32_e32 v59, v59
	v_add_f32_e32 v60, 1.0, v60
	v_rcp_f32_e32 v60, v60
	v_mul_f32_e32 v61, 0x3dd2d3e8, v101
	v_mul_f32_e32 v59, v59, v58
	v_mul_f32_e32 v58, 0x3dd2d3e8, v98
	v_fma_f32 v58, -v58, v98, s33
	v_mul_f32_e32 v58, v58, v98
	v_exp_f32_e32 v58, v58
	v_fma_f32 v61, -v61, v101, s33
	v_mul_f32_e32 v77, 0x3dd2d3e8, v102
	v_mul_f32_e32 v61, v61, v101
	v_add_f32_e32 v58, 1.0, v58
	v_rcp_f32_e32 v58, v58
	v_fma_f32 v77, -v77, v102, s33
	v_mul_f32_e32 v60, v60, v100
	v_exp_f32_e32 v61, v61
	v_mul_f32_e32 v58, v58, v98
	v_mul_f32_e32 v98, 0x3dd2d3e8, v103
	v_mul_f32_e32 v77, v77, v102
	v_fma_f32 v98, -v98, v103, s33
	v_mul_f32_e32 v100, 0x3dd2d3e8, v104
	v_exp_f32_e32 v77, v77
	v_mul_f32_e32 v98, v98, v103
	v_fma_f32 v100, -v100, v104, s33
	v_exp_f32_e32 v98, v98
	v_mul_f32_e32 v100, v100, v104
	v_exp_f32_e32 v100, v100
	v_add_f32_e32 v61, 1.0, v61
	v_rcp_f32_e32 v61, v61
	v_add_f32_e32 v77, 1.0, v77
	v_mul_f32_e32 v105, v59, v59
	v_rcp_f32_e32 v77, v77
	v_add_f32_e32 v98, 1.0, v98
	v_fmac_f32_e32 v105, v99, v99
	v_rcp_f32_e32 v98, v98
	v_add_f32_e32 v100, 1.0, v100
	v_fmac_f32_e32 v105, v58, v58
	v_rcp_f32_e32 v100, v100
	v_fmac_f32_e32 v105, v60, v60
	v_mul_f32_e32 v61, v61, v101
	v_fmac_f32_e32 v105, v61, v61
	v_mul_f32_e32 v77, v77, v102
	v_fmac_f32_e32 v105, v77, v77
	v_mul_f32_e32 v98, v98, v103
	v_fmac_f32_e32 v105, v98, v98
	v_mul_f32_e32 v100, v100, v104
	v_fmac_f32_e32 v105, v100, v100
	ds_bpermute_b32 v101, v68, v105
	s_waitcnt lgkmcnt(0)
	v_add_f32_e32 v101, v105, v101
	v_mov_b32_e32 v102, v101
	s_nop 1
	v_permlane16_swap_b32_e32 v102, v101
	s_waitcnt lgkmcnt(0)
	v_add_f32_e32 v101, v101, v102
	s_nop 1
	v_mov_b32_dpp v102, v101 row_ror:8 row_mask:0xf bank_mask:0xf
	s_waitcnt lgkmcnt(0)
	v_add_f32_e32 v101, v101, v102
	s_nop 1
	v_mov_b32_dpp v102, v101 row_shl:4 row_mask:0xf bank_mask:0x5
	v_mov_b32_dpp v102, v101 row_shr:4 row_mask:0xf bank_mask:0xa
	s_waitcnt lgkmcnt(0)
	v_add_f32_e32 v101, v101, v102
	s_nop 1
	v_mov_b32_dpp v102, v101 quad_perm:[2,3,0,1] row_mask:0xf bank_mask:0xf
	s_waitcnt lgkmcnt(0)
	v_add_f32_e32 v101, v101, v102
	s_nop 1
	v_mov_b32_dpp v102, v101 quad_perm:[1,0,3,2] row_mask:0xf bank_mask:0xf
	s_and_saveexec_b64 s[0:1], vcc
	s_cbranch_execz .LBB0_481
	s_waitcnt lgkmcnt(0)
	v_add_f32_e32 v101, v101, v102
	v_fmamk_f32 v101, v101, 0x3b000000, v246
	s_mov_b32 s2, 0x800000
	v_cmp_gt_f32_e64 s[2:3], s2, v101
	v_mul_f32_e32 v102, 0x4b800000, v101
	s_nop 0
	v_cndmask_b32_e64 v101, v101, v102, s[2:3]
	v_rsq_f32_e32 v101, v101
	s_nop 0
	v_mul_f32_e32 v102, 0x45800000, v101
	v_cndmask_b32_e64 v101, v101, v102, s[2:3]
	v_mul_f32_e32 v58, v58, v101
	v_mul_f32_e32 v99, v99, v101
	v_mul_f32_e32 v59, v59, v101
	v_mul_f32_e32 v58, v58, v162
	v_cvt_pk_bf16_f32 v58, v58, s0
	ds_write_b16 v67, v58 offset:35362
	v_mul_f32_e32 v58, v60, v101
	v_mul_f32_e32 v58, v58, v163
	v_cvt_pk_bf16_f32 v58, v58, s0
	ds_write_b16 v67, v58 offset:35634
	v_mul_f32_e32 v58, v61, v101
	v_mul_f32_e32 v58, v58, v164
	v_cvt_pk_bf16_f32 v58, v58, s0
	ds_write_b16 v67, v58 offset:35906
	v_mul_f32_e32 v58, v77, v101
	v_mul_f32_e32 v58, v58, v165
	v_cvt_pk_bf16_f32 v58, v58, s0
	ds_write_b16 v67, v58 offset:36178
	v_mul_f32_e32 v58, v98, v101
	v_mul_f32_e32 v58, v58, v166
	v_cvt_pk_bf16_f32 v58, v58, s0
	ds_write_b16 v67, v58 offset:36450
	v_mul_f32_e32 v58, v100, v101
	v_mul_f32_e32 v99, v99, v160
	v_mul_f32_e32 v59, v59, v161
	v_mul_f32_e32 v58, v58, v167
	v_cvt_pk_bf16_f32 v99, v99, s0
	v_cvt_pk_bf16_f32 v59, v59, s0
	v_cvt_pk_bf16_f32 v58, v58, s0
	ds_write_b16 v67, v99 offset:34818
	ds_write_b16 v67, v59 offset:35090
	ds_write_b16 v67, v58 offset:36722
; __device__ __forceinline__ float bflo(unsigned w) { return __uint_as_float(w << 16); }
; __device__ __forceinline__ float bfhi(unsigned w) { return __uint_as_float(w & 0xffff0000u); }
; __device__ __forceinline__ unsigned short f2bf(float f) { return (unsigned short)(cvt_pk_bf16(f, 0.f) & 0xffffu); }
; __device__ __forceinline__ void sgu_unit(const Params& p, int l, int un, LAS unsigned char* lds) {
;     ...
;     for (int qi = 0; qi < 16; ++qi) { const int q = wave * 16 + qi;
;         const u32x4 v = vv[qi]; float f[8] = {bflo(v.x), bfhi(v.x), bflo(v.y), bfhi(v.y), bflo(v.z), bfhi(v.z), bflo(v.w), bfhi(v.w)}; float ss = 0.f;
; #pragma unroll
;         for (int j = 0; j < 8; ++j) { f[j] = gelu_tanh(f[j]); ss += f[j] * f[j]; }
;         ss = wave_sum(ss); const float rinv = rsqrtf(ss * (1.0f / 512.0f) + EPS);
;         if ((lane >> 4) == h) { const int c0 = (lane & 15) * 8; const float* g = p.in[I_SGUNG] + l * 512 + h * 128 + c0;
; #pragma unroll
;             for (int j = 0; j < 8; ++j) Vl[(c0 + j) * 136 + q] = f2bf(f[j] * rinv * g[j]); } }
.LBB0_481:
	s_or_b64 exec, exec, s[0:1]
	s_waitcnt vmcnt(13)
	v_lshlrev_b32_e32 v58, 16, v54
	v_lshlrev_b32_e32 v59, 16, v55
	v_and_b32_e32 v61, 0xffff0000, v55
	v_mul_f32_e32 v55, 0x3dd2d3e8, v58
	v_fma_f32 v55, -v55, v58, s33
	v_mul_f32_e32 v55, v55, v58
	v_exp_f32_e32 v55, v55
	v_and_b32_e32 v54, 0xffff0000, v54
	v_lshlrev_b32_e32 v77, 16, v56
	v_and_b32_e32 v98, 0xffff0000, v56
	v_add_f32_e32 v55, 1.0, v55
	v_rcp_f32_e32 v55, v55
	v_mul_f32_e32 v56, 0x3dd2d3e8, v61
	v_fma_f32 v56, -v56, v61, s33
	v_mul_f32_e32 v56, v56, v61
	v_mul_f32_e32 v60, v55, v58
	v_mul_f32_e32 v55, 0x3dd2d3e8, v54
	v_fma_f32 v55, -v55, v54, s33
	v_mul_f32_e32 v55, v55, v54
	v_exp_f32_e32 v55, v55
	v_exp_f32_e32 v56, v56
	v_lshlrev_b32_e32 v99, 16, v57
	v_and_b32_e32 v100, 0xffff0000, v57
	v_add_f32_e32 v55, 1.0, v55
	v_rcp_f32_e32 v55, v55
	v_add_f32_e32 v56, 1.0, v56
	v_rcp_f32_e32 v56, v56
	v_mul_f32_e32 v57, 0x3dd2d3e8, v77
	v_mul_f32_e32 v55, v55, v54
	v_mul_f32_e32 v54, 0x3dd2d3e8, v59
	v_fma_f32 v54, -v54, v59, s33
	v_mul_f32_e32 v54, v54, v59
	v_exp_f32_e32 v54, v54
	v_fma_f32 v57, -v57, v77, s33
	v_mul_f32_e32 v58, 0x3dd2d3e8, v98
	v_mul_f32_e32 v57, v57, v77
	v_add_f32_e32 v54, 1.0, v54
	v_rcp_f32_e32 v54, v54
	v_fma_f32 v58, -v58, v98, s33
	v_mul_f32_e32 v56, v56, v61
	v_exp_f32_e32 v57, v57
	v_mul_f32_e32 v54, v54, v59
	v_mul_f32_e32 v59, 0x3dd2d3e8, v99
	v_mul_f32_e32 v58, v58, v98
	v_fma_f32 v59, -v59, v99, s33
	v_mul_f32_e32 v61, 0x3dd2d3e8, v100
	v_exp_f32_e32 v58, v58
	v_mul_f32_e32 v59, v59, v99
	v_fma_f32 v61, -v61, v100, s33
	v_exp_f32_e32 v59, v59
	v_mul_f32_e32 v61, v61, v100
	v_exp_f32_e32 v61, v61
	v_add_f32_e32 v57, 1.0, v57
	v_rcp_f32_e32 v57, v57
	v_add_f32_e32 v58, 1.0, v58
	v_mul_f32_e32 v101, v55, v55
	v_rcp_f32_e32 v58, v58
	v_add_f32_e32 v59, 1.0, v59
	v_fmac_f32_e32 v101, v60, v60
	v_rcp_f32_e32 v59, v59
	v_add_f32_e32 v61, 1.0, v61
	v_fmac_f32_e32 v101, v54, v54
	v_rcp_f32_e32 v61, v61
	v_fmac_f32_e32 v101, v56, v56
	v_mul_f32_e32 v57, v57, v77
	v_fmac_f32_e32 v101, v57, v57
	v_mul_f32_e32 v58, v58, v98
	v_fmac_f32_e32 v101, v58, v58
	v_mul_f32_e32 v59, v59, v99
	v_fmac_f32_e32 v101, v59, v59
	v_mul_f32_e32 v61, v61, v100
	v_fmac_f32_e32 v101, v61, v61
	ds_bpermute_b32 v77, v68, v101
	s_waitcnt lgkmcnt(0)
	v_add_f32_e32 v77, v101, v77
	v_mov_b32_e32 v98, v77
	s_nop 1
	v_permlane16_swap_b32_e32 v98, v77
	s_waitcnt lgkmcnt(0)
	v_add_f32_e32 v77, v77, v98
	s_nop 1
	v_mov_b32_dpp v98, v77 row_ror:8 row_mask:0xf bank_mask:0xf
	s_waitcnt lgkmcnt(0)
	v_add_f32_e32 v77, v77, v98
	s_nop 1
	v_mov_b32_dpp v98, v77 row_shl:4 row_mask:0xf bank_mask:0x5
	v_mov_b32_dpp v98, v77 row_shr:4 row_mask:0xf bank_mask:0xa
	s_waitcnt lgkmcnt(0)
	v_add_f32_e32 v77, v77, v98
	s_nop 1
	v_mov_b32_dpp v98, v77 quad_perm:[2,3,0,1] row_mask:0xf bank_mask:0xf
	s_waitcnt lgkmcnt(0)
	v_add_f32_e32 v77, v77, v98
	s_nop 1
	v_mov_b32_dpp v98, v77 quad_perm:[1,0,3,2] row_mask:0xf bank_mask:0xf
	s_and_saveexec_b64 s[0:1], vcc
	s_cbranch_execz .LBB0_483
	s_waitcnt lgkmcnt(0)
	v_add_f32_e32 v77, v77, v98
	v_fmamk_f32 v77, v77, 0x3b000000, v246
	s_mov_b32 s2, 0x800000
	v_cmp_gt_f32_e64 s[2:3], s2, v77
	v_mul_f32_e32 v98, 0x4b800000, v77
	s_nop 0
	v_cndmask_b32_e64 v77, v77, v98, s[2:3]
	v_rsq_f32_e32 v77, v77
	s_nop 0
	v_mul_f32_e32 v98, 0x45800000, v77
	v_cndmask_b32_e64 v77, v77, v98, s[2:3]
	v_mul_f32_e32 v54, v54, v77
	v_mul_f32_e32 v60, v60, v77
	v_mul_f32_e32 v55, v55, v77
	v_mul_f32_e32 v54, v54, v162
	v_cvt_pk_bf16_f32 v54, v54, s0
	ds_write_b16 v67, v54 offset:35364
	v_mul_f32_e32 v54, v56, v77
	v_mul_f32_e32 v54, v54, v163
	v_cvt_pk_bf16_f32 v54, v54, s0
	ds_write_b16 v67, v54 offset:35636
	v_mul_f32_e32 v54, v57, v77
	v_mul_f32_e32 v54, v54, v164
	v_cvt_pk_bf16_f32 v54, v54, s0
	ds_write_b16 v67, v54 offset:35908
	v_mul_f32_e32 v54, v58, v77
	v_mul_f32_e32 v54, v54, v165
	v_cvt_pk_bf16_f32 v54, v54, s0
	ds_write_b16 v67, v54 offset:36180
	v_mul_f32_e32 v54, v59, v77
	v_mul_f32_e32 v54, v54, v166
	v_cvt_pk_bf16_f32 v54, v54, s0
	ds_write_b16 v67, v54 offset:36452
	v_mul_f32_e32 v54, v61, v77
	v_mul_f32_e32 v60, v60, v160
	v_mul_f32_e32 v55, v55, v161
	v_mul_f32_e32 v54, v54, v167
	v_cvt_pk_bf16_f32 v60, v60, s0
	v_cvt_pk_bf16_f32 v55, v55, s0
	v_cvt_pk_bf16_f32 v54, v54, s0
	ds_write_b16 v67, v60 offset:34820
	ds_write_b16 v67, v55 offset:35092
	ds_write_b16 v67, v54 offset:36724
; __device__ __forceinline__ float bflo(unsigned w) { return __uint_as_float(w << 16); }
; __device__ __forceinline__ float bfhi(unsigned w) { return __uint_as_float(w & 0xffff0000u); }
; __device__ __forceinline__ unsigned short f2bf(float f) { return (unsigned short)(cvt_pk_bf16(f, 0.f) & 0xffffu); }
; __device__ __forceinline__ void sgu_unit(const Params& p, int l, int un, LAS unsigned char* lds) {
;     ...
;     for (int qi = 0; qi < 16; ++qi) { const int q = wave * 16 + qi;
;         const u32x4 v = vv[qi]; float f[8] = {bflo(v.x), bfhi(v.x), bflo(v.y), bfhi(v.y), bflo(v.z), bfhi(v.z), bflo(v.w), bfhi(v.w)}; float ss = 0.f;
; #pragma unroll
;         for (int j = 0; j < 8; ++j) { f[j] = gelu_tanh(f[j]); ss += f[j] * f[j]; }
;         ss = wave_sum(ss); const float rinv = rsqrtf(ss * (1.0f / 512.0f) + EPS);
;         if ((lane >> 4) == h) { const int c0 = (lane & 15) * 8; const float* g = p.in[I_SGUNG] + l * 512 + h * 128 + c0;
; #pragma unroll
;             for (int j = 0; j < 8; ++j) Vl[(c0 + j) * 136 + q] = f2bf(f[j] * rinv * g[j]); } }
.LBB0_483:
	s_or_b64 exec, exec, s[0:1]
	s_waitcnt vmcnt(12)
	v_lshlrev_b32_e32 v54, 16, v50
	v_lshlrev_b32_e32 v55, 16, v51
	v_and_b32_e32 v57, 0xffff0000, v51
	v_mul_f32_e32 v51, 0x3dd2d3e8, v54
	v_fma_f32 v51, -v51, v54, s33
	v_mul_f32_e32 v51, v51, v54
	v_exp_f32_e32 v51, v51
	v_and_b32_e32 v50, 0xffff0000, v50
	v_lshlrev_b32_e32 v58, 16, v52
	v_and_b32_e32 v59, 0xffff0000, v52
	v_add_f32_e32 v51, 1.0, v51
	v_rcp_f32_e32 v51, v51
	v_mul_f32_e32 v52, 0x3dd2d3e8, v57
	v_fma_f32 v52, -v52, v57, s33
	v_mul_f32_e32 v52, v52, v57
	v_mul_f32_e32 v56, v51, v54
	v_mul_f32_e32 v51, 0x3dd2d3e8, v50
	v_fma_f32 v51, -v51, v50, s33
	v_mul_f32_e32 v51, v51, v50
	v_exp_f32_e32 v51, v51
	v_exp_f32_e32 v52, v52
	v_lshlrev_b32_e32 v60, 16, v53
	v_and_b32_e32 v61, 0xffff0000, v53
	v_add_f32_e32 v51, 1.0, v51
	v_rcp_f32_e32 v51, v51
	v_add_f32_e32 v52, 1.0, v52
	v_rcp_f32_e32 v52, v52
	v_mul_f32_e32 v53, 0x3dd2d3e8, v58
	v_mul_f32_e32 v51, v51, v50
	v_mul_f32_e32 v50, 0x3dd2d3e8, v55
	v_fma_f32 v50, -v50, v55, s33
	v_mul_f32_e32 v50, v50, v55
	v_exp_f32_e32 v50, v50
	v_fma_f32 v53, -v53, v58, s33
	v_mul_f32_e32 v54, 0x3dd2d3e8, v59
	v_mul_f32_e32 v53, v53, v58
	v_add_f32_e32 v50, 1.0, v50
	v_rcp_f32_e32 v50, v50
	v_fma_f32 v54, -v54, v59, s33
	v_mul_f32_e32 v52, v52, v57
	v_exp_f32_e32 v53, v53
	v_mul_f32_e32 v50, v50, v55
	v_mul_f32_e32 v55, 0x3dd2d3e8, v60
	v_mul_f32_e32 v54, v54, v59
	v_fma_f32 v55, -v55, v60, s33
	v_mul_f32_e32 v57, 0x3dd2d3e8, v61
	v_exp_f32_e32 v54, v54
	v_mul_f32_e32 v55, v55, v60
	v_fma_f32 v57, -v57, v61, s33
	v_exp_f32_e32 v55, v55
	v_mul_f32_e32 v57, v57, v61
	v_exp_f32_e32 v57, v57
	v_add_f32_e32 v53, 1.0, v53
	v_rcp_f32_e32 v53, v53
	v_add_f32_e32 v54, 1.0, v54
	v_mul_f32_e32 v77, v51, v51
	v_rcp_f32_e32 v54, v54
	v_add_f32_e32 v55, 1.0, v55
	v_fmac_f32_e32 v77, v56, v56
	v_rcp_f32_e32 v55, v55
	v_add_f32_e32 v57, 1.0, v57
	v_fmac_f32_e32 v77, v50, v50
	v_rcp_f32_e32 v57, v57
	v_fmac_f32_e32 v77, v52, v52
	v_mul_f32_e32 v53, v53, v58
	v_fmac_f32_e32 v77, v53, v53
	v_mul_f32_e32 v54, v54, v59
	v_fmac_f32_e32 v77, v54, v54
	v_mul_f32_e32 v55, v55, v60
	v_fmac_f32_e32 v77, v55, v55
	v_mul_f32_e32 v57, v57, v61
	v_fmac_f32_e32 v77, v57, v57
	ds_bpermute_b32 v58, v68, v77
	s_waitcnt lgkmcnt(0)
	v_add_f32_e32 v58, v77, v58
	v_mov_b32_e32 v59, v58
	s_nop 1
	v_permlane16_swap_b32_e32 v59, v58
	s_waitcnt lgkmcnt(0)
	v_add_f32_e32 v58, v58, v59
	s_nop 1
	v_mov_b32_dpp v59, v58 row_ror:8 row_mask:0xf bank_mask:0xf
	s_waitcnt lgkmcnt(0)
	v_add_f32_e32 v58, v58, v59
	s_nop 1
	v_mov_b32_dpp v59, v58 row_shl:4 row_mask:0xf bank_mask:0x5
	v_mov_b32_dpp v59, v58 row_shr:4 row_mask:0xf bank_mask:0xa
	s_waitcnt lgkmcnt(0)
	v_add_f32_e32 v58, v58, v59
	s_nop 1
	v_mov_b32_dpp v59, v58 quad_perm:[2,3,0,1] row_mask:0xf bank_mask:0xf
	s_waitcnt lgkmcnt(0)
	v_add_f32_e32 v58, v58, v59
	s_nop 1
	v_mov_b32_dpp v59, v58 quad_perm:[1,0,3,2] row_mask:0xf bank_mask:0xf
	s_and_saveexec_b64 s[0:1], vcc
	s_cbranch_execz .LBB0_485
	s_waitcnt lgkmcnt(0)
	v_add_f32_e32 v58, v58, v59
	v_fmamk_f32 v58, v58, 0x3b000000, v246
	s_mov_b32 s2, 0x800000
	v_cmp_gt_f32_e64 s[2:3], s2, v58
	v_mul_f32_e32 v59, 0x4b800000, v58
	s_nop 0
	v_cndmask_b32_e64 v58, v58, v59, s[2:3]
	v_rsq_f32_e32 v58, v58
	s_nop 0
	v_mul_f32_e32 v59, 0x45800000, v58
	v_cndmask_b32_e64 v77, v58, v59, s[2:3]
	v_mul_f32_e32 v50, v50, v77
	v_mul_f32_e32 v56, v56, v77
	v_mul_f32_e32 v51, v51, v77
	v_mul_f32_e32 v50, v50, v162
	v_cvt_pk_bf16_f32 v50, v50, s0
	ds_write_b16 v67, v50 offset:35366
	v_mul_f32_e32 v50, v52, v77
	v_mul_f32_e32 v50, v50, v163
	v_cvt_pk_bf16_f32 v50, v50, s0
	ds_write_b16 v67, v50 offset:35638
	v_mul_f32_e32 v50, v53, v77
	v_mul_f32_e32 v50, v50, v164
	v_cvt_pk_bf16_f32 v50, v50, s0
	ds_write_b16 v67, v50 offset:35910
	v_mul_f32_e32 v50, v54, v77
	v_mul_f32_e32 v50, v50, v165
	v_cvt_pk_bf16_f32 v50, v50, s0
	ds_write_b16 v67, v50 offset:36182
	v_mul_f32_e32 v50, v55, v77
	v_mul_f32_e32 v50, v50, v166
	v_cvt_pk_bf16_f32 v50, v50, s0
	ds_write_b16 v67, v50 offset:36454
	v_mul_f32_e32 v50, v57, v77
	v_mul_f32_e32 v56, v56, v160
	v_mul_f32_e32 v51, v51, v161
	v_mul_f32_e32 v50, v50, v167
	v_cvt_pk_bf16_f32 v56, v56, s0
	v_cvt_pk_bf16_f32 v51, v51, s0
	v_cvt_pk_bf16_f32 v50, v50, s0
	ds_write_b16 v67, v56 offset:34822
	ds_write_b16 v67, v51 offset:35094
	ds_write_b16 v67, v50 offset:36726
; __device__ __forceinline__ float bflo(unsigned w) { return __uint_as_float(w << 16); }
; __device__ __forceinline__ float bfhi(unsigned w) { return __uint_as_float(w & 0xffff0000u); }
; __device__ __forceinline__ unsigned short f2bf(float f) { return (unsigned short)(cvt_pk_bf16(f, 0.f) & 0xffffu); }
; __device__ __forceinline__ void sgu_unit(const Params& p, int l, int un, LAS unsigned char* lds) {
;     ...
;     for (int qi = 0; qi < 16; ++qi) { const int q = wave * 16 + qi;
;         const u32x4 v = vv[qi]; float f[8] = {bflo(v.x), bfhi(v.x), bflo(v.y), bfhi(v.y), bflo(v.z), bfhi(v.z), bflo(v.w), bfhi(v.w)}; float ss = 0.f;
; #pragma unroll
;         for (int j = 0; j < 8; ++j) { f[j] = gelu_tanh(f[j]); ss += f[j] * f[j]; }
;         ss = wave_sum(ss); const float rinv = rsqrtf(ss * (1.0f / 512.0f) + EPS);
;         if ((lane >> 4) == h) { const int c0 = (lane & 15) * 8; const float* g = p.in[I_SGUNG] + l * 512 + h * 128 + c0;
; #pragma unroll
;             for (int j = 0; j < 8; ++j) Vl[(c0 + j) * 136 + q] = f2bf(f[j] * rinv * g[j]); } }
.LBB0_485:
	s_or_b64 exec, exec, s[0:1]
	s_waitcnt vmcnt(11)
	v_lshlrev_b32_e32 v50, 16, v46
	v_lshlrev_b32_e32 v51, 16, v47
	v_and_b32_e32 v53, 0xffff0000, v47
	v_mul_f32_e32 v47, 0x3dd2d3e8, v50
	v_fma_f32 v47, -v47, v50, s33
	v_mul_f32_e32 v47, v47, v50
	v_exp_f32_e32 v47, v47
	v_and_b32_e32 v46, 0xffff0000, v46
	v_lshlrev_b32_e32 v54, 16, v48
	v_and_b32_e32 v55, 0xffff0000, v48
	v_add_f32_e32 v47, 1.0, v47
	v_rcp_f32_e32 v47, v47
	v_mul_f32_e32 v48, 0x3dd2d3e8, v53
	v_fma_f32 v48, -v48, v53, s33
	v_mul_f32_e32 v48, v48, v53
	v_mul_f32_e32 v52, v47, v50
	v_mul_f32_e32 v47, 0x3dd2d3e8, v46
	v_fma_f32 v47, -v47, v46, s33
	v_mul_f32_e32 v47, v47, v46
	v_exp_f32_e32 v47, v47
	v_exp_f32_e32 v48, v48
	v_lshlrev_b32_e32 v56, 16, v49
	v_and_b32_e32 v57, 0xffff0000, v49
	v_add_f32_e32 v47, 1.0, v47
	v_rcp_f32_e32 v47, v47
	v_add_f32_e32 v48, 1.0, v48
	v_rcp_f32_e32 v48, v48
	v_mul_f32_e32 v49, 0x3dd2d3e8, v54
	v_mul_f32_e32 v47, v47, v46
	v_mul_f32_e32 v46, 0x3dd2d3e8, v51
	v_fma_f32 v46, -v46, v51, s33
	v_mul_f32_e32 v46, v46, v51
	v_exp_f32_e32 v46, v46
	v_fma_f32 v49, -v49, v54, s33
	v_mul_f32_e32 v50, 0x3dd2d3e8, v55
	v_mul_f32_e32 v49, v49, v54
	v_add_f32_e32 v46, 1.0, v46
	v_rcp_f32_e32 v46, v46
	v_fma_f32 v50, -v50, v55, s33
	v_mul_f32_e32 v48, v48, v53
	v_exp_f32_e32 v49, v49
	v_mul_f32_e32 v46, v46, v51
	v_mul_f32_e32 v51, 0x3dd2d3e8, v56
	v_mul_f32_e32 v50, v50, v55
	v_fma_f32 v51, -v51, v56, s33
	v_mul_f32_e32 v53, 0x3dd2d3e8, v57
	v_exp_f32_e32 v50, v50
	v_mul_f32_e32 v51, v51, v56
	v_fma_f32 v53, -v53, v57, s33
	v_exp_f32_e32 v51, v51
	v_mul_f32_e32 v53, v53, v57
	v_exp_f32_e32 v53, v53
	v_add_f32_e32 v49, 1.0, v49
	v_rcp_f32_e32 v49, v49
	v_add_f32_e32 v50, 1.0, v50
	v_mul_f32_e32 v58, v47, v47
	v_rcp_f32_e32 v50, v50
	v_add_f32_e32 v51, 1.0, v51
	v_fmac_f32_e32 v58, v52, v52
	v_rcp_f32_e32 v51, v51
	v_add_f32_e32 v53, 1.0, v53
	v_fmac_f32_e32 v58, v46, v46
	v_rcp_f32_e32 v53, v53
	v_fmac_f32_e32 v58, v48, v48
	v_mul_f32_e32 v49, v49, v54
	v_fmac_f32_e32 v58, v49, v49
	v_mul_f32_e32 v50, v50, v55
	v_fmac_f32_e32 v58, v50, v50
	v_mul_f32_e32 v51, v51, v56
	v_fmac_f32_e32 v58, v51, v51
	v_mul_f32_e32 v53, v53, v57
	v_fmac_f32_e32 v58, v53, v53
	ds_bpermute_b32 v54, v68, v58
	s_waitcnt lgkmcnt(0)
	v_add_f32_e32 v54, v58, v54
	v_mov_b32_e32 v55, v54
	s_nop 1
	v_permlane16_swap_b32_e32 v55, v54
	s_waitcnt lgkmcnt(0)
	v_add_f32_e32 v54, v54, v55
	s_nop 1
	v_mov_b32_dpp v55, v54 row_ror:8 row_mask:0xf bank_mask:0xf
	s_waitcnt lgkmcnt(0)
	v_add_f32_e32 v54, v54, v55
	s_nop 1
	v_mov_b32_dpp v55, v54 row_shl:4 row_mask:0xf bank_mask:0x5
	v_mov_b32_dpp v55, v54 row_shr:4 row_mask:0xf bank_mask:0xa
	s_waitcnt lgkmcnt(0)
	v_add_f32_e32 v54, v54, v55
	s_nop 1
	v_mov_b32_dpp v55, v54 quad_perm:[2,3,0,1] row_mask:0xf bank_mask:0xf
	s_waitcnt lgkmcnt(0)
	v_add_f32_e32 v54, v54, v55
	s_nop 1
	v_mov_b32_dpp v55, v54 quad_perm:[1,0,3,2] row_mask:0xf bank_mask:0xf
	s_and_saveexec_b64 s[0:1], vcc
	s_cbranch_execz .LBB0_487
	s_waitcnt lgkmcnt(0)
	v_add_f32_e32 v54, v54, v55
	v_fmamk_f32 v54, v54, 0x3b000000, v246
	s_mov_b32 s2, 0x800000
	v_cmp_gt_f32_e64 s[2:3], s2, v54
	v_mul_f32_e32 v55, 0x4b800000, v54
	s_nop 0
	v_cndmask_b32_e64 v54, v54, v55, s[2:3]
	v_rsq_f32_e32 v54, v54
	s_nop 0
	v_mul_f32_e32 v55, 0x45800000, v54
	v_cndmask_b32_e64 v77, v54, v55, s[2:3]
	v_mul_f32_e32 v46, v46, v77
	v_mul_f32_e32 v52, v52, v77
	v_mul_f32_e32 v47, v47, v77
	v_mul_f32_e32 v46, v46, v162
	v_cvt_pk_bf16_f32 v46, v46, s0
	ds_write_b16 v67, v46 offset:35368
	v_mul_f32_e32 v46, v48, v77
	v_mul_f32_e32 v46, v46, v163
	v_cvt_pk_bf16_f32 v46, v46, s0
	ds_write_b16 v67, v46 offset:35640
	v_mul_f32_e32 v46, v49, v77
	v_mul_f32_e32 v46, v46, v164
	v_cvt_pk_bf16_f32 v46, v46, s0
	ds_write_b16 v67, v46 offset:35912
	v_mul_f32_e32 v46, v50, v77
	v_mul_f32_e32 v46, v46, v165
	v_cvt_pk_bf16_f32 v46, v46, s0
	ds_write_b16 v67, v46 offset:36184
	v_mul_f32_e32 v46, v51, v77
	v_mul_f32_e32 v46, v46, v166
	v_cvt_pk_bf16_f32 v46, v46, s0
	ds_write_b16 v67, v46 offset:36456
	v_mul_f32_e32 v46, v53, v77
	v_mul_f32_e32 v52, v52, v160
	v_mul_f32_e32 v47, v47, v161
	v_mul_f32_e32 v46, v46, v167
	v_cvt_pk_bf16_f32 v52, v52, s0
	v_cvt_pk_bf16_f32 v47, v47, s0
	v_cvt_pk_bf16_f32 v46, v46, s0
	ds_write_b16 v67, v52 offset:34824
	ds_write_b16 v67, v47 offset:35096
	ds_write_b16 v67, v46 offset:36728
; __device__ __forceinline__ float bflo(unsigned w) { return __uint_as_float(w << 16); }
; __device__ __forceinline__ float bfhi(unsigned w) { return __uint_as_float(w & 0xffff0000u); }
; __device__ __forceinline__ unsigned short f2bf(float f) { return (unsigned short)(cvt_pk_bf16(f, 0.f) & 0xffffu); }
; __device__ __forceinline__ void sgu_unit(const Params& p, int l, int un, LAS unsigned char* lds) {
;     ...
;     for (int qi = 0; qi < 16; ++qi) { const int q = wave * 16 + qi;
;         const u32x4 v = vv[qi]; float f[8] = {bflo(v.x), bfhi(v.x), bflo(v.y), bfhi(v.y), bflo(v.z), bfhi(v.z), bflo(v.w), bfhi(v.w)}; float ss = 0.f;
; #pragma unroll
;         for (int j = 0; j < 8; ++j) { f[j] = gelu_tanh(f[j]); ss += f[j] * f[j]; }
;         ss = wave_sum(ss); const float rinv = rsqrtf(ss * (1.0f / 512.0f) + EPS);
;         if ((lane >> 4) == h) { const int c0 = (lane & 15) * 8; const float* g = p.in[I_SGUNG] + l * 512 + h * 128 + c0;
; #pragma unroll
;             for (int j = 0; j < 8; ++j) Vl[(c0 + j) * 136 + q] = f2bf(f[j] * rinv * g[j]); } }
.LBB0_487:
	s_or_b64 exec, exec, s[0:1]
	s_waitcnt vmcnt(10)
	v_lshlrev_b32_e32 v46, 16, v42
	v_lshlrev_b32_e32 v47, 16, v43
	v_and_b32_e32 v49, 0xffff0000, v43
	v_mul_f32_e32 v43, 0x3dd2d3e8, v46
	v_fma_f32 v43, -v43, v46, s33
	v_mul_f32_e32 v43, v43, v46
	v_exp_f32_e32 v43, v43
	v_and_b32_e32 v42, 0xffff0000, v42
	v_lshlrev_b32_e32 v50, 16, v44
	v_and_b32_e32 v51, 0xffff0000, v44
	v_add_f32_e32 v43, 1.0, v43
	v_rcp_f32_e32 v43, v43
	v_mul_f32_e32 v44, 0x3dd2d3e8, v49
	v_fma_f32 v44, -v44, v49, s33
	v_mul_f32_e32 v44, v44, v49
	v_mul_f32_e32 v48, v43, v46
	v_mul_f32_e32 v43, 0x3dd2d3e8, v42
	v_fma_f32 v43, -v43, v42, s33
	v_mul_f32_e32 v43, v43, v42
	v_exp_f32_e32 v43, v43
	v_exp_f32_e32 v44, v44
	v_lshlrev_b32_e32 v52, 16, v45
	v_and_b32_e32 v53, 0xffff0000, v45
	v_add_f32_e32 v43, 1.0, v43
	v_rcp_f32_e32 v43, v43
	v_add_f32_e32 v44, 1.0, v44
	v_rcp_f32_e32 v44, v44
	v_mul_f32_e32 v45, 0x3dd2d3e8, v50
	v_mul_f32_e32 v43, v43, v42
	v_mul_f32_e32 v42, 0x3dd2d3e8, v47
	v_fma_f32 v42, -v42, v47, s33
	v_mul_f32_e32 v42, v42, v47
	v_exp_f32_e32 v42, v42
	v_fma_f32 v45, -v45, v50, s33
	v_mul_f32_e32 v46, 0x3dd2d3e8, v51
	v_mul_f32_e32 v45, v45, v50
	v_add_f32_e32 v42, 1.0, v42
	v_rcp_f32_e32 v42, v42
	v_fma_f32 v46, -v46, v51, s33
	v_mul_f32_e32 v44, v44, v49
	v_exp_f32_e32 v45, v45
	v_mul_f32_e32 v42, v42, v47
	v_mul_f32_e32 v47, 0x3dd2d3e8, v52
	v_mul_f32_e32 v46, v46, v51
	v_fma_f32 v47, -v47, v52, s33
	v_mul_f32_e32 v49, 0x3dd2d3e8, v53
	v_exp_f32_e32 v46, v46
	v_mul_f32_e32 v47, v47, v52
	v_fma_f32 v49, -v49, v53, s33
	v_exp_f32_e32 v47, v47
	v_mul_f32_e32 v49, v49, v53
	v_exp_f32_e32 v49, v49
	v_add_f32_e32 v45, 1.0, v45
	v_rcp_f32_e32 v45, v45
	v_add_f32_e32 v46, 1.0, v46
	v_mul_f32_e32 v54, v43, v43
	v_rcp_f32_e32 v46, v46
	v_add_f32_e32 v47, 1.0, v47
	v_fmac_f32_e32 v54, v48, v48
	v_rcp_f32_e32 v47, v47
	v_add_f32_e32 v49, 1.0, v49
	v_fmac_f32_e32 v54, v42, v42
	v_rcp_f32_e32 v49, v49
	v_fmac_f32_e32 v54, v44, v44
	v_mul_f32_e32 v45, v45, v50
	v_fmac_f32_e32 v54, v45, v45
	v_mul_f32_e32 v46, v46, v51
	v_fmac_f32_e32 v54, v46, v46
	v_mul_f32_e32 v47, v47, v52
	v_fmac_f32_e32 v54, v47, v47
	v_mul_f32_e32 v49, v49, v53
	v_fmac_f32_e32 v54, v49, v49
	v_mov_b32_e32 v50, v54
	s_nop 1
	v_permlane32_swap_b32_e32 v50, v54
	s_waitcnt lgkmcnt(0)
	v_add_f32_e32 v50, v54, v50
	v_mov_b32_e32 v51, v50
	s_nop 1
	v_permlane16_swap_b32_e32 v51, v50
	s_waitcnt lgkmcnt(0)
	v_add_f32_e32 v50, v50, v51
	s_nop 1
	v_mov_b32_dpp v51, v50 row_ror:8 row_mask:0xf bank_mask:0xf
	s_waitcnt lgkmcnt(0)
	v_add_f32_e32 v50, v50, v51
	s_nop 1
	v_mov_b32_dpp v51, v50 row_shl:4 row_mask:0xf bank_mask:0x5
	v_mov_b32_dpp v51, v50 row_shr:4 row_mask:0xf bank_mask:0xa
	s_waitcnt lgkmcnt(0)
	v_add_f32_e32 v50, v50, v51
	s_nop 1
	v_mov_b32_dpp v51, v50 quad_perm:[2,3,0,1] row_mask:0xf bank_mask:0xf
	s_waitcnt lgkmcnt(0)
	v_add_f32_e32 v50, v50, v51
	s_nop 1
	v_mov_b32_dpp v51, v50 quad_perm:[1,0,3,2] row_mask:0xf bank_mask:0xf
	s_and_saveexec_b64 s[0:1], vcc
	s_cbranch_execz .LBB0_489
	s_waitcnt lgkmcnt(0)
	v_add_f32_e32 v50, v50, v51
	v_fmamk_f32 v50, v50, 0x3b000000, v246
	s_mov_b32 s2, 0x800000
	v_cmp_gt_f32_e64 s[2:3], s2, v50
	v_mul_f32_e32 v51, 0x4b800000, v50
	s_nop 0
	v_cndmask_b32_e64 v50, v50, v51, s[2:3]
	v_rsq_f32_e32 v50, v50
	s_nop 0
	v_mul_f32_e32 v51, 0x45800000, v50
	v_cndmask_b32_e64 v58, v50, v51, s[2:3]
	v_mul_f32_e32 v42, v42, v58
	v_mul_f32_e32 v48, v48, v58
	v_mul_f32_e32 v43, v43, v58
	v_mul_f32_e32 v42, v42, v162
	v_cvt_pk_bf16_f32 v42, v42, s0
	ds_write_b16 v67, v42 offset:35370
	v_mul_f32_e32 v42, v44, v58
	v_mul_f32_e32 v42, v42, v163
	v_cvt_pk_bf16_f32 v42, v42, s0
	ds_write_b16 v67, v42 offset:35642
	v_mul_f32_e32 v42, v45, v58
	v_mul_f32_e32 v42, v42, v164
	v_cvt_pk_bf16_f32 v42, v42, s0
	ds_write_b16 v67, v42 offset:35914
	v_mul_f32_e32 v42, v46, v58
	v_mul_f32_e32 v42, v42, v165
	v_cvt_pk_bf16_f32 v42, v42, s0
	ds_write_b16 v67, v42 offset:36186
	v_mul_f32_e32 v42, v47, v58
	v_mul_f32_e32 v42, v42, v166
	v_cvt_pk_bf16_f32 v42, v42, s0
	ds_write_b16 v67, v42 offset:36458
	v_mul_f32_e32 v42, v49, v58
	v_mul_f32_e32 v48, v48, v160
	v_mul_f32_e32 v43, v43, v161
	v_mul_f32_e32 v42, v42, v167
	v_cvt_pk_bf16_f32 v48, v48, s0
	v_cvt_pk_bf16_f32 v43, v43, s0
	v_cvt_pk_bf16_f32 v42, v42, s0
	ds_write_b16 v67, v48 offset:34826
	ds_write_b16 v67, v43 offset:35098
	ds_write_b16 v67, v42 offset:36730
; __device__ __forceinline__ float bflo(unsigned w) { return __uint_as_float(w << 16); }
; __device__ __forceinline__ float bfhi(unsigned w) { return __uint_as_float(w & 0xffff0000u); }
; __device__ __forceinline__ unsigned short f2bf(float f) { return (unsigned short)(cvt_pk_bf16(f, 0.f) & 0xffffu); }
; __device__ __forceinline__ void sgu_unit(const Params& p, int l, int un, LAS unsigned char* lds) {
;     ...
;     for (int qi = 0; qi < 16; ++qi) { const int q = wave * 16 + qi;
;         const u32x4 v = vv[qi]; float f[8] = {bflo(v.x), bfhi(v.x), bflo(v.y), bfhi(v.y), bflo(v.z), bfhi(v.z), bflo(v.w), bfhi(v.w)}; float ss = 0.f;
; #pragma unroll
;         for (int j = 0; j < 8; ++j) { f[j] = gelu_tanh(f[j]); ss += f[j] * f[j]; }
;         ss = wave_sum(ss); const float rinv = rsqrtf(ss * (1.0f / 512.0f) + EPS);
;         if ((lane >> 4) == h) { const int c0 = (lane & 15) * 8; const float* g = p.in[I_SGUNG] + l * 512 + h * 128 + c0;
; #pragma unroll
;             for (int j = 0; j < 8; ++j) Vl[(c0 + j) * 136 + q] = f2bf(f[j] * rinv * g[j]); } }
.LBB0_489:
	s_or_b64 exec, exec, s[0:1]
	s_waitcnt vmcnt(9)
	v_lshlrev_b32_e32 v42, 16, v38
	v_lshlrev_b32_e32 v43, 16, v39
	v_and_b32_e32 v45, 0xffff0000, v39
	v_mul_f32_e32 v39, 0x3dd2d3e8, v42
	v_fma_f32 v39, -v39, v42, s33
	v_mul_f32_e32 v39, v39, v42
	v_exp_f32_e32 v39, v39
	v_and_b32_e32 v38, 0xffff0000, v38
	v_lshlrev_b32_e32 v46, 16, v40
	v_and_b32_e32 v47, 0xffff0000, v40
	v_add_f32_e32 v39, 1.0, v39
	v_rcp_f32_e32 v39, v39
	v_mul_f32_e32 v40, 0x3dd2d3e8, v45
	v_fma_f32 v40, -v40, v45, s33
	v_mul_f32_e32 v40, v40, v45
	v_mul_f32_e32 v44, v39, v42
	v_mul_f32_e32 v39, 0x3dd2d3e8, v38
	v_fma_f32 v39, -v39, v38, s33
	v_mul_f32_e32 v39, v39, v38
	v_exp_f32_e32 v39, v39
	v_exp_f32_e32 v40, v40
	v_lshlrev_b32_e32 v48, 16, v41
	v_and_b32_e32 v49, 0xffff0000, v41
	v_add_f32_e32 v39, 1.0, v39
	v_rcp_f32_e32 v39, v39
	v_add_f32_e32 v40, 1.0, v40
	v_rcp_f32_e32 v40, v40
	v_mul_f32_e32 v41, 0x3dd2d3e8, v46
	v_mul_f32_e32 v39, v39, v38
	v_mul_f32_e32 v38, 0x3dd2d3e8, v43
	v_fma_f32 v38, -v38, v43, s33
	v_mul_f32_e32 v38, v38, v43
	v_exp_f32_e32 v38, v38
	v_fma_f32 v41, -v41, v46, s33
	v_mul_f32_e32 v42, 0x3dd2d3e8, v47
	v_mul_f32_e32 v41, v41, v46
	v_add_f32_e32 v38, 1.0, v38
	v_rcp_f32_e32 v38, v38
	v_fma_f32 v42, -v42, v47, s33
	v_mul_f32_e32 v40, v40, v45
	v_exp_f32_e32 v41, v41
	v_mul_f32_e32 v38, v38, v43
	v_mul_f32_e32 v43, 0x3dd2d3e8, v48
	v_mul_f32_e32 v42, v42, v47
	v_fma_f32 v43, -v43, v48, s33
	v_mul_f32_e32 v45, 0x3dd2d3e8, v49
	v_exp_f32_e32 v42, v42
	v_mul_f32_e32 v43, v43, v48
	v_fma_f32 v45, -v45, v49, s33
	v_exp_f32_e32 v43, v43
	v_mul_f32_e32 v45, v45, v49
	v_exp_f32_e32 v45, v45
	v_add_f32_e32 v41, 1.0, v41
	v_rcp_f32_e32 v41, v41
	v_add_f32_e32 v42, 1.0, v42
	v_mul_f32_e32 v50, v39, v39
	v_rcp_f32_e32 v42, v42
	v_add_f32_e32 v43, 1.0, v43
	v_fmac_f32_e32 v50, v44, v44
	v_rcp_f32_e32 v43, v43
	v_add_f32_e32 v45, 1.0, v45
	v_fmac_f32_e32 v50, v38, v38
	v_rcp_f32_e32 v45, v45
	v_fmac_f32_e32 v50, v40, v40
	v_mul_f32_e32 v41, v41, v46
	v_fmac_f32_e32 v50, v41, v41
	v_mul_f32_e32 v42, v42, v47
	v_fmac_f32_e32 v50, v42, v42
	v_mul_f32_e32 v43, v43, v48
	v_fmac_f32_e32 v50, v43, v43
	v_mul_f32_e32 v45, v45, v49
	v_fmac_f32_e32 v50, v45, v45
	v_mov_b32_e32 v46, v50
	s_nop 1
	v_permlane32_swap_b32_e32 v46, v50
	s_waitcnt lgkmcnt(0)
	v_add_f32_e32 v46, v50, v46
	v_mov_b32_e32 v47, v46
	s_nop 1
	v_permlane16_swap_b32_e32 v47, v46
	s_waitcnt lgkmcnt(0)
	v_add_f32_e32 v46, v46, v47
	s_nop 1
	v_mov_b32_dpp v47, v46 row_ror:8 row_mask:0xf bank_mask:0xf
	s_waitcnt lgkmcnt(0)
	v_add_f32_e32 v46, v46, v47
	s_nop 1
	v_mov_b32_dpp v47, v46 row_shl:4 row_mask:0xf bank_mask:0x5
	v_mov_b32_dpp v47, v46 row_shr:4 row_mask:0xf bank_mask:0xa
	s_waitcnt lgkmcnt(0)
	v_add_f32_e32 v46, v46, v47
	s_nop 1
	v_mov_b32_dpp v47, v46 quad_perm:[2,3,0,1] row_mask:0xf bank_mask:0xf
	s_waitcnt lgkmcnt(0)
	v_add_f32_e32 v46, v46, v47
	s_nop 1
	v_mov_b32_dpp v47, v46 quad_perm:[1,0,3,2] row_mask:0xf bank_mask:0xf
	s_and_saveexec_b64 s[0:1], vcc
	s_cbranch_execz .LBB0_491
	s_waitcnt lgkmcnt(0)
	v_add_f32_e32 v46, v46, v47
	v_fmamk_f32 v46, v46, 0x3b000000, v246
	s_mov_b32 s2, 0x800000
	v_cmp_gt_f32_e64 s[2:3], s2, v46
	v_mul_f32_e32 v47, 0x4b800000, v46
	s_nop 0
	v_cndmask_b32_e64 v46, v46, v47, s[2:3]
	v_rsq_f32_e32 v46, v46
	s_nop 0
	v_mul_f32_e32 v47, 0x45800000, v46
	v_cndmask_b32_e64 v54, v46, v47, s[2:3]
	v_mul_f32_e32 v38, v38, v54
	v_mul_f32_e32 v44, v44, v54
	v_mul_f32_e32 v39, v39, v54
	v_mul_f32_e32 v38, v38, v162
	v_cvt_pk_bf16_f32 v38, v38, s0
	ds_write_b16 v67, v38 offset:35372
	v_mul_f32_e32 v38, v40, v54
	v_mul_f32_e32 v38, v38, v163
	v_cvt_pk_bf16_f32 v38, v38, s0
	ds_write_b16 v67, v38 offset:35644
	v_mul_f32_e32 v38, v41, v54
	v_mul_f32_e32 v38, v38, v164
	v_cvt_pk_bf16_f32 v38, v38, s0
	ds_write_b16 v67, v38 offset:35916
	v_mul_f32_e32 v38, v42, v54
	v_mul_f32_e32 v38, v38, v165
	v_cvt_pk_bf16_f32 v38, v38, s0
	ds_write_b16 v67, v38 offset:36188
	v_mul_f32_e32 v38, v43, v54
	v_mul_f32_e32 v38, v38, v166
	v_cvt_pk_bf16_f32 v38, v38, s0
	ds_write_b16 v67, v38 offset:36460
	v_mul_f32_e32 v38, v45, v54
	v_mul_f32_e32 v44, v44, v160
	v_mul_f32_e32 v39, v39, v161
	v_mul_f32_e32 v38, v38, v167
	v_cvt_pk_bf16_f32 v44, v44, s0
	v_cvt_pk_bf16_f32 v39, v39, s0
	v_cvt_pk_bf16_f32 v38, v38, s0
	ds_write_b16 v67, v44 offset:34828
	ds_write_b16 v67, v39 offset:35100
	ds_write_b16 v67, v38 offset:36732
; __device__ __forceinline__ float bflo(unsigned w) { return __uint_as_float(w << 16); }
; __device__ __forceinline__ float bfhi(unsigned w) { return __uint_as_float(w & 0xffff0000u); }
; __device__ __forceinline__ unsigned short f2bf(float f) { return (unsigned short)(cvt_pk_bf16(f, 0.f) & 0xffffu); }
; __device__ __forceinline__ void sgu_unit(const Params& p, int l, int un, LAS unsigned char* lds) {
;     ...
;     for (int qi = 0; qi < 16; ++qi) { const int q = wave * 16 + qi;
;         const u32x4 v = vv[qi]; float f[8] = {bflo(v.x), bfhi(v.x), bflo(v.y), bfhi(v.y), bflo(v.z), bfhi(v.z), bflo(v.w), bfhi(v.w)}; float ss = 0.f;
; #pragma unroll
;         for (int j = 0; j < 8; ++j) { f[j] = gelu_tanh(f[j]); ss += f[j] * f[j]; }
;         ss = wave_sum(ss); const float rinv = rsqrtf(ss * (1.0f / 512.0f) + EPS);
;         if ((lane >> 4) == h) { const int c0 = (lane & 15) * 8; const float* g = p.in[I_SGUNG] + l * 512 + h * 128 + c0;
; #pragma unroll
;             for (int j = 0; j < 8; ++j) Vl[(c0 + j) * 136 + q] = f2bf(f[j] * rinv * g[j]); } }
.LBB0_491:
	s_or_b64 exec, exec, s[0:1]
	s_waitcnt vmcnt(8)
	v_lshlrev_b32_e32 v38, 16, v34
	v_lshlrev_b32_e32 v39, 16, v35
	v_and_b32_e32 v41, 0xffff0000, v35
	v_mul_f32_e32 v35, 0x3dd2d3e8, v38
	v_fma_f32 v35, -v35, v38, s33
	v_mul_f32_e32 v35, v35, v38
	v_exp_f32_e32 v35, v35
	v_and_b32_e32 v34, 0xffff0000, v34
	v_lshlrev_b32_e32 v42, 16, v36
	v_and_b32_e32 v43, 0xffff0000, v36
	v_add_f32_e32 v35, 1.0, v35
	v_rcp_f32_e32 v35, v35
	v_mul_f32_e32 v36, 0x3dd2d3e8, v41
	v_fma_f32 v36, -v36, v41, s33
	v_mul_f32_e32 v36, v36, v41
	v_mul_f32_e32 v40, v35, v38
	v_mul_f32_e32 v35, 0x3dd2d3e8, v34
	v_fma_f32 v35, -v35, v34, s33
	v_mul_f32_e32 v35, v35, v34
	v_exp_f32_e32 v35, v35
	v_exp_f32_e32 v36, v36
	v_lshlrev_b32_e32 v44, 16, v37
	v_and_b32_e32 v45, 0xffff0000, v37
	v_add_f32_e32 v35, 1.0, v35
	v_rcp_f32_e32 v35, v35
	v_add_f32_e32 v36, 1.0, v36
	v_rcp_f32_e32 v36, v36
	v_mul_f32_e32 v37, 0x3dd2d3e8, v42
	v_mul_f32_e32 v35, v35, v34
	v_mul_f32_e32 v34, 0x3dd2d3e8, v39
	v_fma_f32 v34, -v34, v39, s33
	v_mul_f32_e32 v34, v34, v39
	v_exp_f32_e32 v34, v34
	v_fma_f32 v37, -v37, v42, s33
	v_mul_f32_e32 v38, 0x3dd2d3e8, v43
	v_mul_f32_e32 v37, v37, v42
	v_add_f32_e32 v34, 1.0, v34
	v_rcp_f32_e32 v34, v34
	v_fma_f32 v38, -v38, v43, s33
	v_mul_f32_e32 v36, v36, v41
	v_exp_f32_e32 v37, v37
	v_mul_f32_e32 v34, v34, v39
	v_mul_f32_e32 v39, 0x3dd2d3e8, v44
	v_mul_f32_e32 v38, v38, v43
	v_fma_f32 v39, -v39, v44, s33
	v_mul_f32_e32 v41, 0x3dd2d3e8, v45
	v_exp_f32_e32 v38, v38
	v_mul_f32_e32 v39, v39, v44
	v_fma_f32 v41, -v41, v45, s33
	v_exp_f32_e32 v39, v39
	v_mul_f32_e32 v41, v41, v45
	v_exp_f32_e32 v41, v41
	v_add_f32_e32 v37, 1.0, v37
	v_rcp_f32_e32 v37, v37
	v_add_f32_e32 v38, 1.0, v38
	v_mul_f32_e32 v46, v35, v35
	v_rcp_f32_e32 v38, v38
	v_add_f32_e32 v39, 1.0, v39
	v_fmac_f32_e32 v46, v40, v40
	v_rcp_f32_e32 v39, v39
	v_add_f32_e32 v41, 1.0, v41
	v_fmac_f32_e32 v46, v34, v34
	v_rcp_f32_e32 v41, v41
	v_fmac_f32_e32 v46, v36, v36
	v_mul_f32_e32 v37, v37, v42
	v_fmac_f32_e32 v46, v37, v37
	v_mul_f32_e32 v38, v38, v43
	v_fmac_f32_e32 v46, v38, v38
	v_mul_f32_e32 v39, v39, v44
	v_fmac_f32_e32 v46, v39, v39
	v_mul_f32_e32 v41, v41, v45
	v_fmac_f32_e32 v46, v41, v41
	v_mov_b32_e32 v42, v46
	s_nop 1
	v_permlane32_swap_b32_e32 v42, v46
	s_waitcnt lgkmcnt(0)
	v_add_f32_e32 v42, v46, v42
	v_mov_b32_e32 v43, v42
	s_nop 1
	v_permlane16_swap_b32_e32 v43, v42
	s_waitcnt lgkmcnt(0)
	v_add_f32_e32 v42, v42, v43
	s_nop 1
	v_mov_b32_dpp v43, v42 row_ror:8 row_mask:0xf bank_mask:0xf
	s_waitcnt lgkmcnt(0)
	v_add_f32_e32 v42, v42, v43
	s_nop 1
	v_mov_b32_dpp v43, v42 row_shl:4 row_mask:0xf bank_mask:0x5
	v_mov_b32_dpp v43, v42 row_shr:4 row_mask:0xf bank_mask:0xa
	s_waitcnt lgkmcnt(0)
	v_add_f32_e32 v42, v42, v43
	s_nop 1
	v_mov_b32_dpp v43, v42 quad_perm:[2,3,0,1] row_mask:0xf bank_mask:0xf
	s_waitcnt lgkmcnt(0)
	v_add_f32_e32 v42, v42, v43
	s_nop 1
	v_mov_b32_dpp v43, v42 quad_perm:[1,0,3,2] row_mask:0xf bank_mask:0xf
	s_and_saveexec_b64 s[0:1], vcc
	s_cbranch_execz .LBB0_493
	s_waitcnt lgkmcnt(0)
	v_add_f32_e32 v42, v42, v43
	v_fmamk_f32 v42, v42, 0x3b000000, v246
	s_mov_b32 s2, 0x800000
	v_cmp_gt_f32_e64 s[2:3], s2, v42
	v_mul_f32_e32 v43, 0x4b800000, v42
	s_nop 0
	v_cndmask_b32_e64 v42, v42, v43, s[2:3]
	v_rsq_f32_e32 v42, v42
	s_nop 0
	v_mul_f32_e32 v43, 0x45800000, v42
	v_cndmask_b32_e64 v50, v42, v43, s[2:3]
	v_mul_f32_e32 v34, v34, v50
	v_mul_f32_e32 v40, v40, v50
	v_mul_f32_e32 v35, v35, v50
	v_mul_f32_e32 v34, v34, v162
	v_cvt_pk_bf16_f32 v34, v34, s0
	ds_write_b16 v67, v34 offset:35374
	v_mul_f32_e32 v34, v36, v50
	v_mul_f32_e32 v34, v34, v163
	v_cvt_pk_bf16_f32 v34, v34, s0
	ds_write_b16 v67, v34 offset:35646
	v_mul_f32_e32 v34, v37, v50
	v_mul_f32_e32 v34, v34, v164
	v_cvt_pk_bf16_f32 v34, v34, s0
	ds_write_b16 v67, v34 offset:35918
	v_mul_f32_e32 v34, v38, v50
	v_mul_f32_e32 v34, v34, v165
	v_cvt_pk_bf16_f32 v34, v34, s0
	ds_write_b16 v67, v34 offset:36190
	v_mul_f32_e32 v34, v39, v50
	v_mul_f32_e32 v34, v34, v166
	v_cvt_pk_bf16_f32 v34, v34, s0
	ds_write_b16 v67, v34 offset:36462
	v_mul_f32_e32 v34, v41, v50
	v_mul_f32_e32 v40, v40, v160
	v_mul_f32_e32 v35, v35, v161
	v_mul_f32_e32 v34, v34, v167
	v_cvt_pk_bf16_f32 v40, v40, s0
	v_cvt_pk_bf16_f32 v35, v35, s0
	v_cvt_pk_bf16_f32 v34, v34, s0
	ds_write_b16 v67, v40 offset:34830
	ds_write_b16 v67, v35 offset:35102
	ds_write_b16 v67, v34 offset:36734
; __device__ __forceinline__ float bflo(unsigned w) { return __uint_as_float(w << 16); }
; __device__ __forceinline__ float bfhi(unsigned w) { return __uint_as_float(w & 0xffff0000u); }
; __device__ __forceinline__ unsigned short f2bf(float f) { return (unsigned short)(cvt_pk_bf16(f, 0.f) & 0xffffu); }
; __device__ __forceinline__ void sgu_unit(const Params& p, int l, int un, LAS unsigned char* lds) {
;     ...
;     for (int qi = 0; qi < 16; ++qi) { const int q = wave * 16 + qi;
;         const u32x4 v = vv[qi]; float f[8] = {bflo(v.x), bfhi(v.x), bflo(v.y), bfhi(v.y), bflo(v.z), bfhi(v.z), bflo(v.w), bfhi(v.w)}; float ss = 0.f;
; #pragma unroll
;         for (int j = 0; j < 8; ++j) { f[j] = gelu_tanh(f[j]); ss += f[j] * f[j]; }
;         ss = wave_sum(ss); const float rinv = rsqrtf(ss * (1.0f / 512.0f) + EPS);
;         if ((lane >> 4) == h) { const int c0 = (lane & 15) * 8; const float* g = p.in[I_SGUNG] + l * 512 + h * 128 + c0;
; #pragma unroll
;             for (int j = 0; j < 8; ++j) Vl[(c0 + j) * 136 + q] = f2bf(f[j] * rinv * g[j]); } }
.LBB0_493:
	s_or_b64 exec, exec, s[0:1]
	s_waitcnt vmcnt(7)
	v_lshlrev_b32_e32 v34, 16, v30
	v_lshlrev_b32_e32 v35, 16, v31
	v_and_b32_e32 v37, 0xffff0000, v31
	v_mul_f32_e32 v31, 0x3dd2d3e8, v34
	v_fma_f32 v31, -v31, v34, s33
	v_mul_f32_e32 v31, v31, v34
	v_exp_f32_e32 v31, v31
	v_and_b32_e32 v30, 0xffff0000, v30
	v_lshlrev_b32_e32 v38, 16, v32
	v_and_b32_e32 v39, 0xffff0000, v32
	v_add_f32_e32 v31, 1.0, v31
	v_rcp_f32_e32 v31, v31
	v_mul_f32_e32 v32, 0x3dd2d3e8, v37
	v_fma_f32 v32, -v32, v37, s33
	v_mul_f32_e32 v32, v32, v37
	v_mul_f32_e32 v36, v31, v34
	v_mul_f32_e32 v31, 0x3dd2d3e8, v30
	v_fma_f32 v31, -v31, v30, s33
	v_mul_f32_e32 v31, v31, v30
	v_exp_f32_e32 v31, v31
	v_exp_f32_e32 v32, v32
	v_lshlrev_b32_e32 v40, 16, v33
	v_and_b32_e32 v41, 0xffff0000, v33
	v_add_f32_e32 v31, 1.0, v31
	v_rcp_f32_e32 v31, v31
	v_add_f32_e32 v32, 1.0, v32
	v_rcp_f32_e32 v32, v32
	v_mul_f32_e32 v33, 0x3dd2d3e8, v38
	v_mul_f32_e32 v31, v31, v30
	v_mul_f32_e32 v30, 0x3dd2d3e8, v35
	v_fma_f32 v30, -v30, v35, s33
	v_mul_f32_e32 v30, v30, v35
	v_exp_f32_e32 v30, v30
	v_fma_f32 v33, -v33, v38, s33
	v_mul_f32_e32 v34, 0x3dd2d3e8, v39
	v_mul_f32_e32 v33, v33, v38
	v_add_f32_e32 v30, 1.0, v30
	v_rcp_f32_e32 v30, v30
	v_fma_f32 v34, -v34, v39, s33
	v_mul_f32_e32 v32, v32, v37
	v_exp_f32_e32 v33, v33
	v_mul_f32_e32 v30, v30, v35
	v_mul_f32_e32 v35, 0x3dd2d3e8, v40
	v_mul_f32_e32 v34, v34, v39
	v_fma_f32 v35, -v35, v40, s33
	v_mul_f32_e32 v37, 0x3dd2d3e8, v41
	v_exp_f32_e32 v34, v34
	v_mul_f32_e32 v35, v35, v40
	v_fma_f32 v37, -v37, v41, s33
	v_exp_f32_e32 v35, v35
	v_mul_f32_e32 v37, v37, v41
	v_exp_f32_e32 v37, v37
	v_add_f32_e32 v33, 1.0, v33
	v_rcp_f32_e32 v33, v33
	v_add_f32_e32 v34, 1.0, v34
	v_mul_f32_e32 v42, v31, v31
	v_rcp_f32_e32 v34, v34
	v_add_f32_e32 v35, 1.0, v35
	v_fmac_f32_e32 v42, v36, v36
	v_rcp_f32_e32 v35, v35
	v_add_f32_e32 v37, 1.0, v37
	v_fmac_f32_e32 v42, v30, v30
	v_rcp_f32_e32 v37, v37
	v_fmac_f32_e32 v42, v32, v32
	v_mul_f32_e32 v33, v33, v38
	v_fmac_f32_e32 v42, v33, v33
	v_mul_f32_e32 v34, v34, v39
	v_fmac_f32_e32 v42, v34, v34
	v_mul_f32_e32 v35, v35, v40
	v_fmac_f32_e32 v42, v35, v35
	v_mul_f32_e32 v37, v37, v41
	v_fmac_f32_e32 v42, v37, v37
	v_mov_b32_e32 v38, v42
	s_nop 1
	v_permlane32_swap_b32_e32 v38, v42
	s_waitcnt lgkmcnt(0)
	v_add_f32_e32 v38, v42, v38
	v_mov_b32_e32 v39, v38
	s_nop 1
	v_permlane16_swap_b32_e32 v39, v38
	s_waitcnt lgkmcnt(0)
	v_add_f32_e32 v38, v38, v39
	s_nop 1
	v_mov_b32_dpp v39, v38 row_ror:8 row_mask:0xf bank_mask:0xf
	s_waitcnt lgkmcnt(0)
	v_add_f32_e32 v38, v38, v39
	s_nop 1
	v_mov_b32_dpp v39, v38 row_shl:4 row_mask:0xf bank_mask:0x5
	v_mov_b32_dpp v39, v38 row_shr:4 row_mask:0xf bank_mask:0xa
	s_waitcnt lgkmcnt(0)
	v_add_f32_e32 v38, v38, v39
	s_nop 1
	v_mov_b32_dpp v39, v38 quad_perm:[2,3,0,1] row_mask:0xf bank_mask:0xf
	s_waitcnt lgkmcnt(0)
	v_add_f32_e32 v38, v38, v39
	s_nop 1
	v_mov_b32_dpp v39, v38 quad_perm:[1,0,3,2] row_mask:0xf bank_mask:0xf
	s_and_saveexec_b64 s[0:1], vcc
	s_cbranch_execz .LBB0_495
	s_waitcnt lgkmcnt(0)
	v_add_f32_e32 v38, v38, v39
	v_fmamk_f32 v38, v38, 0x3b000000, v246
	s_mov_b32 s2, 0x800000
	v_cmp_gt_f32_e64 s[2:3], s2, v38
	v_mul_f32_e32 v39, 0x4b800000, v38
	s_nop 0
	v_cndmask_b32_e64 v38, v38, v39, s[2:3]
	v_rsq_f32_e32 v38, v38
	s_nop 0
	v_mul_f32_e32 v39, 0x45800000, v38
	v_cndmask_b32_e64 v46, v38, v39, s[2:3]
	v_mul_f32_e32 v30, v30, v46
	v_mul_f32_e32 v36, v36, v46
	v_mul_f32_e32 v31, v31, v46
	v_mul_f32_e32 v30, v30, v162
	v_cvt_pk_bf16_f32 v30, v30, s0
	ds_write_b16 v67, v30 offset:35376
	v_mul_f32_e32 v30, v32, v46
	v_mul_f32_e32 v30, v30, v163
	v_cvt_pk_bf16_f32 v30, v30, s0
	ds_write_b16 v67, v30 offset:35648
	v_mul_f32_e32 v30, v33, v46
	v_mul_f32_e32 v30, v30, v164
	v_cvt_pk_bf16_f32 v30, v30, s0
	ds_write_b16 v67, v30 offset:35920
	v_mul_f32_e32 v30, v34, v46
	v_mul_f32_e32 v30, v30, v165
	v_cvt_pk_bf16_f32 v30, v30, s0
	ds_write_b16 v67, v30 offset:36192
	v_mul_f32_e32 v30, v35, v46
	v_mul_f32_e32 v30, v30, v166
	v_cvt_pk_bf16_f32 v30, v30, s0
	ds_write_b16 v67, v30 offset:36464
	v_mul_f32_e32 v30, v37, v46
	v_mul_f32_e32 v36, v36, v160
	v_mul_f32_e32 v31, v31, v161
	v_mul_f32_e32 v30, v30, v167
	v_cvt_pk_bf16_f32 v36, v36, s0
	v_cvt_pk_bf16_f32 v31, v31, s0
	v_cvt_pk_bf16_f32 v30, v30, s0
	ds_write_b16 v67, v36 offset:34832
	ds_write_b16 v67, v31 offset:35104
	ds_write_b16 v67, v30 offset:36736
; __device__ __forceinline__ float bflo(unsigned w) { return __uint_as_float(w << 16); }
; __device__ __forceinline__ float bfhi(unsigned w) { return __uint_as_float(w & 0xffff0000u); }
; __device__ __forceinline__ unsigned short f2bf(float f) { return (unsigned short)(cvt_pk_bf16(f, 0.f) & 0xffffu); }
; __device__ __forceinline__ void sgu_unit(const Params& p, int l, int un, LAS unsigned char* lds) {
;     ...
;     for (int qi = 0; qi < 16; ++qi) { const int q = wave * 16 + qi;
;         const u32x4 v = vv[qi]; float f[8] = {bflo(v.x), bfhi(v.x), bflo(v.y), bfhi(v.y), bflo(v.z), bfhi(v.z), bflo(v.w), bfhi(v.w)}; float ss = 0.f;
; #pragma unroll
;         for (int j = 0; j < 8; ++j) { f[j] = gelu_tanh(f[j]); ss += f[j] * f[j]; }
;         ss = wave_sum(ss); const float rinv = rsqrtf(ss * (1.0f / 512.0f) + EPS);
;         if ((lane >> 4) == h) { const int c0 = (lane & 15) * 8; const float* g = p.in[I_SGUNG] + l * 512 + h * 128 + c0;
; #pragma unroll
;             for (int j = 0; j < 8; ++j) Vl[(c0 + j) * 136 + q] = f2bf(f[j] * rinv * g[j]); } }
.LBB0_495:
	s_or_b64 exec, exec, s[0:1]
	s_waitcnt vmcnt(6)
	v_lshlrev_b32_e32 v30, 16, v26
	v_lshlrev_b32_e32 v31, 16, v27
	v_and_b32_e32 v33, 0xffff0000, v27
	v_mul_f32_e32 v27, 0x3dd2d3e8, v30
	v_fma_f32 v27, -v27, v30, s33
	v_mul_f32_e32 v27, v27, v30
	v_exp_f32_e32 v27, v27
	v_and_b32_e32 v26, 0xffff0000, v26
	v_lshlrev_b32_e32 v34, 16, v28
	v_and_b32_e32 v35, 0xffff0000, v28
	v_add_f32_e32 v27, 1.0, v27
	v_rcp_f32_e32 v27, v27
	v_mul_f32_e32 v28, 0x3dd2d3e8, v33
	v_fma_f32 v28, -v28, v33, s33
	v_mul_f32_e32 v28, v28, v33
	v_mul_f32_e32 v32, v27, v30
	v_mul_f32_e32 v27, 0x3dd2d3e8, v26
	v_fma_f32 v27, -v27, v26, s33
	v_mul_f32_e32 v27, v27, v26
	v_exp_f32_e32 v27, v27
	v_exp_f32_e32 v28, v28
	v_lshlrev_b32_e32 v36, 16, v29
	v_and_b32_e32 v37, 0xffff0000, v29
	v_add_f32_e32 v27, 1.0, v27
	v_rcp_f32_e32 v27, v27
	v_add_f32_e32 v28, 1.0, v28
	v_rcp_f32_e32 v28, v28
	v_mul_f32_e32 v29, 0x3dd2d3e8, v34
	v_mul_f32_e32 v27, v27, v26
	v_mul_f32_e32 v26, 0x3dd2d3e8, v31
	v_fma_f32 v26, -v26, v31, s33
	v_mul_f32_e32 v26, v26, v31
	v_exp_f32_e32 v26, v26
	v_fma_f32 v29, -v29, v34, s33
	v_mul_f32_e32 v30, 0x3dd2d3e8, v35
	v_mul_f32_e32 v29, v29, v34
	v_add_f32_e32 v26, 1.0, v26
	v_rcp_f32_e32 v26, v26
	v_fma_f32 v30, -v30, v35, s33
	v_mul_f32_e32 v28, v28, v33
	v_exp_f32_e32 v29, v29
	v_mul_f32_e32 v26, v26, v31
	v_mul_f32_e32 v31, 0x3dd2d3e8, v36
	v_mul_f32_e32 v30, v30, v35
	v_fma_f32 v31, -v31, v36, s33
	v_mul_f32_e32 v33, 0x3dd2d3e8, v37
	v_exp_f32_e32 v30, v30
	v_mul_f32_e32 v31, v31, v36
	v_fma_f32 v33, -v33, v37, s33
	v_exp_f32_e32 v31, v31
	v_mul_f32_e32 v33, v33, v37
	v_exp_f32_e32 v33, v33
	v_add_f32_e32 v29, 1.0, v29
	v_rcp_f32_e32 v29, v29
	v_add_f32_e32 v30, 1.0, v30
	v_mul_f32_e32 v38, v27, v27
	v_rcp_f32_e32 v30, v30
	v_add_f32_e32 v31, 1.0, v31
	v_fmac_f32_e32 v38, v32, v32
	v_rcp_f32_e32 v31, v31
	v_add_f32_e32 v33, 1.0, v33
	v_fmac_f32_e32 v38, v26, v26
	v_rcp_f32_e32 v33, v33
	v_fmac_f32_e32 v38, v28, v28
	v_mul_f32_e32 v29, v29, v34
	v_fmac_f32_e32 v38, v29, v29
	v_mul_f32_e32 v30, v30, v35
	v_fmac_f32_e32 v38, v30, v30
	v_mul_f32_e32 v31, v31, v36
	v_fmac_f32_e32 v38, v31, v31
	v_mul_f32_e32 v33, v33, v37
	v_fmac_f32_e32 v38, v33, v33
	v_mov_b32_e32 v34, v38
	s_nop 1
	v_permlane32_swap_b32_e32 v34, v38
	s_waitcnt lgkmcnt(0)
	v_add_f32_e32 v34, v38, v34
	v_mov_b32_e32 v35, v34
	s_nop 1
	v_permlane16_swap_b32_e32 v35, v34
	s_waitcnt lgkmcnt(0)
	v_add_f32_e32 v34, v34, v35
	s_nop 1
	v_mov_b32_dpp v35, v34 row_ror:8 row_mask:0xf bank_mask:0xf
	s_waitcnt lgkmcnt(0)
	v_add_f32_e32 v34, v34, v35
	s_nop 1
	v_mov_b32_dpp v35, v34 row_shl:4 row_mask:0xf bank_mask:0x5
	v_mov_b32_dpp v35, v34 row_shr:4 row_mask:0xf bank_mask:0xa
	s_waitcnt lgkmcnt(0)
	v_add_f32_e32 v34, v34, v35
	s_nop 1
	v_mov_b32_dpp v35, v34 quad_perm:[2,3,0,1] row_mask:0xf bank_mask:0xf
	s_waitcnt lgkmcnt(0)
	v_add_f32_e32 v34, v34, v35
	s_nop 1
	v_mov_b32_dpp v35, v34 quad_perm:[1,0,3,2] row_mask:0xf bank_mask:0xf
	s_and_saveexec_b64 s[0:1], vcc
	s_cbranch_execz .LBB0_497
	s_waitcnt lgkmcnt(0)
	v_add_f32_e32 v34, v34, v35
	v_fmamk_f32 v34, v34, 0x3b000000, v246
	s_mov_b32 s2, 0x800000
	v_cmp_gt_f32_e64 s[2:3], s2, v34
	v_mul_f32_e32 v35, 0x4b800000, v34
	s_nop 0
	v_cndmask_b32_e64 v34, v34, v35, s[2:3]
	v_rsq_f32_e32 v34, v34
	s_nop 0
	v_mul_f32_e32 v35, 0x45800000, v34
	v_cndmask_b32_e64 v42, v34, v35, s[2:3]
	v_mul_f32_e32 v26, v26, v42
	v_mul_f32_e32 v32, v32, v42
	v_mul_f32_e32 v27, v27, v42
	v_mul_f32_e32 v26, v26, v162
	v_cvt_pk_bf16_f32 v26, v26, s0
	ds_write_b16 v67, v26 offset:35378
	v_mul_f32_e32 v26, v28, v42
	v_mul_f32_e32 v26, v26, v163
	v_cvt_pk_bf16_f32 v26, v26, s0
	ds_write_b16 v67, v26 offset:35650
	v_mul_f32_e32 v26, v29, v42
	v_mul_f32_e32 v26, v26, v164
	v_cvt_pk_bf16_f32 v26, v26, s0
	ds_write_b16 v67, v26 offset:35922
	v_mul_f32_e32 v26, v30, v42
	v_mul_f32_e32 v26, v26, v165
	v_cvt_pk_bf16_f32 v26, v26, s0
	ds_write_b16 v67, v26 offset:36194
	v_mul_f32_e32 v26, v31, v42
	v_mul_f32_e32 v26, v26, v166
	v_cvt_pk_bf16_f32 v26, v26, s0
	ds_write_b16 v67, v26 offset:36466
	v_mul_f32_e32 v26, v33, v42
	v_mul_f32_e32 v32, v32, v160
	v_mul_f32_e32 v27, v27, v161
	v_mul_f32_e32 v26, v26, v167
	v_cvt_pk_bf16_f32 v32, v32, s0
	v_cvt_pk_bf16_f32 v27, v27, s0
	v_cvt_pk_bf16_f32 v26, v26, s0
	ds_write_b16 v67, v32 offset:34834
	ds_write_b16 v67, v27 offset:35106
	ds_write_b16 v67, v26 offset:36738
; __device__ __forceinline__ float bflo(unsigned w) { return __uint_as_float(w << 16); }
; __device__ __forceinline__ float bfhi(unsigned w) { return __uint_as_float(w & 0xffff0000u); }
; __device__ __forceinline__ unsigned short f2bf(float f) { return (unsigned short)(cvt_pk_bf16(f, 0.f) & 0xffffu); }
; __device__ __forceinline__ void sgu_unit(const Params& p, int l, int un, LAS unsigned char* lds) {
;     ...
;     for (int qi = 0; qi < 16; ++qi) { const int q = wave * 16 + qi;
;         const u32x4 v = vv[qi]; float f[8] = {bflo(v.x), bfhi(v.x), bflo(v.y), bfhi(v.y), bflo(v.z), bfhi(v.z), bflo(v.w), bfhi(v.w)}; float ss = 0.f;
; #pragma unroll
;         for (int j = 0; j < 8; ++j) { f[j] = gelu_tanh(f[j]); ss += f[j] * f[j]; }
;         ss = wave_sum(ss); const float rinv = rsqrtf(ss * (1.0f / 512.0f) + EPS);
;         if ((lane >> 4) == h) { const int c0 = (lane & 15) * 8; const float* g = p.in[I_SGUNG] + l * 512 + h * 128 + c0;
; #pragma unroll
;             for (int j = 0; j < 8; ++j) Vl[(c0 + j) * 136 + q] = f2bf(f[j] * rinv * g[j]); } }
.LBB0_497:
	s_or_b64 exec, exec, s[0:1]
	s_waitcnt vmcnt(5)
	v_lshlrev_b32_e32 v26, 16, v22
	v_lshlrev_b32_e32 v27, 16, v23
	v_and_b32_e32 v29, 0xffff0000, v23
	v_mul_f32_e32 v23, 0x3dd2d3e8, v26
	v_fma_f32 v23, -v23, v26, s33
	v_mul_f32_e32 v23, v23, v26
	v_exp_f32_e32 v23, v23
	v_and_b32_e32 v22, 0xffff0000, v22
	v_lshlrev_b32_e32 v30, 16, v24
	v_and_b32_e32 v31, 0xffff0000, v24
	v_add_f32_e32 v23, 1.0, v23
	v_rcp_f32_e32 v23, v23
	v_mul_f32_e32 v24, 0x3dd2d3e8, v29
	v_fma_f32 v24, -v24, v29, s33
	v_mul_f32_e32 v24, v24, v29
	v_mul_f32_e32 v28, v23, v26
	v_mul_f32_e32 v23, 0x3dd2d3e8, v22
	v_fma_f32 v23, -v23, v22, s33
	v_mul_f32_e32 v23, v23, v22
	v_exp_f32_e32 v23, v23
	v_exp_f32_e32 v24, v24
	v_lshlrev_b32_e32 v32, 16, v25
	v_and_b32_e32 v33, 0xffff0000, v25
	v_add_f32_e32 v23, 1.0, v23
	v_rcp_f32_e32 v23, v23
	v_add_f32_e32 v24, 1.0, v24
	v_rcp_f32_e32 v24, v24
	v_mul_f32_e32 v25, 0x3dd2d3e8, v30
	v_mul_f32_e32 v23, v23, v22
	v_mul_f32_e32 v22, 0x3dd2d3e8, v27
	v_fma_f32 v22, -v22, v27, s33
	v_mul_f32_e32 v22, v22, v27
	v_exp_f32_e32 v22, v22
	v_fma_f32 v25, -v25, v30, s33
	v_mul_f32_e32 v26, 0x3dd2d3e8, v31
	v_mul_f32_e32 v25, v25, v30
	v_add_f32_e32 v22, 1.0, v22
	v_rcp_f32_e32 v22, v22
	v_fma_f32 v26, -v26, v31, s33
	v_mul_f32_e32 v24, v24, v29
	v_exp_f32_e32 v25, v25
	v_mul_f32_e32 v22, v22, v27
	v_mul_f32_e32 v27, 0x3dd2d3e8, v32
	v_mul_f32_e32 v26, v26, v31
	v_fma_f32 v27, -v27, v32, s33
	v_mul_f32_e32 v29, 0x3dd2d3e8, v33
	v_exp_f32_e32 v26, v26
	v_mul_f32_e32 v27, v27, v32
	v_fma_f32 v29, -v29, v33, s33
	v_exp_f32_e32 v27, v27
	v_mul_f32_e32 v29, v29, v33
	v_exp_f32_e32 v29, v29
	v_add_f32_e32 v25, 1.0, v25
	v_rcp_f32_e32 v25, v25
	v_add_f32_e32 v26, 1.0, v26
	v_mul_f32_e32 v34, v23, v23
	v_rcp_f32_e32 v26, v26
	v_add_f32_e32 v27, 1.0, v27
	v_fmac_f32_e32 v34, v28, v28
	v_rcp_f32_e32 v27, v27
	v_add_f32_e32 v29, 1.0, v29
	v_fmac_f32_e32 v34, v22, v22
	v_rcp_f32_e32 v29, v29
	v_fmac_f32_e32 v34, v24, v24
	v_mul_f32_e32 v25, v25, v30
	v_fmac_f32_e32 v34, v25, v25
	v_mul_f32_e32 v26, v26, v31
	v_fmac_f32_e32 v34, v26, v26
	v_mul_f32_e32 v27, v27, v32
	v_fmac_f32_e32 v34, v27, v27
	v_mul_f32_e32 v29, v29, v33
	v_fmac_f32_e32 v34, v29, v29
	v_mov_b32_e32 v30, v34
	s_nop 1
	v_permlane32_swap_b32_e32 v30, v34
	s_waitcnt lgkmcnt(0)
	v_add_f32_e32 v30, v34, v30
	v_mov_b32_e32 v31, v30
	s_nop 1
	v_permlane16_swap_b32_e32 v31, v30
	s_waitcnt lgkmcnt(0)
	v_add_f32_e32 v30, v30, v31
	s_nop 1
	v_mov_b32_dpp v31, v30 row_ror:8 row_mask:0xf bank_mask:0xf
	s_waitcnt lgkmcnt(0)
	v_add_f32_e32 v30, v30, v31
	s_nop 1
	v_mov_b32_dpp v31, v30 row_shl:4 row_mask:0xf bank_mask:0x5
	v_mov_b32_dpp v31, v30 row_shr:4 row_mask:0xf bank_mask:0xa
	s_waitcnt lgkmcnt(0)
	v_add_f32_e32 v30, v30, v31
	s_nop 1
	v_mov_b32_dpp v31, v30 quad_perm:[2,3,0,1] row_mask:0xf bank_mask:0xf
	s_waitcnt lgkmcnt(0)
	v_add_f32_e32 v30, v30, v31
	s_nop 1
	v_mov_b32_dpp v31, v30 quad_perm:[1,0,3,2] row_mask:0xf bank_mask:0xf
	s_and_saveexec_b64 s[0:1], vcc
	s_cbranch_execz .LBB0_499
	s_waitcnt lgkmcnt(0)
	v_add_f32_e32 v30, v30, v31
	v_fmamk_f32 v30, v30, 0x3b000000, v246
	s_mov_b32 s2, 0x800000
	v_cmp_gt_f32_e64 s[2:3], s2, v30
	v_mul_f32_e32 v31, 0x4b800000, v30
	s_nop 0
	v_cndmask_b32_e64 v30, v30, v31, s[2:3]
	v_rsq_f32_e32 v30, v30
	s_nop 0
	v_mul_f32_e32 v31, 0x45800000, v30
	v_cndmask_b32_e64 v38, v30, v31, s[2:3]
	v_mul_f32_e32 v22, v22, v38
	v_mul_f32_e32 v28, v28, v38
	v_mul_f32_e32 v23, v23, v38
	v_mul_f32_e32 v22, v22, v162
	v_cvt_pk_bf16_f32 v22, v22, s0
	ds_write_b16 v67, v22 offset:35380
	v_mul_f32_e32 v22, v24, v38
	v_mul_f32_e32 v22, v22, v163
	v_cvt_pk_bf16_f32 v22, v22, s0
	ds_write_b16 v67, v22 offset:35652
	v_mul_f32_e32 v22, v25, v38
	v_mul_f32_e32 v22, v22, v164
	v_cvt_pk_bf16_f32 v22, v22, s0
	ds_write_b16 v67, v22 offset:35924
	v_mul_f32_e32 v22, v26, v38
	v_mul_f32_e32 v22, v22, v165
	v_cvt_pk_bf16_f32 v22, v22, s0
	ds_write_b16 v67, v22 offset:36196
	v_mul_f32_e32 v22, v27, v38
	v_mul_f32_e32 v22, v22, v166
	v_cvt_pk_bf16_f32 v22, v22, s0
	ds_write_b16 v67, v22 offset:36468
	v_mul_f32_e32 v22, v29, v38
	v_mul_f32_e32 v28, v28, v160
	v_mul_f32_e32 v23, v23, v161
	v_mul_f32_e32 v22, v22, v167
	v_cvt_pk_bf16_f32 v28, v28, s0
	v_cvt_pk_bf16_f32 v23, v23, s0
	v_cvt_pk_bf16_f32 v22, v22, s0
	ds_write_b16 v67, v28 offset:34836
	ds_write_b16 v67, v23 offset:35108
	ds_write_b16 v67, v22 offset:36740
; __device__ __forceinline__ float bflo(unsigned w) { return __uint_as_float(w << 16); }
; __device__ __forceinline__ float bfhi(unsigned w) { return __uint_as_float(w & 0xffff0000u); }
; __device__ __forceinline__ unsigned short f2bf(float f) { return (unsigned short)(cvt_pk_bf16(f, 0.f) & 0xffffu); }
; __device__ __forceinline__ void sgu_unit(const Params& p, int l, int un, LAS unsigned char* lds) {
;     ...
;     for (int qi = 0; qi < 16; ++qi) { const int q = wave * 16 + qi;
;         const u32x4 v = vv[qi]; float f[8] = {bflo(v.x), bfhi(v.x), bflo(v.y), bfhi(v.y), bflo(v.z), bfhi(v.z), bflo(v.w), bfhi(v.w)}; float ss = 0.f;
; #pragma unroll
;         for (int j = 0; j < 8; ++j) { f[j] = gelu_tanh(f[j]); ss += f[j] * f[j]; }
;         ss = wave_sum(ss); const float rinv = rsqrtf(ss * (1.0f / 512.0f) + EPS);
;         if ((lane >> 4) == h) { const int c0 = (lane & 15) * 8; const float* g = p.in[I_SGUNG] + l * 512 + h * 128 + c0;
; #pragma unroll
;             for (int j = 0; j < 8; ++j) Vl[(c0 + j) * 136 + q] = f2bf(f[j] * rinv * g[j]); } }
.LBB0_499:
	s_or_b64 exec, exec, s[0:1]
	s_waitcnt vmcnt(4)
	v_lshlrev_b32_e32 v22, 16, v18
	v_lshlrev_b32_e32 v23, 16, v19
	v_and_b32_e32 v25, 0xffff0000, v19
	v_mul_f32_e32 v19, 0x3dd2d3e8, v22
	v_fma_f32 v19, -v19, v22, s33
	v_mul_f32_e32 v19, v19, v22
	v_exp_f32_e32 v19, v19
	v_and_b32_e32 v18, 0xffff0000, v18
	v_lshlrev_b32_e32 v26, 16, v20
	v_and_b32_e32 v27, 0xffff0000, v20
	v_add_f32_e32 v19, 1.0, v19
	v_rcp_f32_e32 v19, v19
	v_mul_f32_e32 v20, 0x3dd2d3e8, v25
	v_fma_f32 v20, -v20, v25, s33
	v_mul_f32_e32 v20, v20, v25
	v_mul_f32_e32 v24, v19, v22
	v_mul_f32_e32 v19, 0x3dd2d3e8, v18
	v_fma_f32 v19, -v19, v18, s33
	v_mul_f32_e32 v19, v19, v18
	v_exp_f32_e32 v19, v19
	v_exp_f32_e32 v20, v20
	v_lshlrev_b32_e32 v28, 16, v21
	v_and_b32_e32 v29, 0xffff0000, v21
	v_add_f32_e32 v19, 1.0, v19
	v_rcp_f32_e32 v19, v19
	v_add_f32_e32 v20, 1.0, v20
	v_rcp_f32_e32 v20, v20
	v_mul_f32_e32 v21, 0x3dd2d3e8, v26
	v_mul_f32_e32 v19, v19, v18
	v_mul_f32_e32 v18, 0x3dd2d3e8, v23
	v_fma_f32 v18, -v18, v23, s33
	v_mul_f32_e32 v18, v18, v23
	v_exp_f32_e32 v18, v18
	v_fma_f32 v21, -v21, v26, s33
	v_mul_f32_e32 v22, 0x3dd2d3e8, v27
	v_mul_f32_e32 v21, v21, v26
	v_add_f32_e32 v18, 1.0, v18
	v_rcp_f32_e32 v18, v18
	v_fma_f32 v22, -v22, v27, s33
	v_mul_f32_e32 v20, v20, v25
	v_exp_f32_e32 v21, v21
	v_mul_f32_e32 v18, v18, v23
	v_mul_f32_e32 v23, 0x3dd2d3e8, v28
	v_mul_f32_e32 v22, v22, v27
	v_fma_f32 v23, -v23, v28, s33
	v_mul_f32_e32 v25, 0x3dd2d3e8, v29
	v_exp_f32_e32 v22, v22
	v_mul_f32_e32 v23, v23, v28
	v_fma_f32 v25, -v25, v29, s33
	v_exp_f32_e32 v23, v23
	v_mul_f32_e32 v25, v25, v29
	v_exp_f32_e32 v25, v25
	v_add_f32_e32 v21, 1.0, v21
	v_rcp_f32_e32 v21, v21
	v_add_f32_e32 v22, 1.0, v22
	v_mul_f32_e32 v30, v19, v19
	v_rcp_f32_e32 v22, v22
	v_add_f32_e32 v23, 1.0, v23
	v_fmac_f32_e32 v30, v24, v24
	v_rcp_f32_e32 v23, v23
	v_add_f32_e32 v25, 1.0, v25
	v_fmac_f32_e32 v30, v18, v18
	v_rcp_f32_e32 v25, v25
	v_fmac_f32_e32 v30, v20, v20
	v_mul_f32_e32 v21, v21, v26
	v_fmac_f32_e32 v30, v21, v21
	v_mul_f32_e32 v22, v22, v27
	v_fmac_f32_e32 v30, v22, v22
	v_mul_f32_e32 v23, v23, v28
	v_fmac_f32_e32 v30, v23, v23
	v_mul_f32_e32 v25, v25, v29
	v_fmac_f32_e32 v30, v25, v25
	v_mov_b32_e32 v26, v30
	s_nop 1
	v_permlane32_swap_b32_e32 v26, v30
	s_waitcnt lgkmcnt(0)
	v_add_f32_e32 v26, v30, v26
	v_mov_b32_e32 v27, v26
	s_nop 1
	v_permlane16_swap_b32_e32 v27, v26
	s_waitcnt lgkmcnt(0)
	v_add_f32_e32 v26, v26, v27
	s_nop 1
	v_mov_b32_dpp v27, v26 row_ror:8 row_mask:0xf bank_mask:0xf
	s_waitcnt lgkmcnt(0)
	v_add_f32_e32 v26, v26, v27
	s_nop 1
	v_mov_b32_dpp v27, v26 row_shl:4 row_mask:0xf bank_mask:0x5
	v_mov_b32_dpp v27, v26 row_shr:4 row_mask:0xf bank_mask:0xa
	s_waitcnt lgkmcnt(0)
	v_add_f32_e32 v26, v26, v27
	s_nop 1
	v_mov_b32_dpp v27, v26 quad_perm:[2,3,0,1] row_mask:0xf bank_mask:0xf
	s_waitcnt lgkmcnt(0)
	v_add_f32_e32 v26, v26, v27
	s_nop 1
	v_mov_b32_dpp v27, v26 quad_perm:[1,0,3,2] row_mask:0xf bank_mask:0xf
	s_and_saveexec_b64 s[0:1], vcc
	s_cbranch_execz .LBB0_501
	s_waitcnt lgkmcnt(0)
	v_add_f32_e32 v26, v26, v27
	v_fmamk_f32 v26, v26, 0x3b000000, v246
	s_mov_b32 s2, 0x800000
	v_cmp_gt_f32_e64 s[2:3], s2, v26
	v_mul_f32_e32 v27, 0x4b800000, v26
	s_nop 0
	v_cndmask_b32_e64 v26, v26, v27, s[2:3]
	v_rsq_f32_e32 v26, v26
	s_nop 0
	v_mul_f32_e32 v27, 0x45800000, v26
	v_cndmask_b32_e64 v34, v26, v27, s[2:3]
	v_mul_f32_e32 v18, v18, v34
	v_mul_f32_e32 v24, v24, v34
	v_mul_f32_e32 v19, v19, v34
	v_mul_f32_e32 v18, v18, v162
	v_cvt_pk_bf16_f32 v18, v18, s0
	ds_write_b16 v67, v18 offset:35382
	v_mul_f32_e32 v18, v20, v34
	v_mul_f32_e32 v18, v18, v163
	v_cvt_pk_bf16_f32 v18, v18, s0
	ds_write_b16 v67, v18 offset:35654
	v_mul_f32_e32 v18, v21, v34
	v_mul_f32_e32 v18, v18, v164
	v_cvt_pk_bf16_f32 v18, v18, s0
	ds_write_b16 v67, v18 offset:35926
	v_mul_f32_e32 v18, v22, v34
	v_mul_f32_e32 v18, v18, v165
	v_cvt_pk_bf16_f32 v18, v18, s0
	ds_write_b16 v67, v18 offset:36198
	v_mul_f32_e32 v18, v23, v34
	v_mul_f32_e32 v18, v18, v166
	v_cvt_pk_bf16_f32 v18, v18, s0
	ds_write_b16 v67, v18 offset:36470
	v_mul_f32_e32 v18, v25, v34
	v_mul_f32_e32 v24, v24, v160
	v_mul_f32_e32 v19, v19, v161
	v_mul_f32_e32 v18, v18, v167
	v_cvt_pk_bf16_f32 v24, v24, s0
	v_cvt_pk_bf16_f32 v19, v19, s0
	v_cvt_pk_bf16_f32 v18, v18, s0
	ds_write_b16 v67, v24 offset:34838
	ds_write_b16 v67, v19 offset:35110
	ds_write_b16 v67, v18 offset:36742
; __device__ __forceinline__ float bflo(unsigned w) { return __uint_as_float(w << 16); }
; __device__ __forceinline__ float bfhi(unsigned w) { return __uint_as_float(w & 0xffff0000u); }
; __device__ __forceinline__ unsigned short f2bf(float f) { return (unsigned short)(cvt_pk_bf16(f, 0.f) & 0xffffu); }
; __device__ __forceinline__ void sgu_unit(const Params& p, int l, int un, LAS unsigned char* lds) {
;     ...
;     for (int qi = 0; qi < 16; ++qi) { const int q = wave * 16 + qi;
;         const u32x4 v = vv[qi]; float f[8] = {bflo(v.x), bfhi(v.x), bflo(v.y), bfhi(v.y), bflo(v.z), bfhi(v.z), bflo(v.w), bfhi(v.w)}; float ss = 0.f;
; #pragma unroll
;         for (int j = 0; j < 8; ++j) { f[j] = gelu_tanh(f[j]); ss += f[j] * f[j]; }
;         ss = wave_sum(ss); const float rinv = rsqrtf(ss * (1.0f / 512.0f) + EPS);
;         if ((lane >> 4) == h) { const int c0 = (lane & 15) * 8; const float* g = p.in[I_SGUNG] + l * 512 + h * 128 + c0;
; #pragma unroll
;             for (int j = 0; j < 8; ++j) Vl[(c0 + j) * 136 + q] = f2bf(f[j] * rinv * g[j]); } }
.LBB0_501:
	s_or_b64 exec, exec, s[0:1]
	s_waitcnt vmcnt(3)
	v_lshlrev_b32_e32 v18, 16, v14
	v_lshlrev_b32_e32 v19, 16, v15
	v_and_b32_e32 v21, 0xffff0000, v15
	v_mul_f32_e32 v15, 0x3dd2d3e8, v18
	v_fma_f32 v15, -v15, v18, s33
	v_mul_f32_e32 v15, v15, v18
	v_exp_f32_e32 v15, v15
	v_and_b32_e32 v14, 0xffff0000, v14
	v_lshlrev_b32_e32 v22, 16, v16
	v_and_b32_e32 v23, 0xffff0000, v16
	v_add_f32_e32 v15, 1.0, v15
	v_rcp_f32_e32 v15, v15
	v_mul_f32_e32 v16, 0x3dd2d3e8, v21
	v_fma_f32 v16, -v16, v21, s33
	v_mul_f32_e32 v16, v16, v21
	v_mul_f32_e32 v20, v15, v18
	v_mul_f32_e32 v15, 0x3dd2d3e8, v14
	v_fma_f32 v15, -v15, v14, s33
	v_mul_f32_e32 v15, v15, v14
	v_exp_f32_e32 v15, v15
	v_exp_f32_e32 v16, v16
	v_lshlrev_b32_e32 v24, 16, v17
	v_and_b32_e32 v25, 0xffff0000, v17
	v_add_f32_e32 v15, 1.0, v15
	v_rcp_f32_e32 v15, v15
	v_add_f32_e32 v16, 1.0, v16
	v_rcp_f32_e32 v16, v16
	v_mul_f32_e32 v17, 0x3dd2d3e8, v22
	v_mul_f32_e32 v15, v15, v14
	v_mul_f32_e32 v14, 0x3dd2d3e8, v19
	v_fma_f32 v14, -v14, v19, s33
	v_mul_f32_e32 v14, v14, v19
	v_exp_f32_e32 v14, v14
	v_fma_f32 v17, -v17, v22, s33
	v_mul_f32_e32 v18, 0x3dd2d3e8, v23
	v_mul_f32_e32 v17, v17, v22
	v_add_f32_e32 v14, 1.0, v14
	v_rcp_f32_e32 v14, v14
	v_fma_f32 v18, -v18, v23, s33
	v_mul_f32_e32 v16, v16, v21
	v_exp_f32_e32 v17, v17
	v_mul_f32_e32 v14, v14, v19
	v_mul_f32_e32 v19, 0x3dd2d3e8, v24
	v_mul_f32_e32 v18, v18, v23
	v_fma_f32 v19, -v19, v24, s33
	v_mul_f32_e32 v21, 0x3dd2d3e8, v25
	v_exp_f32_e32 v18, v18
	v_mul_f32_e32 v19, v19, v24
	v_fma_f32 v21, -v21, v25, s33
	v_exp_f32_e32 v19, v19
	v_mul_f32_e32 v21, v21, v25
	v_exp_f32_e32 v21, v21
	v_add_f32_e32 v17, 1.0, v17
	v_rcp_f32_e32 v17, v17
	v_add_f32_e32 v18, 1.0, v18
	v_mul_f32_e32 v26, v15, v15
	v_rcp_f32_e32 v18, v18
	v_add_f32_e32 v19, 1.0, v19
	v_fmac_f32_e32 v26, v20, v20
	v_rcp_f32_e32 v19, v19
	v_add_f32_e32 v21, 1.0, v21
	v_fmac_f32_e32 v26, v14, v14
	v_rcp_f32_e32 v21, v21
	v_fmac_f32_e32 v26, v16, v16
	v_mul_f32_e32 v17, v17, v22
	v_fmac_f32_e32 v26, v17, v17
	v_mul_f32_e32 v18, v18, v23
	v_fmac_f32_e32 v26, v18, v18
	v_mul_f32_e32 v19, v19, v24
	v_fmac_f32_e32 v26, v19, v19
	v_mul_f32_e32 v21, v21, v25
	v_fmac_f32_e32 v26, v21, v21
	v_mov_b32_e32 v22, v26
	s_nop 1
	v_permlane32_swap_b32_e32 v22, v26
	s_waitcnt lgkmcnt(0)
	v_add_f32_e32 v22, v26, v22
	v_mov_b32_e32 v23, v22
	s_nop 1
	v_permlane16_swap_b32_e32 v23, v22
	s_waitcnt lgkmcnt(0)
	v_add_f32_e32 v22, v22, v23
	s_nop 1
	v_mov_b32_dpp v23, v22 row_ror:8 row_mask:0xf bank_mask:0xf
	s_waitcnt lgkmcnt(0)
	v_add_f32_e32 v22, v22, v23
	s_nop 1
	v_mov_b32_dpp v23, v22 row_shl:4 row_mask:0xf bank_mask:0x5
	v_mov_b32_dpp v23, v22 row_shr:4 row_mask:0xf bank_mask:0xa
	s_waitcnt lgkmcnt(0)
	v_add_f32_e32 v22, v22, v23
	s_nop 1
	v_mov_b32_dpp v23, v22 quad_perm:[2,3,0,1] row_mask:0xf bank_mask:0xf
	s_waitcnt lgkmcnt(0)
	v_add_f32_e32 v22, v22, v23
	s_nop 1
	v_mov_b32_dpp v23, v22 quad_perm:[1,0,3,2] row_mask:0xf bank_mask:0xf
	s_and_saveexec_b64 s[0:1], vcc
	s_cbranch_execz .LBB0_503
	s_waitcnt lgkmcnt(0)
	v_add_f32_e32 v22, v22, v23
	v_fmamk_f32 v22, v22, 0x3b000000, v246
	s_mov_b32 s2, 0x800000
	v_cmp_gt_f32_e64 s[2:3], s2, v22
	v_mul_f32_e32 v23, 0x4b800000, v22
	s_nop 0
	v_cndmask_b32_e64 v22, v22, v23, s[2:3]
	v_rsq_f32_e32 v22, v22
	s_nop 0
	v_mul_f32_e32 v23, 0x45800000, v22
	v_cndmask_b32_e64 v30, v22, v23, s[2:3]
	v_mul_f32_e32 v14, v14, v30
	v_mul_f32_e32 v20, v20, v30
	v_mul_f32_e32 v15, v15, v30
	v_mul_f32_e32 v14, v14, v162
	v_cvt_pk_bf16_f32 v14, v14, s0
	ds_write_b16 v67, v14 offset:35384
	v_mul_f32_e32 v14, v16, v30
	v_mul_f32_e32 v14, v14, v163
	v_cvt_pk_bf16_f32 v14, v14, s0
	ds_write_b16 v67, v14 offset:35656
	v_mul_f32_e32 v14, v17, v30
	v_mul_f32_e32 v14, v14, v164
	v_cvt_pk_bf16_f32 v14, v14, s0
	ds_write_b16 v67, v14 offset:35928
	v_mul_f32_e32 v14, v18, v30
	v_mul_f32_e32 v14, v14, v165
	v_cvt_pk_bf16_f32 v14, v14, s0
	ds_write_b16 v67, v14 offset:36200
	v_mul_f32_e32 v14, v19, v30
	v_mul_f32_e32 v14, v14, v166
	v_cvt_pk_bf16_f32 v14, v14, s0
	ds_write_b16 v67, v14 offset:36472
	v_mul_f32_e32 v14, v21, v30
	v_mul_f32_e32 v20, v20, v160
	v_mul_f32_e32 v15, v15, v161
	v_mul_f32_e32 v14, v14, v167
	v_cvt_pk_bf16_f32 v20, v20, s0
	v_cvt_pk_bf16_f32 v15, v15, s0
	v_cvt_pk_bf16_f32 v14, v14, s0
	ds_write_b16 v67, v20 offset:34840
	ds_write_b16 v67, v15 offset:35112
	ds_write_b16 v67, v14 offset:36744
; __device__ __forceinline__ float bflo(unsigned w) { return __uint_as_float(w << 16); }
; __device__ __forceinline__ float bfhi(unsigned w) { return __uint_as_float(w & 0xffff0000u); }
; __device__ __forceinline__ unsigned short f2bf(float f) { return (unsigned short)(cvt_pk_bf16(f, 0.f) & 0xffffu); }
; __device__ __forceinline__ void sgu_unit(const Params& p, int l, int un, LAS unsigned char* lds) {
;     ...
;     for (int qi = 0; qi < 16; ++qi) { const int q = wave * 16 + qi;
;         const u32x4 v = vv[qi]; float f[8] = {bflo(v.x), bfhi(v.x), bflo(v.y), bfhi(v.y), bflo(v.z), bfhi(v.z), bflo(v.w), bfhi(v.w)}; float ss = 0.f;
; #pragma unroll
;         for (int j = 0; j < 8; ++j) { f[j] = gelu_tanh(f[j]); ss += f[j] * f[j]; }
;         ss = wave_sum(ss); const float rinv = rsqrtf(ss * (1.0f / 512.0f) + EPS);
;         if ((lane >> 4) == h) { const int c0 = (lane & 15) * 8; const float* g = p.in[I_SGUNG] + l * 512 + h * 128 + c0;
; #pragma unroll
;             for (int j = 0; j < 8; ++j) Vl[(c0 + j) * 136 + q] = f2bf(f[j] * rinv * g[j]); } }
.LBB0_503:
	s_or_b64 exec, exec, s[0:1]
	s_waitcnt vmcnt(2)
	v_lshlrev_b32_e32 v14, 16, v10
	v_lshlrev_b32_e32 v15, 16, v11
	v_and_b32_e32 v17, 0xffff0000, v11
	v_mul_f32_e32 v11, 0x3dd2d3e8, v14
	v_fma_f32 v11, -v11, v14, s33
	v_mul_f32_e32 v11, v11, v14
	v_exp_f32_e32 v11, v11
	v_and_b32_e32 v10, 0xffff0000, v10
	v_lshlrev_b32_e32 v18, 16, v12
	v_and_b32_e32 v19, 0xffff0000, v12
	v_add_f32_e32 v11, 1.0, v11
	v_rcp_f32_e32 v11, v11
	v_mul_f32_e32 v12, 0x3dd2d3e8, v17
	v_fma_f32 v12, -v12, v17, s33
	v_mul_f32_e32 v12, v12, v17
	v_mul_f32_e32 v16, v11, v14
	v_mul_f32_e32 v11, 0x3dd2d3e8, v10
	v_fma_f32 v11, -v11, v10, s33
	v_mul_f32_e32 v11, v11, v10
	v_exp_f32_e32 v11, v11
	v_exp_f32_e32 v12, v12
	v_lshlrev_b32_e32 v20, 16, v13
	v_and_b32_e32 v21, 0xffff0000, v13
	v_add_f32_e32 v11, 1.0, v11
	v_rcp_f32_e32 v11, v11
	v_add_f32_e32 v12, 1.0, v12
	v_rcp_f32_e32 v12, v12
	v_mul_f32_e32 v13, 0x3dd2d3e8, v18
	v_mul_f32_e32 v11, v11, v10
	v_mul_f32_e32 v10, 0x3dd2d3e8, v15
	v_fma_f32 v10, -v10, v15, s33
	v_mul_f32_e32 v10, v10, v15
	v_exp_f32_e32 v10, v10
	v_fma_f32 v13, -v13, v18, s33
	v_mul_f32_e32 v14, 0x3dd2d3e8, v19
	v_mul_f32_e32 v13, v13, v18
	v_add_f32_e32 v10, 1.0, v10
	v_rcp_f32_e32 v10, v10
	v_fma_f32 v14, -v14, v19, s33
	v_mul_f32_e32 v12, v12, v17
	v_exp_f32_e32 v13, v13
	v_mul_f32_e32 v10, v10, v15
	v_mul_f32_e32 v15, 0x3dd2d3e8, v20
	v_mul_f32_e32 v14, v14, v19
	v_fma_f32 v15, -v15, v20, s33
	v_mul_f32_e32 v17, 0x3dd2d3e8, v21
	v_exp_f32_e32 v14, v14
	v_mul_f32_e32 v15, v15, v20
	v_fma_f32 v17, -v17, v21, s33
	v_exp_f32_e32 v15, v15
	v_mul_f32_e32 v17, v17, v21
	v_exp_f32_e32 v17, v17
	v_add_f32_e32 v13, 1.0, v13
	v_rcp_f32_e32 v13, v13
	v_add_f32_e32 v14, 1.0, v14
	v_mul_f32_e32 v22, v11, v11
	v_rcp_f32_e32 v14, v14
	v_add_f32_e32 v15, 1.0, v15
	v_fmac_f32_e32 v22, v16, v16
	v_rcp_f32_e32 v15, v15
	v_add_f32_e32 v17, 1.0, v17
	v_fmac_f32_e32 v22, v10, v10
	v_rcp_f32_e32 v17, v17
	v_fmac_f32_e32 v22, v12, v12
	v_mul_f32_e32 v13, v13, v18
	v_fmac_f32_e32 v22, v13, v13
	v_mul_f32_e32 v14, v14, v19
	v_fmac_f32_e32 v22, v14, v14
	v_mul_f32_e32 v15, v15, v20
	v_fmac_f32_e32 v22, v15, v15
	v_mul_f32_e32 v17, v17, v21
	v_fmac_f32_e32 v22, v17, v17
	v_mov_b32_e32 v18, v22
	s_nop 1
	v_permlane32_swap_b32_e32 v18, v22
	s_waitcnt lgkmcnt(0)
	v_add_f32_e32 v18, v22, v18
	v_mov_b32_e32 v19, v18
	s_nop 1
	v_permlane16_swap_b32_e32 v19, v18
	s_waitcnt lgkmcnt(0)
	v_add_f32_e32 v18, v18, v19
	s_nop 1
	v_mov_b32_dpp v19, v18 row_ror:8 row_mask:0xf bank_mask:0xf
	s_waitcnt lgkmcnt(0)
	v_add_f32_e32 v18, v18, v19
	s_nop 1
	v_mov_b32_dpp v19, v18 row_shl:4 row_mask:0xf bank_mask:0x5
	v_mov_b32_dpp v19, v18 row_shr:4 row_mask:0xf bank_mask:0xa
	s_waitcnt lgkmcnt(0)
	v_add_f32_e32 v18, v18, v19
	s_nop 1
	v_mov_b32_dpp v19, v18 quad_perm:[2,3,0,1] row_mask:0xf bank_mask:0xf
	s_waitcnt lgkmcnt(0)
	v_add_f32_e32 v18, v18, v19
	s_nop 1
	v_mov_b32_dpp v19, v18 quad_perm:[1,0,3,2] row_mask:0xf bank_mask:0xf
	s_and_saveexec_b64 s[0:1], vcc
	s_cbranch_execz .LBB0_505
	s_waitcnt lgkmcnt(0)
	v_add_f32_e32 v18, v18, v19
	v_fmamk_f32 v18, v18, 0x3b000000, v246
	s_mov_b32 s2, 0x800000
	v_cmp_gt_f32_e64 s[2:3], s2, v18
	v_mul_f32_e32 v19, 0x4b800000, v18
	s_nop 0
	v_cndmask_b32_e64 v18, v18, v19, s[2:3]
	v_rsq_f32_e32 v18, v18
	s_nop 0
	v_mul_f32_e32 v19, 0x45800000, v18
	v_cndmask_b32_e64 v26, v18, v19, s[2:3]
	v_mul_f32_e32 v10, v10, v26
	v_mul_f32_e32 v16, v16, v26
	v_mul_f32_e32 v11, v11, v26
	v_mul_f32_e32 v10, v10, v162
	v_cvt_pk_bf16_f32 v10, v10, s0
	ds_write_b16 v67, v10 offset:35386
	v_mul_f32_e32 v10, v12, v26
	v_mul_f32_e32 v10, v10, v163
	v_cvt_pk_bf16_f32 v10, v10, s0
	ds_write_b16 v67, v10 offset:35658
	v_mul_f32_e32 v10, v13, v26
	v_mul_f32_e32 v10, v10, v164
	v_cvt_pk_bf16_f32 v10, v10, s0
	ds_write_b16 v67, v10 offset:35930
	v_mul_f32_e32 v10, v14, v26
	v_mul_f32_e32 v10, v10, v165
	v_cvt_pk_bf16_f32 v10, v10, s0
	ds_write_b16 v67, v10 offset:36202
	v_mul_f32_e32 v10, v15, v26
	v_mul_f32_e32 v10, v10, v166
	v_cvt_pk_bf16_f32 v10, v10, s0
	ds_write_b16 v67, v10 offset:36474
	v_mul_f32_e32 v10, v17, v26
	v_mul_f32_e32 v16, v16, v160
	v_mul_f32_e32 v11, v11, v161
	v_mul_f32_e32 v10, v10, v167
	v_cvt_pk_bf16_f32 v16, v16, s0
	v_cvt_pk_bf16_f32 v11, v11, s0
	v_cvt_pk_bf16_f32 v10, v10, s0
	ds_write_b16 v67, v16 offset:34842
	ds_write_b16 v67, v11 offset:35114
	ds_write_b16 v67, v10 offset:36746
; __device__ __forceinline__ float bflo(unsigned w) { return __uint_as_float(w << 16); }
; __device__ __forceinline__ float bfhi(unsigned w) { return __uint_as_float(w & 0xffff0000u); }
; __device__ __forceinline__ unsigned short f2bf(float f) { return (unsigned short)(cvt_pk_bf16(f, 0.f) & 0xffffu); }
; __device__ __forceinline__ void sgu_unit(const Params& p, int l, int un, LAS unsigned char* lds) {
;     ...
;     for (int qi = 0; qi < 16; ++qi) { const int q = wave * 16 + qi;
;         const u32x4 v = vv[qi]; float f[8] = {bflo(v.x), bfhi(v.x), bflo(v.y), bfhi(v.y), bflo(v.z), bfhi(v.z), bflo(v.w), bfhi(v.w)}; float ss = 0.f;
; #pragma unroll
;         for (int j = 0; j < 8; ++j) { f[j] = gelu_tanh(f[j]); ss += f[j] * f[j]; }
;         ss = wave_sum(ss); const float rinv = rsqrtf(ss * (1.0f / 512.0f) + EPS);
;         if ((lane >> 4) == h) { const int c0 = (lane & 15) * 8; const float* g = p.in[I_SGUNG] + l * 512 + h * 128 + c0;
; #pragma unroll
;             for (int j = 0; j < 8; ++j) Vl[(c0 + j) * 136 + q] = f2bf(f[j] * rinv * g[j]); } }
.LBB0_505:
	s_or_b64 exec, exec, s[0:1]
	s_waitcnt vmcnt(1)
	v_lshlrev_b32_e32 v10, 16, v6
	v_lshlrev_b32_e32 v11, 16, v7
	v_and_b32_e32 v13, 0xffff0000, v7
	v_mul_f32_e32 v7, 0x3dd2d3e8, v10
	v_fma_f32 v7, -v7, v10, s33
	v_mul_f32_e32 v7, v7, v10
	v_exp_f32_e32 v7, v7
	v_and_b32_e32 v6, 0xffff0000, v6
	v_lshlrev_b32_e32 v14, 16, v8
	v_and_b32_e32 v15, 0xffff0000, v8
	v_add_f32_e32 v7, 1.0, v7
	v_rcp_f32_e32 v7, v7
	v_mul_f32_e32 v8, 0x3dd2d3e8, v13
	v_fma_f32 v8, -v8, v13, s33
	v_mul_f32_e32 v8, v8, v13
	v_mul_f32_e32 v12, v7, v10
	v_mul_f32_e32 v7, 0x3dd2d3e8, v6
	v_fma_f32 v7, -v7, v6, s33
	v_mul_f32_e32 v7, v7, v6
	v_exp_f32_e32 v7, v7
	v_exp_f32_e32 v8, v8
	v_lshlrev_b32_e32 v16, 16, v9
	v_and_b32_e32 v17, 0xffff0000, v9
	v_add_f32_e32 v7, 1.0, v7
	v_rcp_f32_e32 v7, v7
	v_add_f32_e32 v8, 1.0, v8
	v_rcp_f32_e32 v8, v8
	v_mul_f32_e32 v9, 0x3dd2d3e8, v14
	v_mul_f32_e32 v7, v7, v6
	v_mul_f32_e32 v6, 0x3dd2d3e8, v11
	v_fma_f32 v6, -v6, v11, s33
	v_mul_f32_e32 v6, v6, v11
	v_exp_f32_e32 v6, v6
	v_fma_f32 v9, -v9, v14, s33
	v_mul_f32_e32 v10, 0x3dd2d3e8, v15
	v_mul_f32_e32 v9, v9, v14
	v_add_f32_e32 v6, 1.0, v6
	v_rcp_f32_e32 v6, v6
	v_fma_f32 v10, -v10, v15, s33
	v_mul_f32_e32 v8, v8, v13
	v_exp_f32_e32 v9, v9
	v_mul_f32_e32 v6, v6, v11
	v_mul_f32_e32 v11, 0x3dd2d3e8, v16
	v_mul_f32_e32 v10, v10, v15
	v_fma_f32 v11, -v11, v16, s33
	v_mul_f32_e32 v13, 0x3dd2d3e8, v17
	v_exp_f32_e32 v10, v10
	v_mul_f32_e32 v11, v11, v16
	v_fma_f32 v13, -v13, v17, s33
	v_exp_f32_e32 v11, v11
	v_mul_f32_e32 v13, v13, v17
	v_exp_f32_e32 v13, v13
	v_add_f32_e32 v9, 1.0, v9
	v_rcp_f32_e32 v9, v9
	v_add_f32_e32 v10, 1.0, v10
	v_mul_f32_e32 v18, v7, v7
	v_rcp_f32_e32 v10, v10
	v_add_f32_e32 v11, 1.0, v11
	v_fmac_f32_e32 v18, v12, v12
	v_rcp_f32_e32 v11, v11
	v_add_f32_e32 v13, 1.0, v13
	v_fmac_f32_e32 v18, v6, v6
	v_rcp_f32_e32 v13, v13
	v_fmac_f32_e32 v18, v8, v8
	v_mul_f32_e32 v9, v9, v14
	v_fmac_f32_e32 v18, v9, v9
	v_mul_f32_e32 v10, v10, v15
	v_fmac_f32_e32 v18, v10, v10
	v_mul_f32_e32 v11, v11, v16
	v_fmac_f32_e32 v18, v11, v11
	v_mul_f32_e32 v13, v13, v17
	v_fmac_f32_e32 v18, v13, v13
	v_mov_b32_e32 v14, v18
	s_nop 1
	v_permlane32_swap_b32_e32 v14, v18
	s_waitcnt lgkmcnt(0)
	v_add_f32_e32 v14, v18, v14
	v_mov_b32_e32 v15, v14
	s_nop 1
	v_permlane16_swap_b32_e32 v15, v14
	s_waitcnt lgkmcnt(0)
	v_add_f32_e32 v14, v14, v15
	s_nop 1
	v_mov_b32_dpp v15, v14 row_ror:8 row_mask:0xf bank_mask:0xf
	s_waitcnt lgkmcnt(0)
	v_add_f32_e32 v14, v14, v15
	s_nop 1
	v_mov_b32_dpp v15, v14 row_shl:4 row_mask:0xf bank_mask:0x5
	v_mov_b32_dpp v15, v14 row_shr:4 row_mask:0xf bank_mask:0xa
	s_waitcnt lgkmcnt(0)
	v_add_f32_e32 v14, v14, v15
	s_nop 1
	v_mov_b32_dpp v15, v14 quad_perm:[2,3,0,1] row_mask:0xf bank_mask:0xf
	s_waitcnt lgkmcnt(0)
	v_add_f32_e32 v14, v14, v15
	s_nop 1
	v_mov_b32_dpp v15, v14 quad_perm:[1,0,3,2] row_mask:0xf bank_mask:0xf
	s_and_saveexec_b64 s[0:1], vcc
	s_cbranch_execz .LBB0_507
	s_waitcnt lgkmcnt(0)
	v_add_f32_e32 v14, v14, v15
	v_fmamk_f32 v14, v14, 0x3b000000, v246
	s_mov_b32 s2, 0x800000
	v_cmp_gt_f32_e64 s[2:3], s2, v14
	v_mul_f32_e32 v15, 0x4b800000, v14
	s_nop 0
	v_cndmask_b32_e64 v14, v14, v15, s[2:3]
	v_rsq_f32_e32 v14, v14
	s_nop 0
	v_mul_f32_e32 v15, 0x45800000, v14
	v_cndmask_b32_e64 v22, v14, v15, s[2:3]
	v_mul_f32_e32 v6, v6, v22
	v_mul_f32_e32 v12, v12, v22
	v_mul_f32_e32 v7, v7, v22
	v_mul_f32_e32 v6, v6, v162
	v_cvt_pk_bf16_f32 v6, v6, s0
	ds_write_b16 v67, v6 offset:35388
	v_mul_f32_e32 v6, v8, v22
	v_mul_f32_e32 v6, v6, v163
	v_cvt_pk_bf16_f32 v6, v6, s0
	ds_write_b16 v67, v6 offset:35660
	v_mul_f32_e32 v6, v9, v22
	v_mul_f32_e32 v6, v6, v164
	v_cvt_pk_bf16_f32 v6, v6, s0
	ds_write_b16 v67, v6 offset:35932
	v_mul_f32_e32 v6, v10, v22
	v_mul_f32_e32 v6, v6, v165
	v_cvt_pk_bf16_f32 v6, v6, s0
	ds_write_b16 v67, v6 offset:36204
	v_mul_f32_e32 v6, v11, v22
	v_mul_f32_e32 v6, v6, v166
	v_cvt_pk_bf16_f32 v6, v6, s0
	ds_write_b16 v67, v6 offset:36476
	v_mul_f32_e32 v6, v13, v22
	v_mul_f32_e32 v12, v12, v160
	v_mul_f32_e32 v7, v7, v161
	v_mul_f32_e32 v6, v6, v167
	v_cvt_pk_bf16_f32 v12, v12, s0
	v_cvt_pk_bf16_f32 v7, v7, s0
	v_cvt_pk_bf16_f32 v6, v6, s0
	ds_write_b16 v67, v12 offset:34844
	ds_write_b16 v67, v7 offset:35116
	ds_write_b16 v67, v6 offset:36748
; __device__ __forceinline__ float bflo(unsigned w) { return __uint_as_float(w << 16); }
; __device__ __forceinline__ float bfhi(unsigned w) { return __uint_as_float(w & 0xffff0000u); }
; __device__ __forceinline__ unsigned short f2bf(float f) { return (unsigned short)(cvt_pk_bf16(f, 0.f) & 0xffffu); }
; __device__ __forceinline__ void sgu_unit(const Params& p, int l, int un, LAS unsigned char* lds) {
;     ...
;     for (int qi = 0; qi < 16; ++qi) { const int q = wave * 16 + qi;
;         const u32x4 v = vv[qi]; float f[8] = {bflo(v.x), bfhi(v.x), bflo(v.y), bfhi(v.y), bflo(v.z), bfhi(v.z), bflo(v.w), bfhi(v.w)}; float ss = 0.f;
; #pragma unroll
;         for (int j = 0; j < 8; ++j) { f[j] = gelu_tanh(f[j]); ss += f[j] * f[j]; }
;         ss = wave_sum(ss); const float rinv = rsqrtf(ss * (1.0f / 512.0f) + EPS);
;         if ((lane >> 4) == h) { const int c0 = (lane & 15) * 8; const float* g = p.in[I_SGUNG] + l * 512 + h * 128 + c0;
; #pragma unroll
;             for (int j = 0; j < 8; ++j) Vl[(c0 + j) * 136 + q] = f2bf(f[j] * rinv * g[j]); } }
.LBB0_507:
	s_or_b64 exec, exec, s[0:1]
	s_waitcnt vmcnt(0)
	v_lshlrev_b32_e32 v6, 16, v2
	v_lshlrev_b32_e32 v7, 16, v3
	v_and_b32_e32 v9, 0xffff0000, v3
	v_mul_f32_e32 v3, 0x3dd2d3e8, v6
	v_fma_f32 v3, -v3, v6, s33
	v_mul_f32_e32 v3, v3, v6
	v_exp_f32_e32 v3, v3
	v_and_b32_e32 v2, 0xffff0000, v2
	v_lshlrev_b32_e32 v10, 16, v4
	v_and_b32_e32 v11, 0xffff0000, v4
	v_add_f32_e32 v3, 1.0, v3
	v_rcp_f32_e32 v3, v3
	v_mul_f32_e32 v4, 0x3dd2d3e8, v9
	v_fma_f32 v4, -v4, v9, s33
	v_mul_f32_e32 v4, v4, v9
	v_mul_f32_e32 v8, v3, v6
	v_mul_f32_e32 v3, 0x3dd2d3e8, v2
	v_fma_f32 v3, -v3, v2, s33
	v_mul_f32_e32 v3, v3, v2
	v_exp_f32_e32 v3, v3
	v_exp_f32_e32 v4, v4
	v_lshlrev_b32_e32 v12, 16, v5
	v_and_b32_e32 v13, 0xffff0000, v5
	v_add_f32_e32 v3, 1.0, v3
	v_rcp_f32_e32 v3, v3
	v_add_f32_e32 v4, 1.0, v4
	v_rcp_f32_e32 v4, v4
	v_mul_f32_e32 v5, 0x3dd2d3e8, v10
	v_mul_f32_e32 v3, v3, v2
	v_mul_f32_e32 v2, 0x3dd2d3e8, v7
	v_fma_f32 v2, -v2, v7, s33
	v_mul_f32_e32 v2, v2, v7
	v_exp_f32_e32 v2, v2
	v_fma_f32 v5, -v5, v10, s33
	v_mul_f32_e32 v6, 0x3dd2d3e8, v11
	v_mul_f32_e32 v5, v5, v10
	v_add_f32_e32 v2, 1.0, v2
	v_rcp_f32_e32 v2, v2
	v_fma_f32 v6, -v6, v11, s33
	v_mul_f32_e32 v4, v4, v9
	v_exp_f32_e32 v5, v5
	v_mul_f32_e32 v2, v2, v7
	v_mul_f32_e32 v7, 0x3dd2d3e8, v12
	v_mul_f32_e32 v6, v6, v11
	v_fma_f32 v7, -v7, v12, s33
	v_mul_f32_e32 v9, 0x3dd2d3e8, v13
	v_exp_f32_e32 v6, v6
	v_mul_f32_e32 v7, v7, v12
	v_fma_f32 v9, -v9, v13, s33
	v_exp_f32_e32 v7, v7
	v_mul_f32_e32 v9, v9, v13
	v_exp_f32_e32 v9, v9
	v_add_f32_e32 v5, 1.0, v5
	v_rcp_f32_e32 v5, v5
	v_add_f32_e32 v6, 1.0, v6
	v_mul_f32_e32 v14, v3, v3
	v_rcp_f32_e32 v6, v6
	v_add_f32_e32 v7, 1.0, v7
	v_fmac_f32_e32 v14, v8, v8
	v_rcp_f32_e32 v7, v7
	v_add_f32_e32 v9, 1.0, v9
	v_fmac_f32_e32 v14, v2, v2
	v_rcp_f32_e32 v9, v9
	v_fmac_f32_e32 v14, v4, v4
	v_mul_f32_e32 v5, v5, v10
	v_fmac_f32_e32 v14, v5, v5
	v_mul_f32_e32 v6, v6, v11
	v_fmac_f32_e32 v14, v6, v6
	v_mul_f32_e32 v7, v7, v12
	v_fmac_f32_e32 v14, v7, v7
	v_mul_f32_e32 v9, v9, v13
	v_fmac_f32_e32 v14, v9, v9
	v_mov_b32_e32 v10, v14
	s_nop 1
	v_permlane32_swap_b32_e32 v10, v14
	s_waitcnt lgkmcnt(0)
	v_add_f32_e32 v10, v14, v10
	v_mov_b32_e32 v11, v10
	s_nop 1
	v_permlane16_swap_b32_e32 v11, v10
	s_waitcnt lgkmcnt(0)
	v_add_f32_e32 v10, v10, v11
	s_nop 1
	v_mov_b32_dpp v11, v10 row_ror:8 row_mask:0xf bank_mask:0xf
	s_waitcnt lgkmcnt(0)
	v_add_f32_e32 v10, v10, v11
	s_nop 1
	v_mov_b32_dpp v11, v10 row_shl:4 row_mask:0xf bank_mask:0x5
	v_mov_b32_dpp v11, v10 row_shr:4 row_mask:0xf bank_mask:0xa
	s_waitcnt lgkmcnt(0)
	v_add_f32_e32 v10, v10, v11
	s_nop 1
	v_mov_b32_dpp v11, v10 quad_perm:[2,3,0,1] row_mask:0xf bank_mask:0xf
	s_waitcnt lgkmcnt(0)
	v_add_f32_e32 v10, v10, v11
	s_nop 1
	v_mov_b32_dpp v11, v10 quad_perm:[1,0,3,2] row_mask:0xf bank_mask:0xf
	s_and_saveexec_b64 s[0:1], vcc
	s_cbranch_execz .LBB0_509
	s_waitcnt lgkmcnt(0)
	v_add_f32_e32 v10, v10, v11
	v_fmamk_f32 v10, v10, 0x3b000000, v246
	s_mov_b32 s2, 0x800000
	v_cmp_gt_f32_e32 vcc, s2, v10
	v_mul_f32_e32 v11, 0x4b800000, v10
	s_nop 0
	v_cndmask_b32_e32 v10, v10, v11, vcc
	v_rsq_f32_e32 v10, v10
	s_nop 0
	v_mul_f32_e32 v11, 0x45800000, v10
	v_cndmask_b32_e32 v18, v10, v11, vcc
	v_mul_f32_e32 v2, v2, v18
	v_mul_f32_e32 v8, v8, v18
	v_mul_f32_e32 v3, v3, v18
	v_mul_f32_e32 v2, v2, v162
	v_cvt_pk_bf16_f32 v2, v2, s0
	ds_write_b16 v67, v2 offset:35390
	v_mul_f32_e32 v2, v4, v18
	v_mul_f32_e32 v2, v2, v163
	v_cvt_pk_bf16_f32 v2, v2, s0
	ds_write_b16 v67, v2 offset:35662
	v_mul_f32_e32 v2, v5, v18
	v_mul_f32_e32 v2, v2, v164
	v_cvt_pk_bf16_f32 v2, v2, s0
	ds_write_b16 v67, v2 offset:35934
	v_mul_f32_e32 v2, v6, v18
	v_mul_f32_e32 v2, v2, v165
	v_cvt_pk_bf16_f32 v2, v2, s0
	ds_write_b16 v67, v2 offset:36206
	v_mul_f32_e32 v2, v7, v18
	v_mul_f32_e32 v2, v2, v166
	v_cvt_pk_bf16_f32 v2, v2, s0
	ds_write_b16 v67, v2 offset:36478
	v_mul_f32_e32 v2, v9, v18
	v_mul_f32_e32 v8, v8, v160
	v_mul_f32_e32 v3, v3, v161
	v_mul_f32_e32 v2, v2, v167
	v_cvt_pk_bf16_f32 v8, v8, s0
	v_cvt_pk_bf16_f32 v3, v3, s0
	v_cvt_pk_bf16_f32 v2, v2, s0
	ds_write_b16 v67, v8 offset:34846
	ds_write_b16 v67, v3 offset:35118
	ds_write_b16 v67, v2 offset:36750

;     __device__ __forceinline__ void init(const void* A_, const void* B_, int G_, int c_) { T.init(A_, B_, DM, DM, NLAT / 256, INP / 256, 1, 0, 0, G_, c_, 0); }
; __device__ __forceinline__ void sgu_unit(const Params& p, int l, int un, LAS unsigned char* lds) {
;     ...
;     const float* Wg = p.in[I_SGUW] + ((size_t)l * 4 + h) * 128 * 128;
;     f32x4 wq[8]; u32x4 vv[16];
; #pragma unroll
;     for (int i = 0; i < 8; ++i) wq[i] = *(const f32x4*)(Wg + (i * 512 + tid) * 4);
; #pragma unroll
;     for (int qi = 0; qi < 16; ++qi) vv[qi] = *(const u32x4*)(P + (size_t)(row0 + wave * 16 + qi) * INP + C_SGU_V + lane * 8);
; __global__ void __launch_bounds__(512, 2) fwd(Params p) {
;     ...
;             { pg8::TileSched S; S.init(ws + WS_UPK, (bf16_t*)(ws + WS_G2B) + (size_t)l * 32 * 256 * 512, 512, 512, 3, 1, 32, (size_t)768 * 512 * 2, (size_t)256 * 512 * 2, G, c, (l == 0 && G == 256) ? 32 : 0);
;               pg8::EpiS2 E{(bf16_t*)(ws + WS_GB)};
;               pg8::Unit u0; if (S.next(0, u0)) { carry_wait(p, l); pg8::gemm_phase(lds, pg8::Desc{512, 512, 512}, S, E); }
;               else if (G == 256) { const int un = c - (l == 0 ? 128 : 96); if (un >= 0) sgu_unit(p, l, un, lds); } }
.LBB0_1258:
	v_readlane_b32 s0, v251, 50
	v_readlane_b32 s2, v252, 20
	v_readlane_b32 s1, v251, 51
	v_readlane_b32 s3, v252, 21
	s_and_b64 s[0:1], s[0:1], s[2:3]
	s_and_b64 s[0:1], s[0:1], exec
	s_cselect_b32 s0, 32, 0
	v_readlane_b32 s2, v255, 11
	s_mul_hi_u32 s1, s0, s2
	v_readlane_b32 s3, v255, 12
	s_mul_i32 s1, s1, s3
	s_sub_i32 s0, s0, s1
	s_sub_i32 s1, s0, s3
	s_cmp_ge_u32 s0, s3
	s_cselect_b32 s0, s1, s0
	s_sub_i32 s1, s0, s3
	s_cmp_ge_u32 s0, s3
	s_cselect_b32 s0, s1, s0
	v_readlane_b32 s1, v255, 42
	s_sub_i32 s0, s1, s0
	s_ashr_i32 s1, s0, 31
	s_abs_i32 s0, s0
	s_mul_hi_u32 s2, s0, s2
	s_mul_i32 s2, s2, s3
	s_sub_i32 s0, s0, s2
	s_sub_i32 s2, s0, s3
	s_cmp_ge_u32 s0, s3
	s_cselect_b32 s0, s2, s0
	s_sub_i32 s2, s0, s3
	s_cmp_ge_u32 s0, s3
	s_cselect_b32 s0, s2, s0
	s_xor_b32 s0, s0, s1
	s_sub_i32 s26, s0, s1
	s_cmpk_gt_i32 s26, 0x5f
	s_mov_b64 s[0:1], -1
	s_barrier
	s_cbranch_scc0 .LBB0_1294
	v_readlane_b32 s0, v252, 20
	v_readlane_b32 s1, v252, 21
	s_and_b64 s[0:1], s[0:1], exec
	s_movk_i32 s0, 0xff80
	s_cselect_b32 s0, s0, 0xffffffa0
	s_add_i32 s0, s0, s92
	v_readlane_b32 s12, v251, 50
	s_cmp_lt_i32 s0, 0
	v_readlane_b32 s13, v251, 51
	s_cselect_b64 s[2:3], -1, 0
	s_xor_b64 s[12:13], s[12:13], -1
	s_or_b64 s[2:3], s[2:3], s[12:13]
	s_and_b64 vcc, exec, s[2:3]
	s_cbranch_vccnz .LBB0_1293
	v_readlane_b32 s2, v252, 5
	v_readlane_b32 s44, v251, 16
	s_lshl_b32 s1, s0, 5
	s_lshl_b32 s0, s2, 9
	v_readlane_b32 s2, v253, 39
	v_readlane_b32 s48, v251, 20
	v_readlane_b32 s49, v251, 21
	v_readlane_b32 s3, v252, 6
	s_or_b32 s40, s0, s2
	s_mov_b32 s41, s5
	v_readlane_b32 s50, v251, 22
	v_readlane_b32 s51, v251, 23
	v_readlane_b32 s52, v251, 24
	v_readlane_b32 s53, v251, 25
	v_readlane_b32 s54, v251, 26
	v_readlane_b32 s55, v251, 27
	s_mov_b64 s[12:13], s[48:49]
	s_lshl_b64 s[2:3], s[40:41], 9
	s_mov_b64 s[14:15], s[50:51]
	v_mov_b32_e32 v64, v0
	s_add_u32 s2, s14, s2
	s_addc_u32 s3, s15, s3
	v_lshlrev_b32_e32 v2, 2, v64
	v_ashrrev_i32_e32 v3, 31, v2
	v_add_u32_e32 v62, 0x800, v2
	s_mov_b64 s[14:15], 0
	v_lshl_add_u64 v[4:5], v[2:3], 2, s[2:3]
	v_ashrrev_i32_e32 v63, 31, v62
	v_lshl_add_u64 v[6:7], v[62:63], 2, s[2:3]
	global_load_dwordx4 v[66:69], v[4:5], off
	global_load_dwordx4 v[70:73], v[6:7], off
	v_add_u32_e32 v102, 0x1000, v2
	v_ashrrev_i32_e32 v103, 31, v102
	v_add_u32_e32 v104, 0x1800, v2
	v_lshl_add_u64 v[4:5], v[102:103], 2, s[2:3]
	v_ashrrev_i32_e32 v105, 31, v104
	s_and_b32 s12, s1, 0x7fffff80
	s_mov_b32 s1, s5
	v_lshl_add_u64 v[6:7], v[104:105], 2, s[2:3]
	global_load_dwordx4 v[74:77], v[4:5], off
	global_load_dwordx4 v[78:81], v[6:7], off
	s_lshl_b64 s[0:1], s[0:1], 2
	v_readlane_b32 s13, v253, 41
	v_add_u32_e32 v106, 0x2000, v2
	s_add_u32 s0, s13, s0
	v_readlane_b32 s13, v253, 42
	v_ashrrev_i32_e32 v107, 31, v106
	v_add_u32_e32 v108, 0x2800, v2
	s_addc_u32 s1, s13, s1
	v_lshl_add_u64 v[4:5], v[106:107], 2, s[2:3]
	v_ashrrev_i32_e32 v109, 31, v108
	s_add_u32 s36, s84, s14
	v_lshl_add_u64 v[6:7], v[108:109], 2, s[2:3]
	global_load_dwordx4 v[82:85], v[4:5], off
	global_load_dwordx4 v[86:89], v[6:7], off
	s_addc_u32 s37, s85, s15
	v_add_u32_e32 v110, 0x3000, v2
	v_add_u32_e32 v112, 0x3800, v2
	s_add_u32 s38, s36, 0x1f1b8000
	v_ashrrev_i32_e32 v111, 31, v110
	v_ashrrev_i32_e32 v113, 31, v112
	v_ashrrev_i32_e32 v103, 6, v64
	s_addc_u32 s39, s37, 0
	v_lshl_add_u64 v[4:5], v[110:111], 2, s[2:3]
	v_lshl_add_u64 v[2:3], v[112:113], 2, s[2:3]
	v_lshlrev_b32_e32 v65, 4, v103
	v_and_b32_e32 v8, 63, v64
	global_load_dwordx4 v[90:93], v[4:5], off
	global_load_dwordx4 v[94:97], v[2:3], off
	v_add_u32_e32 v9, s12, v65
	v_mov_b64_e32 v[2:3], s[38:39]
	s_movk_i32 s13, 0x1e00
	v_mad_i64_i32 v[4:5], s[2:3], v9, s13, v[2:3]
	v_lshlrev_b32_e32 v206, 4, v8
	v_or_b32_e32 v6, 1, v9
	v_lshl_add_u64 v[4:5], v[4:5], 0, v[206:207]
	v_mad_i64_i32 v[6:7], s[2:3], v6, s13, v[2:3]
	v_lshl_add_u64 v[6:7], v[6:7], 0, v[206:207]
	global_load_dwordx4 v[98:101], v[4:5], off offset:1024
	global_load_dwordx4 v[58:61], v[6:7], off offset:1024
	v_or_b32_e32 v4, 2, v9
	v_or_b32_e32 v6, 3, v9
	v_mad_i64_i32 v[4:5], s[2:3], v4, s13, v[2:3]
	v_mad_i64_i32 v[6:7], s[2:3], v6, s13, v[2:3]
	v_lshl_add_u64 v[4:5], v[4:5], 0, v[206:207]
	v_lshl_add_u64 v[6:7], v[6:7], 0, v[206:207]
	global_load_dwordx4 v[54:57], v[4:5], off offset:1024
	global_load_dwordx4 v[50:53], v[6:7], off offset:1024
	v_or_b32_e32 v4, 4, v9
	v_or_b32_e32 v6, 5, v9
	v_mad_i64_i32 v[4:5], s[2:3], v4, s13, v[2:3]
	v_mad_i64_i32 v[6:7], s[2:3], v6, s13, v[2:3]
	v_lshl_add_u64 v[4:5], v[4:5], 0, v[206:207]
	v_lshl_add_u64 v[6:7], v[6:7], 0, v[206:207]
	global_load_dwordx4 v[46:49], v[4:5], off offset:1024
	global_load_dwordx4 v[42:45], v[6:7], off offset:1024
	v_or_b32_e32 v4, 6, v9
	v_or_b32_e32 v6, 7, v9
	v_mad_i64_i32 v[4:5], s[2:3], v4, s13, v[2:3]
	v_mad_i64_i32 v[6:7], s[2:3], v6, s13, v[2:3]
	v_lshl_add_u64 v[4:5], v[4:5], 0, v[206:207]
	v_lshl_add_u64 v[6:7], v[6:7], 0, v[206:207]
	global_load_dwordx4 v[38:41], v[4:5], off offset:1024
	global_load_dwordx4 v[34:37], v[6:7], off offset:1024
	v_or_b32_e32 v4, 8, v9
	v_or_b32_e32 v6, 9, v9
	v_mad_i64_i32 v[4:5], s[2:3], v4, s13, v[2:3]
	v_mad_i64_i32 v[6:7], s[2:3], v6, s13, v[2:3]
	v_lshl_add_u64 v[4:5], v[4:5], 0, v[206:207]
	v_lshl_add_u64 v[6:7], v[6:7], 0, v[206:207]
	global_load_dwordx4 v[30:33], v[4:5], off offset:1024
	global_load_dwordx4 v[26:29], v[6:7], off offset:1024
	v_or_b32_e32 v4, 10, v9
	v_or_b32_e32 v6, 11, v9
	v_mad_i64_i32 v[4:5], s[2:3], v4, s13, v[2:3]
	v_mad_i64_i32 v[6:7], s[2:3], v6, s13, v[2:3]
	v_lshl_add_u64 v[4:5], v[4:5], 0, v[206:207]
	v_lshl_add_u64 v[6:7], v[6:7], 0, v[206:207]
	global_load_dwordx4 v[22:25], v[4:5], off offset:1024
	global_load_dwordx4 v[18:21], v[6:7], off offset:1024
	v_or_b32_e32 v4, 12, v9
	v_or_b32_e32 v6, 13, v9
	v_mad_i64_i32 v[4:5], s[2:3], v4, s13, v[2:3]
	v_mad_i64_i32 v[6:7], s[2:3], v6, s13, v[2:3]
	v_lshl_add_u64 v[4:5], v[4:5], 0, v[206:207]
	v_lshl_add_u64 v[6:7], v[6:7], 0, v[206:207]
	v_lshlrev_b32_e32 v105, 3, v64
	global_load_dwordx4 v[14:17], v[4:5], off offset:1024
	global_load_dwordx4 v[10:13], v[6:7], off offset:1024
	v_or_b32_e32 v4, 14, v9
	v_or_b32_e32 v6, 15, v9
	v_and_b32_e32 v63, 0xf8, v105
	v_mad_i64_i32 v[4:5], s[2:3], v4, s13, v[2:3]
	v_mad_i64_i32 v[2:3], s[2:3], v6, s13, v[2:3]
	v_add_u32_e32 v114, 0, v63
	v_bfe_i32 v63, v64, 5, 25
	s_movk_i32 s13, 0x110
	v_lshl_add_u64 v[4:5], v[4:5], 0, v[206:207]
	v_lshl_add_u64 v[2:3], v[2:3], 0, v[206:207]
	s_waitcnt vmcnt(21)
; #define LAS __attribute__((address_space(3)))
; __device__ __forceinline__ unsigned cvt_pk_bf16(float lo, float hi) { const f32x2 v = {lo, hi}; const bf16x2_t b = __builtin_convertvector(v, bf16x2_t); return __builtin_bit_cast(unsigned, b); }
; __device__ __forceinline__ float bflo(unsigned w) { return __uint_as_float(w << 16); }
; __device__ __forceinline__ float bfhi(unsigned w) { return __uint_as_float(w & 0xffff0000u); }
; __device__ __forceinline__ void sgu_unit(const Params& p, int l, int un, LAS unsigned char* lds) {
;     ...
;     for (int i = 0; i < 8; ++i) { const int e4 = (i * 512 + tid) * 4, r = e4 >> 7, c = e4 & 127; const f32x4 v = wq[i];
;         u32x2 w; w.x = cvt_pk_bf16(v[0], v[1]); w.y = cvt_pk_bf16(v[2], v[3]); *(LAS u32x2*)(Wl + r * 136 + c) = w; }
; #pragma unroll
;     for (int qi = 0; qi < 16; ++qi) { const int q = wave * 16 + qi;
;         const u32x4 v = vv[qi]; float f[8] = {bflo(v.x), bfhi(v.x), bflo(v.y), bfhi(v.y), bflo(v.z), bfhi(v.z), bflo(v.w), bfhi(v.w)}; float ss = 0.f;
; #pragma unroll
;         for (int j = 0; j < 8; ++j) { f[j] = gelu_tanh(f[j]); ss += f[j] * f[j]; }
;         ss = wave_sum(ss); const float rinv = rsqrtf(ss * (1.0f / 512.0f) + EPS);
	v_cvt_pk_bf16_f32 v66, v66, v67
	v_cvt_pk_bf16_f32 v67, v68, v69
	v_mad_u64_u32 v[68:69], s[2:3], v63, s13, v[114:115]
	global_load_dwordx4 v[6:9], v[4:5], off offset:1024
	s_nop 0
	global_load_dwordx4 v[2:5], v[2:3], off offset:1024
	ds_write_b64 v68, v[66:67]
	v_ashrrev_i32_e32 v66, 7, v62
	s_waitcnt vmcnt(22)
	v_cvt_pk_bf16_f32 v62, v70, v71
	v_cvt_pk_bf16_f32 v63, v72, v73
	v_mad_u64_u32 v[66:67], s[2:3], v66, s13, v[114:115]
	ds_write_b64 v66, v[62:63]
	v_ashrrev_i32_e32 v66, 7, v102
	s_waitcnt vmcnt(21)
	v_cvt_pk_bf16_f32 v62, v74, v75
	v_cvt_pk_bf16_f32 v63, v76, v77
	v_mad_u64_u32 v[66:67], s[2:3], v66, s13, v[114:115]
	ds_write_b64 v66, v[62:63]
	v_ashrrev_i32_e32 v66, 7, v104
	s_waitcnt vmcnt(20)
	v_cvt_pk_bf16_f32 v62, v78, v79
	v_cvt_pk_bf16_f32 v63, v80, v81
	v_mad_u64_u32 v[66:67], s[2:3], v66, s13, v[114:115]
	ds_write_b64 v66, v[62:63]
	v_ashrrev_i32_e32 v66, 7, v106
	s_waitcnt vmcnt(19)
	v_cvt_pk_bf16_f32 v62, v82, v83
	v_cvt_pk_bf16_f32 v63, v84, v85
	v_mad_u64_u32 v[66:67], s[2:3], v66, s13, v[114:115]
	ds_write_b64 v66, v[62:63]
	v_ashrrev_i32_e32 v66, 7, v108
	s_waitcnt vmcnt(18)
	v_cvt_pk_bf16_f32 v62, v86, v87
	v_cvt_pk_bf16_f32 v63, v88, v89
	v_mad_u64_u32 v[66:67], s[2:3], v66, s13, v[114:115]
	ds_write_b64 v66, v[62:63]
	v_ashrrev_i32_e32 v66, 7, v110
	s_waitcnt vmcnt(17)
	v_cvt_pk_bf16_f32 v62, v90, v91
	v_cvt_pk_bf16_f32 v63, v92, v93
	v_mad_u64_u32 v[66:67], s[2:3], v66, s13, v[114:115]
	ds_write_b64 v66, v[62:63]
	v_ashrrev_i32_e32 v66, 7, v112
	v_mad_u64_u32 v[66:67], s[2:3], v66, s13, v[114:115]
	s_waitcnt vmcnt(15)
	v_and_b32_e32 v67, 0xffff0000, v98
	v_mul_f32_e32 v73, 0x3dd2d3e8, v67
	v_fma_f32 v73, -v73, v67, s33
	v_mul_f32_e32 v73, v73, v67
	v_exp_f32_e32 v73, v73
	v_cvt_pk_bf16_f32 v62, v94, v95
	v_cvt_pk_bf16_f32 v63, v96, v97
	ds_write_b64 v66, v[62:63]
	v_lshlrev_b32_e32 v66, 16, v98
	v_add_f32_e32 v73, 1.0, v73
	v_mul_f32_e32 v72, 0x3dd2d3e8, v66
	v_rcp_f32_e32 v73, v73
	v_fma_f32 v72, -v72, v66, s33
	v_mul_f32_e32 v72, v72, v66
	v_lshlrev_b32_e32 v69, 16, v99
	v_exp_f32_e32 v72, v72
	v_mul_f32_e32 v79, v73, v67
	v_mul_f32_e32 v67, 0x3dd2d3e8, v69
	v_fma_f32 v67, -v67, v69, s33
	v_mul_f32_e32 v67, v67, v69
	v_add_f32_e32 v72, 1.0, v72
	v_exp_f32_e32 v67, v67
	v_rcp_f32_e32 v72, v72
	v_lshlrev_b32_e32 v71, 16, v100
	v_and_b32_e32 v70, 0xffff0000, v99
	v_add_f32_e32 v67, 1.0, v67
	v_mul_f32_e32 v73, 0x3dd2d3e8, v71
	v_mul_f32_e32 v81, v72, v66
	v_mul_f32_e32 v72, 0x3dd2d3e8, v70
	v_rcp_f32_e32 v67, v67
	v_fma_f32 v73, -v73, v71, s33
	v_fma_f32 v72, -v72, v70, s33
	v_mul_f32_e32 v73, v73, v71
	v_mul_f32_e32 v72, v72, v70
	v_exp_f32_e32 v73, v73
	v_and_b32_e32 v74, 0xffff0000, v100
	v_exp_f32_e32 v72, v72
	v_mul_f32_e32 v80, v67, v69
	v_mul_f32_e32 v69, 0x3dd2d3e8, v74
	v_fma_f32 v69, -v69, v74, s33
	v_add_f32_e32 v67, 1.0, v73
	v_mul_f32_e32 v69, v69, v74
	v_add_f32_e32 v72, 1.0, v72
	v_rcp_f32_e32 v67, v67
	v_exp_f32_e32 v69, v69
	v_rcp_f32_e32 v72, v72
	v_lshlrev_b32_e32 v75, 16, v101
	v_and_b32_e32 v82, 0xffff0000, v101
	v_mul_f32_e32 v76, v67, v71
	v_add_f32_e32 v67, 1.0, v69
	v_mul_f32_e32 v69, 0x3dd2d3e8, v75
	v_mul_f32_e32 v78, v72, v70
	v_fma_f32 v69, -v69, v75, s33
	v_mul_f32_e32 v70, 0x3dd2d3e8, v82
	v_mul_f32_e32 v69, v69, v75
	v_fma_f32 v70, -v70, v82, s33
	v_rcp_f32_e32 v67, v67
	v_exp_f32_e32 v69, v69
	v_mul_f32_e32 v70, v70, v82
	v_exp_f32_e32 v70, v70
	v_mul_f32_e32 v66, v79, v79
	v_mul_f32_e32 v77, v67, v74
	v_add_f32_e32 v67, 1.0, v69
	v_fmac_f32_e32 v66, v81, v81
	v_rcp_f32_e32 v67, v67
	v_add_f32_e32 v69, 1.0, v70
	v_fmac_f32_e32 v66, v80, v80
	v_rcp_f32_e32 v69, v69
	v_and_b32_e32 v62, 64, v249
	v_fmac_f32_e32 v66, v78, v78
	v_add_u32_e32 v62, 64, v62
	v_xor_b32_e32 v63, 32, v249
	v_fmac_f32_e32 v66, v76, v76
	v_cmp_lt_i32_e32 vcc, v63, v62
	v_fmac_f32_e32 v66, v77, v77
	v_mul_f32_e32 v75, v67, v75
	v_cndmask_b32_e32 v63, v249, v63, vcc
	v_fmac_f32_e32 v66, v75, v75
	v_mul_f32_e32 v74, v69, v82
	v_lshlrev_b32_e32 v68, 2, v63
	v_fmac_f32_e32 v66, v74, v74
	v_mov_b32_e32 v67, v66
	s_nop 1
	v_permlane32_swap_b32_e32 v67, v66
	v_xor_b32_e32 v63, 16, v249
	v_cmp_lt_i32_e32 vcc, v63, v62
	v_and_b32_e32 v84, 0x78, v105
	v_readlane_b32 s2, v253, 40
	v_cndmask_b32_e32 v63, v249, v63, vcc
	v_lshlrev_b32_e32 v69, 2, v63
	s_waitcnt lgkmcnt(0)
	v_add_f32_e32 v66, v66, v67
	v_mov_b32_e32 v67, v66
	s_nop 1
	v_permlane16_swap_b32_e32 v67, v66
	v_xor_b32_e32 v63, 8, v249
	v_cmp_lt_i32_e32 vcc, v63, v62
	v_lshlrev_b32_e32 v206, 2, v84
	v_readlane_b32 s45, v251, 17
	v_cndmask_b32_e32 v63, v249, v63, vcc
	v_lshlrev_b32_e32 v70, 2, v63
	s_waitcnt lgkmcnt(0)
	v_add_f32_e32 v66, v66, v67
	s_nop 1
	v_mov_b32_dpp v67, v66 row_ror:8 row_mask:0xf bank_mask:0xf
	v_xor_b32_e32 v63, 4, v249
	v_cmp_lt_i32_e32 vcc, v63, v62
	v_readlane_b32 s46, v251, 18
	v_readlane_b32 s47, v251, 19
	v_cndmask_b32_e32 v63, v249, v63, vcc
	v_lshlrev_b32_e32 v71, 2, v63
	s_waitcnt lgkmcnt(0)
	v_add_f32_e32 v66, v66, v67
	v_xor_b32_e32 v63, 2, v249
	s_nop 1
	v_mov_b32_dpp v67, v66 row_shl:4 row_mask:0xf bank_mask:0x5
	v_mov_b32_dpp v67, v66 row_shr:4 row_mask:0xf bank_mask:0xa
	v_cmp_lt_i32_e32 vcc, v63, v62
	v_readlane_b32 s56, v251, 28
	v_readlane_b32 s57, v251, 29
	v_cndmask_b32_e32 v63, v249, v63, vcc
	v_lshlrev_b32_e32 v72, 2, v63
	v_xor_b32_e32 v63, 1, v249
	v_cmp_lt_i32_e32 vcc, v63, v62
	v_readlane_b32 s58, v251, 30
	v_readlane_b32 s59, v251, 31
	v_cndmask_b32_e32 v62, v249, v63, vcc
	s_waitcnt lgkmcnt(0)
	v_add_f32_e32 v63, v66, v67
	s_nop 1
	v_mov_b32_dpp v67, v63 quad_perm:[2,3,0,1] row_mask:0xf bank_mask:0xf
	v_lshlrev_b32_e32 v73, 2, v62
	v_bfe_u32 v66, v64, 4, 2
	v_cmp_eq_u32_e32 vcc, s2, v66
	s_mov_b64 s[16:17], s[52:53]
	s_waitcnt lgkmcnt(0)
	v_add_f32_e32 v82, v63, v67
	s_nop 1
	v_mov_b32_dpp v83, v82 quad_perm:[1,0,3,2] row_mask:0xf bank_mask:0xf
	v_lshl_add_u32 v67, v103, 5, 0
	v_lshl_add_u64 v[62:63], s[0:1], 0, v[206:207]
	v_mad_u32_u24 v67, v84, s13, v67
	s_mov_b64 s[18:19], s[54:55]
	s_and_saveexec_b64 s[0:1], vcc
	s_cbranch_execz .LBB0_1262
; __device__ __forceinline__ float bflo(unsigned w) { return __uint_as_float(w << 16); }
; __device__ __forceinline__ float bfhi(unsigned w) { return __uint_as_float(w & 0xffff0000u); }
; __device__ __forceinline__ unsigned short f2bf(float f) { return (unsigned short)(cvt_pk_bf16(f, 0.f) & 0xffffu); }
; __device__ __forceinline__ void sgu_unit(const Params& p, int l, int un, LAS unsigned char* lds) {
;     ...
;     for (int qi = 0; qi < 16; ++qi) { const int q = wave * 16 + qi;
;         const u32x4 v = vv[qi]; float f[8] = {bflo(v.x), bfhi(v.x), bflo(v.y), bfhi(v.y), bflo(v.z), bfhi(v.z), bflo(v.w), bfhi(v.w)}; float ss = 0.f;
; #pragma unroll
;         for (int j = 0; j < 8; ++j) { f[j] = gelu_tanh(f[j]); ss += f[j] * f[j]; }
;         ss = wave_sum(ss); const float rinv = rsqrtf(ss * (1.0f / 512.0f) + EPS);
;         if ((lane >> 4) == h) { const int c0 = (lane & 15) * 8; const float* g = p.in[I_SGUNG] + l * 512 + h * 128 + c0;
; #pragma unroll
;             for (int j = 0; j < 8; ++j) Vl[(c0 + j) * 136 + q] = f2bf(f[j] * rinv * g[j]); } }
	s_waitcnt lgkmcnt(0)
	v_add_f32_e32 v82, v82, v83
	v_fmamk_f32 v82, v82, 0x3b000000, v246
	s_mov_b32 s2, 0x800000
	v_cmp_gt_f32_e64 s[2:3], s2, v82
	v_mul_f32_e32 v83, 0x4b800000, v82
	s_nop 0
	v_cndmask_b32_e64 v82, v82, v83, s[2:3]
	v_rsq_f32_e32 v82, v82
	s_nop 0
	v_mul_f32_e32 v83, 0x45800000, v82
	v_cndmask_b32_e64 v90, v82, v83, s[2:3]
	global_load_dwordx4 v[82:85], v[62:63], off offset:16
	global_load_dwordx4 v[86:89], v[62:63], off
	v_mul_f32_e32 v79, v79, v90
	v_mul_f32_e32 v76, v76, v90
	v_mul_f32_e32 v81, v81, v90
	v_mul_f32_e32 v78, v78, v90
	v_mul_f32_e32 v75, v75, v90
	v_mul_f32_e32 v74, v74, v90
	s_waitcnt vmcnt(1)
	v_mul_f32_e32 v76, v76, v82
	s_waitcnt vmcnt(0)
	v_mov_b32_e32 v160, v86
	v_mov_b32_e32 v161, v87
	v_mov_b32_e32 v162, v88
	v_mov_b32_e32 v163, v89
	v_mov_b32_e32 v164, v82
	v_mov_b32_e32 v165, v83
	v_mov_b32_e32 v166, v84
	v_mov_b32_e32 v167, v85
	v_mul_f32_e32 v79, v79, v87
	v_cvt_pk_bf16_f32 v79, v79, s0
	v_cvt_pk_bf16_f32 v76, v76, s0
	ds_write_b16 v67, v79 offset:35088
	v_mul_f32_e32 v79, v80, v90
	ds_write_b16 v67, v76 offset:35904
	v_mul_f32_e32 v76, v77, v90
	v_mul_f32_e32 v81, v81, v86
	v_mul_f32_e32 v79, v79, v88
	v_mul_f32_e32 v78, v78, v89
	v_mul_f32_e32 v76, v76, v83
	v_mul_f32_e32 v75, v75, v84
	v_mul_f32_e32 v74, v74, v85
	v_cvt_pk_bf16_f32 v81, v81, s0
	v_cvt_pk_bf16_f32 v79, v79, s0
	v_cvt_pk_bf16_f32 v78, v78, s0
	v_cvt_pk_bf16_f32 v76, v76, s0
	v_cvt_pk_bf16_f32 v75, v75, s0
	v_cvt_pk_bf16_f32 v74, v74, s0
	ds_write_b16 v67, v81 offset:34816
	ds_write_b16 v67, v79 offset:35360
	ds_write_b16 v67, v78 offset:35632
	ds_write_b16 v67, v76 offset:36176
	ds_write_b16 v67, v75 offset:36448
	ds_write_b16 v67, v74 offset:36720
.LBB0_1262:
	s_or_b64 exec, exec, s[0:1]
	s_waitcnt vmcnt(14)
	v_lshlrev_b32_e32 v74, 16, v58
	v_lshlrev_b32_e32 v75, 16, v59
	v_and_b32_e32 v77, 0xffff0000, v59
	v_mul_f32_e32 v59, 0x3dd2d3e8, v74
	v_fma_f32 v59, -v59, v74, s33
	v_mul_f32_e32 v59, v59, v74
	v_exp_f32_e32 v59, v59
	v_and_b32_e32 v58, 0xffff0000, v58
	v_lshlrev_b32_e32 v78, 16, v60
	v_and_b32_e32 v79, 0xffff0000, v60
	v_add_f32_e32 v59, 1.0, v59
	v_rcp_f32_e32 v59, v59
	v_mul_f32_e32 v60, 0x3dd2d3e8, v77
	v_fma_f32 v60, -v60, v77, s33
	v_mul_f32_e32 v60, v60, v77
	v_mul_f32_e32 v76, v59, v74
	v_mul_f32_e32 v59, 0x3dd2d3e8, v58
	v_fma_f32 v59, -v59, v58, s33
	v_mul_f32_e32 v59, v59, v58
	v_exp_f32_e32 v59, v59
	v_exp_f32_e32 v60, v60
	v_lshlrev_b32_e32 v80, 16, v61
	v_and_b32_e32 v81, 0xffff0000, v61
	v_add_f32_e32 v59, 1.0, v59
	v_rcp_f32_e32 v59, v59
	v_add_f32_e32 v60, 1.0, v60
	v_rcp_f32_e32 v60, v60
	v_mul_f32_e32 v61, 0x3dd2d3e8, v78
	v_mul_f32_e32 v59, v59, v58
	v_mul_f32_e32 v58, 0x3dd2d3e8, v75
	v_fma_f32 v58, -v58, v75, s33
	v_mul_f32_e32 v58, v58, v75
	v_exp_f32_e32 v58, v58
	v_fma_f32 v61, -v61, v78, s33
	v_mul_f32_e32 v74, 0x3dd2d3e8, v79
	v_mul_f32_e32 v61, v61, v78
	v_add_f32_e32 v58, 1.0, v58
	v_rcp_f32_e32 v58, v58
	v_fma_f32 v74, -v74, v79, s33
	v_mul_f32_e32 v60, v60, v77
	v_exp_f32_e32 v61, v61
	v_mul_f32_e32 v58, v58, v75
	v_mul_f32_e32 v75, 0x3dd2d3e8, v80
	v_mul_f32_e32 v74, v74, v79
	v_fma_f32 v75, -v75, v80, s33
	v_mul_f32_e32 v77, 0x3dd2d3e8, v81
	v_exp_f32_e32 v74, v74
	v_mul_f32_e32 v75, v75, v80
	v_fma_f32 v77, -v77, v81, s33
	v_exp_f32_e32 v75, v75
	v_mul_f32_e32 v77, v77, v81
	v_exp_f32_e32 v77, v77
	v_add_f32_e32 v61, 1.0, v61
	v_rcp_f32_e32 v61, v61
	v_add_f32_e32 v74, 1.0, v74
	v_mul_f32_e32 v82, v59, v59
	v_rcp_f32_e32 v74, v74
	v_add_f32_e32 v75, 1.0, v75
	v_fmac_f32_e32 v82, v76, v76
	v_rcp_f32_e32 v75, v75
	v_add_f32_e32 v77, 1.0, v77
	v_fmac_f32_e32 v82, v58, v58
	v_rcp_f32_e32 v77, v77
	v_fmac_f32_e32 v82, v60, v60
	v_mul_f32_e32 v61, v61, v78
	v_fmac_f32_e32 v82, v61, v61
	v_mul_f32_e32 v74, v74, v79
	v_fmac_f32_e32 v82, v74, v74
	v_mul_f32_e32 v75, v75, v80
	v_fmac_f32_e32 v82, v75, v75
	v_mul_f32_e32 v77, v77, v81
	v_fmac_f32_e32 v82, v77, v77
	ds_bpermute_b32 v78, v68, v82
	s_waitcnt lgkmcnt(0)
	v_add_f32_e32 v78, v82, v78
	v_mov_b32_e32 v79, v78
	s_nop 1
	v_permlane16_swap_b32_e32 v79, v78
	s_waitcnt lgkmcnt(0)
	v_add_f32_e32 v78, v78, v79
	s_nop 1
	v_mov_b32_dpp v79, v78 row_ror:8 row_mask:0xf bank_mask:0xf
	s_waitcnt lgkmcnt(0)
	v_add_f32_e32 v78, v78, v79
	s_nop 1
	v_mov_b32_dpp v79, v78 row_shl:4 row_mask:0xf bank_mask:0x5
	v_mov_b32_dpp v79, v78 row_shr:4 row_mask:0xf bank_mask:0xa
	s_waitcnt lgkmcnt(0)
	v_add_f32_e32 v78, v78, v79
	s_nop 1
	v_mov_b32_dpp v79, v78 quad_perm:[2,3,0,1] row_mask:0xf bank_mask:0xf
	s_waitcnt lgkmcnt(0)
	v_add_f32_e32 v78, v78, v79
	s_nop 1
	v_mov_b32_dpp v79, v78 quad_perm:[1,0,3,2] row_mask:0xf bank_mask:0xf
	s_and_saveexec_b64 s[0:1], vcc
	s_cbranch_execz .LBB0_1264
	s_waitcnt lgkmcnt(0)
	v_add_f32_e32 v78, v78, v79
	v_fmamk_f32 v78, v78, 0x3b000000, v246
	s_mov_b32 s2, 0x800000
	v_cmp_gt_f32_e64 s[2:3], s2, v78
	v_mul_f32_e32 v79, 0x4b800000, v78
	s_nop 0
	v_cndmask_b32_e64 v78, v78, v79, s[2:3]
	v_rsq_f32_e32 v78, v78
	s_nop 0
	v_mul_f32_e32 v79, 0x45800000, v78
	v_cndmask_b32_e64 v86, v78, v79, s[2:3]
	v_mul_f32_e32 v58, v58, v86
	v_mul_f32_e32 v76, v76, v86
	v_mul_f32_e32 v59, v59, v86
	v_mul_f32_e32 v58, v58, v162
	v_cvt_pk_bf16_f32 v58, v58, s0
	ds_write_b16 v67, v58 offset:35362
	v_mul_f32_e32 v58, v60, v86
	v_mul_f32_e32 v58, v58, v163
	v_cvt_pk_bf16_f32 v58, v58, s0
	ds_write_b16 v67, v58 offset:35634
	v_mul_f32_e32 v58, v61, v86
	v_mul_f32_e32 v58, v58, v164
	v_cvt_pk_bf16_f32 v58, v58, s0
	ds_write_b16 v67, v58 offset:35906
	v_mul_f32_e32 v58, v74, v86
	v_mul_f32_e32 v58, v58, v165
	v_cvt_pk_bf16_f32 v58, v58, s0
	ds_write_b16 v67, v58 offset:36178
	v_mul_f32_e32 v58, v75, v86
	v_mul_f32_e32 v58, v58, v166
	v_cvt_pk_bf16_f32 v58, v58, s0
	ds_write_b16 v67, v58 offset:36450
	v_mul_f32_e32 v58, v77, v86
	v_mul_f32_e32 v76, v76, v160
	v_mul_f32_e32 v59, v59, v161
	v_mul_f32_e32 v58, v58, v167
	v_cvt_pk_bf16_f32 v76, v76, s0
	v_cvt_pk_bf16_f32 v59, v59, s0
	v_cvt_pk_bf16_f32 v58, v58, s0
	ds_write_b16 v67, v76 offset:34818
	ds_write_b16 v67, v59 offset:35090
	ds_write_b16 v67, v58 offset:36722
; __device__ __forceinline__ float bflo(unsigned w) { return __uint_as_float(w << 16); }
; __device__ __forceinline__ float bfhi(unsigned w) { return __uint_as_float(w & 0xffff0000u); }
; __device__ __forceinline__ unsigned short f2bf(float f) { return (unsigned short)(cvt_pk_bf16(f, 0.f) & 0xffffu); }
; __device__ __forceinline__ void sgu_unit(const Params& p, int l, int un, LAS unsigned char* lds) {
;     ...
;     for (int qi = 0; qi < 16; ++qi) { const int q = wave * 16 + qi;
;         const u32x4 v = vv[qi]; float f[8] = {bflo(v.x), bfhi(v.x), bflo(v.y), bfhi(v.y), bflo(v.z), bfhi(v.z), bflo(v.w), bfhi(v.w)}; float ss = 0.f;
; #pragma unroll
;         for (int j = 0; j < 8; ++j) { f[j] = gelu_tanh(f[j]); ss += f[j] * f[j]; }
;         ss = wave_sum(ss); const float rinv = rsqrtf(ss * (1.0f / 512.0f) + EPS);
;         if ((lane >> 4) == h) { const int c0 = (lane & 15) * 8; const float* g = p.in[I_SGUNG] + l * 512 + h * 128 + c0;
; #pragma unroll
;             for (int j = 0; j < 8; ++j) Vl[(c0 + j) * 136 + q] = f2bf(f[j] * rinv * g[j]); } }
.LBB0_1264:
	s_or_b64 exec, exec, s[0:1]
	s_waitcnt vmcnt(13)
	v_lshlrev_b32_e32 v58, 16, v54
	v_lshlrev_b32_e32 v59, 16, v55
	v_and_b32_e32 v61, 0xffff0000, v55
	v_mul_f32_e32 v55, 0x3dd2d3e8, v58
	v_fma_f32 v55, -v55, v58, s33
	v_mul_f32_e32 v55, v55, v58
	v_exp_f32_e32 v55, v55
	v_and_b32_e32 v54, 0xffff0000, v54
	v_lshlrev_b32_e32 v74, 16, v56
	v_and_b32_e32 v75, 0xffff0000, v56
	v_add_f32_e32 v55, 1.0, v55
	v_rcp_f32_e32 v55, v55
	v_mul_f32_e32 v56, 0x3dd2d3e8, v61
	v_fma_f32 v56, -v56, v61, s33
	v_mul_f32_e32 v56, v56, v61
	v_mul_f32_e32 v60, v55, v58
	v_mul_f32_e32 v55, 0x3dd2d3e8, v54
	v_fma_f32 v55, -v55, v54, s33
	v_mul_f32_e32 v55, v55, v54
	v_exp_f32_e32 v55, v55
	v_exp_f32_e32 v56, v56
	v_lshlrev_b32_e32 v76, 16, v57
	v_and_b32_e32 v77, 0xffff0000, v57
	v_add_f32_e32 v55, 1.0, v55
	v_rcp_f32_e32 v55, v55
	v_add_f32_e32 v56, 1.0, v56
	v_rcp_f32_e32 v56, v56
	v_mul_f32_e32 v57, 0x3dd2d3e8, v74
	v_mul_f32_e32 v55, v55, v54
	v_mul_f32_e32 v54, 0x3dd2d3e8, v59
	v_fma_f32 v54, -v54, v59, s33
	v_mul_f32_e32 v54, v54, v59
	v_exp_f32_e32 v54, v54
	v_fma_f32 v57, -v57, v74, s33
	v_mul_f32_e32 v58, 0x3dd2d3e8, v75
	v_mul_f32_e32 v57, v57, v74
	v_add_f32_e32 v54, 1.0, v54
	v_rcp_f32_e32 v54, v54
	v_fma_f32 v58, -v58, v75, s33
	v_mul_f32_e32 v56, v56, v61
	v_exp_f32_e32 v57, v57
	v_mul_f32_e32 v54, v54, v59
	v_mul_f32_e32 v59, 0x3dd2d3e8, v76
	v_mul_f32_e32 v58, v58, v75
	v_fma_f32 v59, -v59, v76, s33
	v_mul_f32_e32 v61, 0x3dd2d3e8, v77
	v_exp_f32_e32 v58, v58
	v_mul_f32_e32 v59, v59, v76
	v_fma_f32 v61, -v61, v77, s33
	v_exp_f32_e32 v59, v59
	v_mul_f32_e32 v61, v61, v77
	v_exp_f32_e32 v61, v61
	v_add_f32_e32 v57, 1.0, v57
	v_rcp_f32_e32 v57, v57
	v_add_f32_e32 v58, 1.0, v58
	v_mul_f32_e32 v78, v55, v55
	v_rcp_f32_e32 v58, v58
	v_add_f32_e32 v59, 1.0, v59
	v_fmac_f32_e32 v78, v60, v60
	v_rcp_f32_e32 v59, v59
	v_add_f32_e32 v61, 1.0, v61
	v_fmac_f32_e32 v78, v54, v54
	v_rcp_f32_e32 v61, v61
	v_fmac_f32_e32 v78, v56, v56
	v_mul_f32_e32 v57, v57, v74
	v_fmac_f32_e32 v78, v57, v57
	v_mul_f32_e32 v58, v58, v75
	v_fmac_f32_e32 v78, v58, v58
	v_mul_f32_e32 v59, v59, v76
	v_fmac_f32_e32 v78, v59, v59
	v_mul_f32_e32 v61, v61, v77
	v_fmac_f32_e32 v78, v61, v61
	ds_bpermute_b32 v74, v68, v78
	s_waitcnt lgkmcnt(0)
	v_add_f32_e32 v74, v78, v74
	v_mov_b32_e32 v75, v74
	s_nop 1
	v_permlane16_swap_b32_e32 v75, v74
	s_waitcnt lgkmcnt(0)
	v_add_f32_e32 v74, v74, v75
	s_nop 1
	v_mov_b32_dpp v75, v74 row_ror:8 row_mask:0xf bank_mask:0xf
	s_waitcnt lgkmcnt(0)
	v_add_f32_e32 v74, v74, v75
	s_nop 1
	v_mov_b32_dpp v75, v74 row_shl:4 row_mask:0xf bank_mask:0x5
	v_mov_b32_dpp v75, v74 row_shr:4 row_mask:0xf bank_mask:0xa
	s_waitcnt lgkmcnt(0)
	v_add_f32_e32 v74, v74, v75
	s_nop 1
	v_mov_b32_dpp v75, v74 quad_perm:[2,3,0,1] row_mask:0xf bank_mask:0xf
	s_waitcnt lgkmcnt(0)
	v_add_f32_e32 v74, v74, v75
	s_nop 1
	v_mov_b32_dpp v75, v74 quad_perm:[1,0,3,2] row_mask:0xf bank_mask:0xf
	s_and_saveexec_b64 s[0:1], vcc
	s_cbranch_execz .LBB0_1266
	s_waitcnt lgkmcnt(0)
	v_add_f32_e32 v74, v74, v75
	v_fmamk_f32 v74, v74, 0x3b000000, v246
	s_mov_b32 s2, 0x800000
	v_cmp_gt_f32_e64 s[2:3], s2, v74
	v_mul_f32_e32 v75, 0x4b800000, v74
	s_nop 0
	v_cndmask_b32_e64 v74, v74, v75, s[2:3]
	v_rsq_f32_e32 v74, v74
	s_nop 0
	v_mul_f32_e32 v75, 0x45800000, v74
	v_cndmask_b32_e64 v82, v74, v75, s[2:3]
	v_mul_f32_e32 v54, v54, v82
	v_mul_f32_e32 v60, v60, v82
	v_mul_f32_e32 v55, v55, v82
	v_mul_f32_e32 v54, v54, v162
	v_cvt_pk_bf16_f32 v54, v54, s0
	ds_write_b16 v67, v54 offset:35364
	v_mul_f32_e32 v54, v56, v82
	v_mul_f32_e32 v54, v54, v163
	v_cvt_pk_bf16_f32 v54, v54, s0
	ds_write_b16 v67, v54 offset:35636
	v_mul_f32_e32 v54, v57, v82
	v_mul_f32_e32 v54, v54, v164
	v_cvt_pk_bf16_f32 v54, v54, s0
	ds_write_b16 v67, v54 offset:35908
	v_mul_f32_e32 v54, v58, v82
	v_mul_f32_e32 v54, v54, v165
	v_cvt_pk_bf16_f32 v54, v54, s0
	ds_write_b16 v67, v54 offset:36180
	v_mul_f32_e32 v54, v59, v82
	v_mul_f32_e32 v54, v54, v166
	v_cvt_pk_bf16_f32 v54, v54, s0
	ds_write_b16 v67, v54 offset:36452
	v_mul_f32_e32 v54, v61, v82
	v_mul_f32_e32 v60, v60, v160
	v_mul_f32_e32 v55, v55, v161
	v_mul_f32_e32 v54, v54, v167
	v_cvt_pk_bf16_f32 v60, v60, s0
	v_cvt_pk_bf16_f32 v55, v55, s0
	v_cvt_pk_bf16_f32 v54, v54, s0
	ds_write_b16 v67, v60 offset:34820
	ds_write_b16 v67, v55 offset:35092
	ds_write_b16 v67, v54 offset:36724
; __device__ __forceinline__ float bflo(unsigned w) { return __uint_as_float(w << 16); }
; __device__ __forceinline__ float bfhi(unsigned w) { return __uint_as_float(w & 0xffff0000u); }
; __device__ __forceinline__ unsigned short f2bf(float f) { return (unsigned short)(cvt_pk_bf16(f, 0.f) & 0xffffu); }
; __device__ __forceinline__ void sgu_unit(const Params& p, int l, int un, LAS unsigned char* lds) {
;     ...
;     for (int qi = 0; qi < 16; ++qi) { const int q = wave * 16 + qi;
;         const u32x4 v = vv[qi]; float f[8] = {bflo(v.x), bfhi(v.x), bflo(v.y), bfhi(v.y), bflo(v.z), bfhi(v.z), bflo(v.w), bfhi(v.w)}; float ss = 0.f;
; #pragma unroll
;         for (int j = 0; j < 8; ++j) { f[j] = gelu_tanh(f[j]); ss += f[j] * f[j]; }
;         ss = wave_sum(ss); const float rinv = rsqrtf(ss * (1.0f / 512.0f) + EPS);
;         if ((lane >> 4) == h) { const int c0 = (lane & 15) * 8; const float* g = p.in[I_SGUNG] + l * 512 + h * 128 + c0;
; #pragma unroll
;             for (int j = 0; j < 8; ++j) Vl[(c0 + j) * 136 + q] = f2bf(f[j] * rinv * g[j]); } }
.LBB0_1266:
	s_or_b64 exec, exec, s[0:1]
	s_waitcnt vmcnt(12)
	v_lshlrev_b32_e32 v54, 16, v50
	v_lshlrev_b32_e32 v55, 16, v51
	v_and_b32_e32 v57, 0xffff0000, v51
	v_mul_f32_e32 v51, 0x3dd2d3e8, v54
	v_fma_f32 v51, -v51, v54, s33
	v_mul_f32_e32 v51, v51, v54
	v_exp_f32_e32 v51, v51
	v_and_b32_e32 v50, 0xffff0000, v50
	v_lshlrev_b32_e32 v58, 16, v52
	v_and_b32_e32 v59, 0xffff0000, v52
	v_add_f32_e32 v51, 1.0, v51
	v_rcp_f32_e32 v51, v51
	v_mul_f32_e32 v52, 0x3dd2d3e8, v57
	v_fma_f32 v52, -v52, v57, s33
	v_mul_f32_e32 v52, v52, v57
	v_mul_f32_e32 v56, v51, v54
	v_mul_f32_e32 v51, 0x3dd2d3e8, v50
	v_fma_f32 v51, -v51, v50, s33
	v_mul_f32_e32 v51, v51, v50
	v_exp_f32_e32 v51, v51
	v_exp_f32_e32 v52, v52
	v_lshlrev_b32_e32 v60, 16, v53
	v_and_b32_e32 v61, 0xffff0000, v53
	v_add_f32_e32 v51, 1.0, v51
	v_rcp_f32_e32 v51, v51
	v_add_f32_e32 v52, 1.0, v52
	v_rcp_f32_e32 v52, v52
	v_mul_f32_e32 v53, 0x3dd2d3e8, v58
	v_mul_f32_e32 v51, v51, v50
	v_mul_f32_e32 v50, 0x3dd2d3e8, v55
	v_fma_f32 v50, -v50, v55, s33
	v_mul_f32_e32 v50, v50, v55
	v_exp_f32_e32 v50, v50
	v_fma_f32 v53, -v53, v58, s33
	v_mul_f32_e32 v54, 0x3dd2d3e8, v59
	v_mul_f32_e32 v53, v53, v58
	v_add_f32_e32 v50, 1.0, v50
	v_rcp_f32_e32 v50, v50
	v_fma_f32 v54, -v54, v59, s33
	v_mul_f32_e32 v52, v52, v57
	v_exp_f32_e32 v53, v53
	v_mul_f32_e32 v50, v50, v55
	v_mul_f32_e32 v55, 0x3dd2d3e8, v60
	v_mul_f32_e32 v54, v54, v59
	v_fma_f32 v55, -v55, v60, s33
	v_mul_f32_e32 v57, 0x3dd2d3e8, v61
	v_exp_f32_e32 v54, v54
	v_mul_f32_e32 v55, v55, v60
	v_fma_f32 v57, -v57, v61, s33
	v_exp_f32_e32 v55, v55
	v_mul_f32_e32 v57, v57, v61
	v_exp_f32_e32 v57, v57
	v_add_f32_e32 v53, 1.0, v53
	v_rcp_f32_e32 v53, v53
	v_add_f32_e32 v54, 1.0, v54
	v_mul_f32_e32 v74, v51, v51
	v_rcp_f32_e32 v54, v54
	v_add_f32_e32 v55, 1.0, v55
	v_fmac_f32_e32 v74, v56, v56
	v_rcp_f32_e32 v55, v55
	v_add_f32_e32 v57, 1.0, v57
	v_fmac_f32_e32 v74, v50, v50
	v_rcp_f32_e32 v57, v57
	v_fmac_f32_e32 v74, v52, v52
	v_mul_f32_e32 v53, v53, v58
	v_fmac_f32_e32 v74, v53, v53
	v_mul_f32_e32 v54, v54, v59
	v_fmac_f32_e32 v74, v54, v54
	v_mul_f32_e32 v55, v55, v60
	v_fmac_f32_e32 v74, v55, v55
	v_mul_f32_e32 v57, v57, v61
	v_fmac_f32_e32 v74, v57, v57
	ds_bpermute_b32 v58, v68, v74
	s_waitcnt lgkmcnt(0)
	v_add_f32_e32 v58, v74, v58
	v_mov_b32_e32 v59, v58
	s_nop 1
	v_permlane16_swap_b32_e32 v59, v58
	s_waitcnt lgkmcnt(0)
	v_add_f32_e32 v58, v58, v59
	s_nop 1
	v_mov_b32_dpp v59, v58 row_ror:8 row_mask:0xf bank_mask:0xf
	s_waitcnt lgkmcnt(0)
	v_add_f32_e32 v58, v58, v59
	s_nop 1
	v_mov_b32_dpp v59, v58 row_shl:4 row_mask:0xf bank_mask:0x5
	v_mov_b32_dpp v59, v58 row_shr:4 row_mask:0xf bank_mask:0xa
	s_waitcnt lgkmcnt(0)
	v_add_f32_e32 v58, v58, v59
	s_nop 1
	v_mov_b32_dpp v59, v58 quad_perm:[2,3,0,1] row_mask:0xf bank_mask:0xf
	s_waitcnt lgkmcnt(0)
	v_add_f32_e32 v58, v58, v59
	s_nop 1
	v_mov_b32_dpp v59, v58 quad_perm:[1,0,3,2] row_mask:0xf bank_mask:0xf
	s_and_saveexec_b64 s[0:1], vcc
	s_cbranch_execz .LBB0_1268
	s_waitcnt lgkmcnt(0)
	v_add_f32_e32 v58, v58, v59
	v_fmamk_f32 v58, v58, 0x3b000000, v246
	s_mov_b32 s2, 0x800000
	v_cmp_gt_f32_e64 s[2:3], s2, v58
	v_mul_f32_e32 v59, 0x4b800000, v58
	s_nop 0
	v_cndmask_b32_e64 v58, v58, v59, s[2:3]
	v_rsq_f32_e32 v58, v58
	s_nop 0
	v_mul_f32_e32 v59, 0x45800000, v58
	v_cndmask_b32_e64 v78, v58, v59, s[2:3]
	v_mul_f32_e32 v50, v50, v78
	v_mul_f32_e32 v56, v56, v78
	v_mul_f32_e32 v51, v51, v78
	v_mul_f32_e32 v50, v50, v162
	v_cvt_pk_bf16_f32 v50, v50, s0
	ds_write_b16 v67, v50 offset:35366
	v_mul_f32_e32 v50, v52, v78
	v_mul_f32_e32 v50, v50, v163
	v_cvt_pk_bf16_f32 v50, v50, s0
	ds_write_b16 v67, v50 offset:35638
	v_mul_f32_e32 v50, v53, v78
	v_mul_f32_e32 v50, v50, v164
	v_cvt_pk_bf16_f32 v50, v50, s0
	ds_write_b16 v67, v50 offset:35910
	v_mul_f32_e32 v50, v54, v78
	v_mul_f32_e32 v50, v50, v165
	v_cvt_pk_bf16_f32 v50, v50, s0
	ds_write_b16 v67, v50 offset:36182
	v_mul_f32_e32 v50, v55, v78
	v_mul_f32_e32 v50, v50, v166
	v_cvt_pk_bf16_f32 v50, v50, s0
	ds_write_b16 v67, v50 offset:36454
	v_mul_f32_e32 v50, v57, v78
	v_mul_f32_e32 v56, v56, v160
	v_mul_f32_e32 v51, v51, v161
	v_mul_f32_e32 v50, v50, v167
	v_cvt_pk_bf16_f32 v56, v56, s0
	v_cvt_pk_bf16_f32 v51, v51, s0
	v_cvt_pk_bf16_f32 v50, v50, s0
	ds_write_b16 v67, v56 offset:34822
	ds_write_b16 v67, v51 offset:35094
	ds_write_b16 v67, v50 offset:36726
; __device__ __forceinline__ float bflo(unsigned w) { return __uint_as_float(w << 16); }
; __device__ __forceinline__ float bfhi(unsigned w) { return __uint_as_float(w & 0xffff0000u); }
; __device__ __forceinline__ unsigned short f2bf(float f) { return (unsigned short)(cvt_pk_bf16(f, 0.f) & 0xffffu); }
; __device__ __forceinline__ void sgu_unit(const Params& p, int l, int un, LAS unsigned char* lds) {
;     ...
;     for (int qi = 0; qi < 16; ++qi) { const int q = wave * 16 + qi;
;         const u32x4 v = vv[qi]; float f[8] = {bflo(v.x), bfhi(v.x), bflo(v.y), bfhi(v.y), bflo(v.z), bfhi(v.z), bflo(v.w), bfhi(v.w)}; float ss = 0.f;
; #pragma unroll
;         for (int j = 0; j < 8; ++j) { f[j] = gelu_tanh(f[j]); ss += f[j] * f[j]; }
;         ss = wave_sum(ss); const float rinv = rsqrtf(ss * (1.0f / 512.0f) + EPS);
;         if ((lane >> 4) == h) { const int c0 = (lane & 15) * 8; const float* g = p.in[I_SGUNG] + l * 512 + h * 128 + c0;
; #pragma unroll
;             for (int j = 0; j < 8; ++j) Vl[(c0 + j) * 136 + q] = f2bf(f[j] * rinv * g[j]); } }
.LBB0_1268:
	s_or_b64 exec, exec, s[0:1]
	s_waitcnt vmcnt(11)
	v_lshlrev_b32_e32 v50, 16, v46
	v_lshlrev_b32_e32 v51, 16, v47
	v_and_b32_e32 v53, 0xffff0000, v47
	v_mul_f32_e32 v47, 0x3dd2d3e8, v50
	v_fma_f32 v47, -v47, v50, s33
	v_mul_f32_e32 v47, v47, v50
	v_exp_f32_e32 v47, v47
	v_and_b32_e32 v46, 0xffff0000, v46
	v_lshlrev_b32_e32 v54, 16, v48
	v_and_b32_e32 v55, 0xffff0000, v48
	v_add_f32_e32 v47, 1.0, v47
	v_rcp_f32_e32 v47, v47
	v_mul_f32_e32 v48, 0x3dd2d3e8, v53
	v_fma_f32 v48, -v48, v53, s33
	v_mul_f32_e32 v48, v48, v53
	v_mul_f32_e32 v52, v47, v50
	v_mul_f32_e32 v47, 0x3dd2d3e8, v46
	v_fma_f32 v47, -v47, v46, s33
	v_mul_f32_e32 v47, v47, v46
	v_exp_f32_e32 v47, v47
	v_exp_f32_e32 v48, v48
	v_lshlrev_b32_e32 v56, 16, v49
	v_and_b32_e32 v57, 0xffff0000, v49
	v_add_f32_e32 v47, 1.0, v47
	v_rcp_f32_e32 v47, v47
	v_add_f32_e32 v48, 1.0, v48
	v_rcp_f32_e32 v48, v48
	v_mul_f32_e32 v49, 0x3dd2d3e8, v54
	v_mul_f32_e32 v47, v47, v46
	v_mul_f32_e32 v46, 0x3dd2d3e8, v51
	v_fma_f32 v46, -v46, v51, s33
	v_mul_f32_e32 v46, v46, v51
	v_exp_f32_e32 v46, v46
	v_fma_f32 v49, -v49, v54, s33
	v_mul_f32_e32 v50, 0x3dd2d3e8, v55
	v_mul_f32_e32 v49, v49, v54
	v_add_f32_e32 v46, 1.0, v46
	v_rcp_f32_e32 v46, v46
	v_fma_f32 v50, -v50, v55, s33
	v_mul_f32_e32 v48, v48, v53
	v_exp_f32_e32 v49, v49
	v_mul_f32_e32 v46, v46, v51
	v_mul_f32_e32 v51, 0x3dd2d3e8, v56
	v_mul_f32_e32 v50, v50, v55
	v_fma_f32 v51, -v51, v56, s33
	v_mul_f32_e32 v53, 0x3dd2d3e8, v57
	v_exp_f32_e32 v50, v50
	v_mul_f32_e32 v51, v51, v56
	v_fma_f32 v53, -v53, v57, s33
	v_exp_f32_e32 v51, v51
	v_mul_f32_e32 v53, v53, v57
	v_exp_f32_e32 v53, v53
	v_add_f32_e32 v49, 1.0, v49
	v_rcp_f32_e32 v49, v49
	v_add_f32_e32 v50, 1.0, v50
	v_mul_f32_e32 v58, v47, v47
	v_rcp_f32_e32 v50, v50
	v_add_f32_e32 v51, 1.0, v51
	v_fmac_f32_e32 v58, v52, v52
	v_rcp_f32_e32 v51, v51
	v_add_f32_e32 v53, 1.0, v53
	v_fmac_f32_e32 v58, v46, v46
	v_rcp_f32_e32 v53, v53
	v_fmac_f32_e32 v58, v48, v48
	v_mul_f32_e32 v49, v49, v54
	v_fmac_f32_e32 v58, v49, v49
	v_mul_f32_e32 v50, v50, v55
	v_fmac_f32_e32 v58, v50, v50
	v_mul_f32_e32 v51, v51, v56
	v_fmac_f32_e32 v58, v51, v51
	v_mul_f32_e32 v53, v53, v57
	v_fmac_f32_e32 v58, v53, v53
	ds_bpermute_b32 v54, v68, v58
	s_waitcnt lgkmcnt(0)
	v_add_f32_e32 v54, v58, v54
	v_mov_b32_e32 v55, v54
	s_nop 1
	v_permlane16_swap_b32_e32 v55, v54
	s_waitcnt lgkmcnt(0)
	v_add_f32_e32 v54, v54, v55
	s_nop 1
	v_mov_b32_dpp v55, v54 row_ror:8 row_mask:0xf bank_mask:0xf
	s_waitcnt lgkmcnt(0)
	v_add_f32_e32 v54, v54, v55
	s_nop 1
	v_mov_b32_dpp v55, v54 row_shl:4 row_mask:0xf bank_mask:0x5
	v_mov_b32_dpp v55, v54 row_shr:4 row_mask:0xf bank_mask:0xa
	s_waitcnt lgkmcnt(0)
	v_add_f32_e32 v54, v54, v55
	s_nop 1
	v_mov_b32_dpp v55, v54 quad_perm:[2,3,0,1] row_mask:0xf bank_mask:0xf
	s_waitcnt lgkmcnt(0)
	v_add_f32_e32 v54, v54, v55
	s_nop 1
	v_mov_b32_dpp v55, v54 quad_perm:[1,0,3,2] row_mask:0xf bank_mask:0xf
	s_and_saveexec_b64 s[0:1], vcc
	s_cbranch_execz .LBB0_1270
	s_waitcnt lgkmcnt(0)
	v_add_f32_e32 v54, v54, v55
	v_fmamk_f32 v54, v54, 0x3b000000, v246
	s_mov_b32 s2, 0x800000
	v_cmp_gt_f32_e64 s[2:3], s2, v54
	v_mul_f32_e32 v55, 0x4b800000, v54
	s_nop 0
	v_cndmask_b32_e64 v54, v54, v55, s[2:3]
	v_rsq_f32_e32 v54, v54
	s_nop 0
	v_mul_f32_e32 v55, 0x45800000, v54
	v_cndmask_b32_e64 v74, v54, v55, s[2:3]
	v_mul_f32_e32 v46, v46, v74
	v_mul_f32_e32 v52, v52, v74
	v_mul_f32_e32 v47, v47, v74
	v_mul_f32_e32 v46, v46, v162
	v_cvt_pk_bf16_f32 v46, v46, s0
	ds_write_b16 v67, v46 offset:35368
	v_mul_f32_e32 v46, v48, v74
	v_mul_f32_e32 v46, v46, v163
	v_cvt_pk_bf16_f32 v46, v46, s0
	ds_write_b16 v67, v46 offset:35640
	v_mul_f32_e32 v46, v49, v74
	v_mul_f32_e32 v46, v46, v164
	v_cvt_pk_bf16_f32 v46, v46, s0
	ds_write_b16 v67, v46 offset:35912
	v_mul_f32_e32 v46, v50, v74
	v_mul_f32_e32 v46, v46, v165
	v_cvt_pk_bf16_f32 v46, v46, s0
	ds_write_b16 v67, v46 offset:36184
	v_mul_f32_e32 v46, v51, v74
	v_mul_f32_e32 v46, v46, v166
	v_cvt_pk_bf16_f32 v46, v46, s0
	ds_write_b16 v67, v46 offset:36456
	v_mul_f32_e32 v46, v53, v74
	v_mul_f32_e32 v52, v52, v160
	v_mul_f32_e32 v47, v47, v161
	v_mul_f32_e32 v46, v46, v167
	v_cvt_pk_bf16_f32 v52, v52, s0
	v_cvt_pk_bf16_f32 v47, v47, s0
	v_cvt_pk_bf16_f32 v46, v46, s0
	ds_write_b16 v67, v52 offset:34824
	ds_write_b16 v67, v47 offset:35096
	ds_write_b16 v67, v46 offset:36728

; __device__ __forceinline__ void sgu_unit(const Params& p, int l, int un, LAS unsigned char* lds) {
;     ...
;     const float* Wg = p.in[I_SGUW] + ((size_t)l * 4 + h) * 128 * 128;
;     f32x4 wq[8]; u32x4 vv[16];
; #pragma unroll
;     for (int i = 0; i < 8; ++i) wq[i] = *(const f32x4*)(Wg + (i * 512 + tid) * 4);
; #pragma unroll
;     for (int qi = 0; qi < 16; ++qi) vv[qi] = *(const u32x4*)(P + (size_t)(row0 + wave * 16 + qi) * INP + C_SGU_V + lane * 8);
; __global__ void __launch_bounds__(512, 2) fwd(Params p) {
;     ...
;             if (c < (l == 0 ? 72 : 64) || G != 256) pg8::gemm_phase(lds, pg8::Desc{512, 512, 512}, S, E);
;             else { const int un = (l == 0 ? 128 + (c - 72) : 160 + (c - 64)); if (un < (l == 0 ? B_SGU : 256)) sgu_unit(p, l, un, lds); }
.LBB0_1393:
	s_andn2_b64 vcc, exec, s[0:1]
	s_cbranch_vccnz .LBB0_1501
	v_readlane_b32 s0, v252, 5
	v_readlane_b32 s1, v252, 6
	s_lshl_b32 s4, s0, 9
	v_readlane_b32 s0, v252, 20
	v_readlane_b32 s1, v252, 21
	s_and_b64 s[0:1], s[0:1], exec
	s_cselect_b32 s0, 0x48, 64
	s_cmp_ge_i32 s92, s0
	v_readlane_b32 s12, v255, 40
	s_cselect_b64 s[2:3], -1, 0
	v_readlane_b32 s13, v255, 41
	s_and_b64 s[2:3], s[12:13], s[2:3]
	s_mov_b64 s[0:1], -1
	s_and_b64 vcc, exec, s[2:3]
	s_cbranch_vccz .LBB0_1430
	v_readlane_b32 s2, v252, 20
	v_readlane_b32 s3, v252, 21
	s_and_b64 s[0:1], s[2:3], exec
	s_cselect_b32 s0, 56, 0x60
	s_add_i32 s0, s0, s92
	s_and_b64 s[2:3], s[2:3], exec
	s_movk_i32 s1, 0x120
	s_cselect_b32 s1, s1, 0x100
	s_cmp_ge_u32 s0, s1
	s_cbranch_scc1 .LBB0_1429
	v_readlane_b32 s44, v251, 16
	s_lshl_b32 s12, s0, 5
	v_readlane_b32 s0, v253, 39
	v_readlane_b32 s48, v251, 20
	v_readlane_b32 s49, v251, 21
	s_or_b32 s40, s4, s0
	s_mov_b32 s41, s5
	v_readlane_b32 s50, v251, 22
	v_readlane_b32 s51, v251, 23
	v_readlane_b32 s52, v251, 24
	v_readlane_b32 s53, v251, 25
	v_readlane_b32 s54, v251, 26
	v_readlane_b32 s55, v251, 27
	s_mov_b64 s[16:17], s[48:49]
	s_lshl_b64 s[0:1], s[40:41], 9
	s_mov_b64 s[18:19], s[50:51]
	s_waitcnt vmcnt(0)
	v_mov_b32_e32 v64, v0
	s_add_u32 s2, s18, s0
	s_addc_u32 s3, s19, s1
	v_lshlrev_b32_e32 v2, 2, v64
	v_ashrrev_i32_e32 v3, 31, v2
	v_add_u32_e32 v62, 0x800, v2
	s_mov_b64 s[14:15], 0
	v_lshl_add_u64 v[4:5], v[2:3], 2, s[2:3]
	v_ashrrev_i32_e32 v63, 31, v62
	v_lshl_add_u64 v[6:7], v[62:63], 2, s[2:3]
	global_load_dwordx4 v[66:69], v[4:5], off
	global_load_dwordx4 v[70:73], v[6:7], off
	v_add_u32_e32 v102, 0x1000, v2
	v_ashrrev_i32_e32 v103, 31, v102
	v_add_u32_e32 v104, 0x1800, v2
	v_lshl_add_u64 v[4:5], v[102:103], 2, s[2:3]
	v_ashrrev_i32_e32 v105, 31, v104
	v_lshl_add_u64 v[6:7], v[104:105], 2, s[2:3]
	global_load_dwordx4 v[74:77], v[4:5], off
	global_load_dwordx4 v[78:81], v[6:7], off
	s_and_b32 s12, s12, 0x7fffff80
	s_lshl_b64 s[0:1], s[4:5], 2
	v_readlane_b32 s13, v253, 41
	v_add_u32_e32 v106, 0x2000, v2
	s_add_u32 s0, s13, s0
	v_readlane_b32 s13, v253, 42
	v_ashrrev_i32_e32 v107, 31, v106
	v_add_u32_e32 v108, 0x2800, v2
	s_addc_u32 s1, s13, s1
	v_lshl_add_u64 v[4:5], v[106:107], 2, s[2:3]
	v_ashrrev_i32_e32 v109, 31, v108
	s_add_u32 s36, s84, s14
	v_lshl_add_u64 v[6:7], v[108:109], 2, s[2:3]
	global_load_dwordx4 v[82:85], v[4:5], off
	global_load_dwordx4 v[86:89], v[6:7], off
	s_addc_u32 s37, s85, s15
	v_add_u32_e32 v110, 0x3000, v2
	v_add_u32_e32 v112, 0x3800, v2
	s_add_u32 s38, s36, 0x1f1b8000
	v_ashrrev_i32_e32 v111, 31, v110
	v_ashrrev_i32_e32 v113, 31, v112
	v_ashrrev_i32_e32 v103, 6, v64
	s_addc_u32 s39, s37, 0
	v_lshl_add_u64 v[4:5], v[110:111], 2, s[2:3]
	v_lshl_add_u64 v[2:3], v[112:113], 2, s[2:3]
	v_lshlrev_b32_e32 v65, 4, v103
	v_and_b32_e32 v8, 63, v64
	global_load_dwordx4 v[90:93], v[4:5], off
	global_load_dwordx4 v[94:97], v[2:3], off
	v_add_u32_e32 v9, s12, v65
	v_mov_b64_e32 v[2:3], s[38:39]
	s_movk_i32 s13, 0x1e00
	v_mad_i64_i32 v[4:5], s[2:3], v9, s13, v[2:3]
	v_lshlrev_b32_e32 v206, 4, v8
	v_or_b32_e32 v6, 1, v9
	v_lshl_add_u64 v[4:5], v[4:5], 0, v[206:207]
	v_mad_i64_i32 v[6:7], s[2:3], v6, s13, v[2:3]
	v_lshl_add_u64 v[6:7], v[6:7], 0, v[206:207]
	global_load_dwordx4 v[98:101], v[4:5], off offset:1024
	global_load_dwordx4 v[58:61], v[6:7], off offset:1024
	v_or_b32_e32 v4, 2, v9
	v_or_b32_e32 v6, 3, v9
	v_mad_i64_i32 v[4:5], s[2:3], v4, s13, v[2:3]
	v_mad_i64_i32 v[6:7], s[2:3], v6, s13, v[2:3]
	v_lshl_add_u64 v[4:5], v[4:5], 0, v[206:207]
	v_lshl_add_u64 v[6:7], v[6:7], 0, v[206:207]
	global_load_dwordx4 v[54:57], v[4:5], off offset:1024
	global_load_dwordx4 v[50:53], v[6:7], off offset:1024
	v_or_b32_e32 v4, 4, v9
	v_or_b32_e32 v6, 5, v9
	v_mad_i64_i32 v[4:5], s[2:3], v4, s13, v[2:3]
	v_mad_i64_i32 v[6:7], s[2:3], v6, s13, v[2:3]
	v_lshl_add_u64 v[4:5], v[4:5], 0, v[206:207]
	v_lshl_add_u64 v[6:7], v[6:7], 0, v[206:207]
	global_load_dwordx4 v[46:49], v[4:5], off offset:1024
	global_load_dwordx4 v[42:45], v[6:7], off offset:1024
	v_or_b32_e32 v4, 6, v9
	v_or_b32_e32 v6, 7, v9
	v_mad_i64_i32 v[4:5], s[2:3], v4, s13, v[2:3]
	v_mad_i64_i32 v[6:7], s[2:3], v6, s13, v[2:3]
	v_lshl_add_u64 v[4:5], v[4:5], 0, v[206:207]
	v_lshl_add_u64 v[6:7], v[6:7], 0, v[206:207]
	global_load_dwordx4 v[38:41], v[4:5], off offset:1024
	global_load_dwordx4 v[34:37], v[6:7], off offset:1024
	v_or_b32_e32 v4, 8, v9
	v_or_b32_e32 v6, 9, v9
	v_mad_i64_i32 v[4:5], s[2:3], v4, s13, v[2:3]
	v_mad_i64_i32 v[6:7], s[2:3], v6, s13, v[2:3]
	v_lshl_add_u64 v[4:5], v[4:5], 0, v[206:207]
	v_lshl_add_u64 v[6:7], v[6:7], 0, v[206:207]
	global_load_dwordx4 v[30:33], v[4:5], off offset:1024
	global_load_dwordx4 v[26:29], v[6:7], off offset:1024
	v_or_b32_e32 v4, 10, v9
	v_or_b32_e32 v6, 11, v9
	v_mad_i64_i32 v[4:5], s[2:3], v4, s13, v[2:3]
	v_mad_i64_i32 v[6:7], s[2:3], v6, s13, v[2:3]
	v_lshl_add_u64 v[4:5], v[4:5], 0, v[206:207]
	v_lshl_add_u64 v[6:7], v[6:7], 0, v[206:207]
	global_load_dwordx4 v[22:25], v[4:5], off offset:1024
	global_load_dwordx4 v[18:21], v[6:7], off offset:1024
	v_or_b32_e32 v4, 12, v9
	v_or_b32_e32 v6, 13, v9
	v_mad_i64_i32 v[4:5], s[2:3], v4, s13, v[2:3]
	v_mad_i64_i32 v[6:7], s[2:3], v6, s13, v[2:3]
	v_lshl_add_u64 v[4:5], v[4:5], 0, v[206:207]
	v_lshl_add_u64 v[6:7], v[6:7], 0, v[206:207]
	v_lshlrev_b32_e32 v105, 3, v64
	global_load_dwordx4 v[14:17], v[4:5], off offset:1024
	global_load_dwordx4 v[10:13], v[6:7], off offset:1024
	v_or_b32_e32 v4, 14, v9
	v_or_b32_e32 v6, 15, v9
	v_and_b32_e32 v63, 0xf8, v105
	v_mad_i64_i32 v[4:5], s[2:3], v4, s13, v[2:3]
	v_mad_i64_i32 v[2:3], s[2:3], v6, s13, v[2:3]
	v_add_u32_e32 v114, 0, v63
	v_bfe_i32 v63, v64, 5, 25
	s_movk_i32 s13, 0x110
	v_lshl_add_u64 v[4:5], v[4:5], 0, v[206:207]
	v_lshl_add_u64 v[2:3], v[2:3], 0, v[206:207]
	s_waitcnt vmcnt(21)
; #define LAS __attribute__((address_space(3)))
; __device__ __forceinline__ unsigned cvt_pk_bf16(float lo, float hi) { const f32x2 v = {lo, hi}; const bf16x2_t b = __builtin_convertvector(v, bf16x2_t); return __builtin_bit_cast(unsigned, b); }
; __device__ __forceinline__ float bflo(unsigned w) { return __uint_as_float(w << 16); }
; __device__ __forceinline__ float bfhi(unsigned w) { return __uint_as_float(w & 0xffff0000u); }
; __device__ __forceinline__ void sgu_unit(const Params& p, int l, int un, LAS unsigned char* lds) {
;     ...
;     for (int i = 0; i < 8; ++i) { const int e4 = (i * 512 + tid) * 4, r = e4 >> 7, c = e4 & 127; const f32x4 v = wq[i];
;         u32x2 w; w.x = cvt_pk_bf16(v[0], v[1]); w.y = cvt_pk_bf16(v[2], v[3]); *(LAS u32x2*)(Wl + r * 136 + c) = w; }
; #pragma unroll
;     for (int qi = 0; qi < 16; ++qi) { const int q = wave * 16 + qi;
;         const u32x4 v = vv[qi]; float f[8] = {bflo(v.x), bfhi(v.x), bflo(v.y), bfhi(v.y), bflo(v.z), bfhi(v.z), bflo(v.w), bfhi(v.w)}; float ss = 0.f;
; #pragma unroll
;         for (int j = 0; j < 8; ++j) { f[j] = gelu_tanh(f[j]); ss += f[j] * f[j]; }
;         ss = wave_sum(ss); const float rinv = rsqrtf(ss * (1.0f / 512.0f) + EPS);
	v_cvt_pk_bf16_f32 v66, v66, v67
	v_cvt_pk_bf16_f32 v67, v68, v69
	v_mad_u64_u32 v[68:69], s[2:3], v63, s13, v[114:115]
	global_load_dwordx4 v[6:9], v[4:5], off offset:1024
	s_nop 0
	global_load_dwordx4 v[2:5], v[2:3], off offset:1024
	ds_write_b64 v68, v[66:67]
	v_ashrrev_i32_e32 v66, 7, v62
	s_waitcnt vmcnt(22)
	v_cvt_pk_bf16_f32 v62, v70, v71
	v_cvt_pk_bf16_f32 v63, v72, v73
	v_mad_u64_u32 v[66:67], s[2:3], v66, s13, v[114:115]
	ds_write_b64 v66, v[62:63]
	v_ashrrev_i32_e32 v66, 7, v102
	s_waitcnt vmcnt(21)
	v_cvt_pk_bf16_f32 v62, v74, v75
	v_cvt_pk_bf16_f32 v63, v76, v77
	v_mad_u64_u32 v[66:67], s[2:3], v66, s13, v[114:115]
	ds_write_b64 v66, v[62:63]
	v_ashrrev_i32_e32 v66, 7, v104
	s_waitcnt vmcnt(20)
	v_cvt_pk_bf16_f32 v62, v78, v79
	v_cvt_pk_bf16_f32 v63, v80, v81
	v_mad_u64_u32 v[66:67], s[2:3], v66, s13, v[114:115]
	ds_write_b64 v66, v[62:63]
	v_ashrrev_i32_e32 v66, 7, v106
	s_waitcnt vmcnt(19)
	v_cvt_pk_bf16_f32 v62, v82, v83
	v_cvt_pk_bf16_f32 v63, v84, v85
	v_mad_u64_u32 v[66:67], s[2:3], v66, s13, v[114:115]
	ds_write_b64 v66, v[62:63]
	v_ashrrev_i32_e32 v66, 7, v108
	s_waitcnt vmcnt(18)
	v_cvt_pk_bf16_f32 v62, v86, v87
	v_cvt_pk_bf16_f32 v63, v88, v89
	v_mad_u64_u32 v[66:67], s[2:3], v66, s13, v[114:115]
	ds_write_b64 v66, v[62:63]
	v_ashrrev_i32_e32 v66, 7, v110
	s_waitcnt vmcnt(17)
	v_cvt_pk_bf16_f32 v62, v90, v91
	v_cvt_pk_bf16_f32 v63, v92, v93
	v_mad_u64_u32 v[66:67], s[2:3], v66, s13, v[114:115]
	ds_write_b64 v66, v[62:63]
	v_ashrrev_i32_e32 v66, 7, v112
	v_mad_u64_u32 v[66:67], s[2:3], v66, s13, v[114:115]
	s_waitcnt vmcnt(15)
	v_and_b32_e32 v67, 0xffff0000, v98
	v_mul_f32_e32 v73, 0x3dd2d3e8, v67
	v_fma_f32 v73, -v73, v67, s33
	v_mul_f32_e32 v73, v73, v67
	v_exp_f32_e32 v73, v73
	v_cvt_pk_bf16_f32 v62, v94, v95
	v_cvt_pk_bf16_f32 v63, v96, v97
	ds_write_b64 v66, v[62:63]
	v_lshlrev_b32_e32 v66, 16, v98
	v_add_f32_e32 v73, 1.0, v73
	v_mul_f32_e32 v72, 0x3dd2d3e8, v66
	v_rcp_f32_e32 v73, v73
	v_fma_f32 v72, -v72, v66, s33
	v_mul_f32_e32 v72, v72, v66
	v_lshlrev_b32_e32 v69, 16, v99
	v_exp_f32_e32 v72, v72
	v_mul_f32_e32 v79, v73, v67
	v_mul_f32_e32 v67, 0x3dd2d3e8, v69
	v_fma_f32 v67, -v67, v69, s33
	v_mul_f32_e32 v67, v67, v69
	v_add_f32_e32 v72, 1.0, v72
	v_exp_f32_e32 v67, v67
	v_rcp_f32_e32 v72, v72
	v_lshlrev_b32_e32 v71, 16, v100
	v_and_b32_e32 v70, 0xffff0000, v99
	v_add_f32_e32 v67, 1.0, v67
	v_mul_f32_e32 v73, 0x3dd2d3e8, v71
	v_mul_f32_e32 v81, v72, v66
	v_mul_f32_e32 v72, 0x3dd2d3e8, v70
	v_rcp_f32_e32 v67, v67
	v_fma_f32 v73, -v73, v71, s33
	v_fma_f32 v72, -v72, v70, s33
	v_mul_f32_e32 v73, v73, v71
	v_mul_f32_e32 v72, v72, v70
	v_exp_f32_e32 v73, v73
	v_and_b32_e32 v74, 0xffff0000, v100
	v_exp_f32_e32 v72, v72
	v_mul_f32_e32 v80, v67, v69
	v_mul_f32_e32 v69, 0x3dd2d3e8, v74
	v_fma_f32 v69, -v69, v74, s33
	v_add_f32_e32 v67, 1.0, v73
	v_mul_f32_e32 v69, v69, v74
	v_add_f32_e32 v72, 1.0, v72
	v_rcp_f32_e32 v67, v67
	v_exp_f32_e32 v69, v69
	v_rcp_f32_e32 v72, v72
	v_lshlrev_b32_e32 v75, 16, v101
	v_and_b32_e32 v82, 0xffff0000, v101
	v_mul_f32_e32 v76, v67, v71
	v_add_f32_e32 v67, 1.0, v69
	v_mul_f32_e32 v69, 0x3dd2d3e8, v75
	v_mul_f32_e32 v78, v72, v70
	v_fma_f32 v69, -v69, v75, s33
	v_mul_f32_e32 v70, 0x3dd2d3e8, v82
	v_mul_f32_e32 v69, v69, v75
	v_fma_f32 v70, -v70, v82, s33
	v_rcp_f32_e32 v67, v67
	v_exp_f32_e32 v69, v69
	v_mul_f32_e32 v70, v70, v82
	v_exp_f32_e32 v70, v70
	v_mul_f32_e32 v66, v79, v79
	v_mul_f32_e32 v77, v67, v74
	v_add_f32_e32 v67, 1.0, v69
	v_fmac_f32_e32 v66, v81, v81
	v_rcp_f32_e32 v67, v67
	v_add_f32_e32 v69, 1.0, v70
	v_fmac_f32_e32 v66, v80, v80
	v_rcp_f32_e32 v69, v69
	v_and_b32_e32 v62, 64, v249
	v_fmac_f32_e32 v66, v78, v78
	v_add_u32_e32 v62, 64, v62
	v_xor_b32_e32 v63, 32, v249
	v_fmac_f32_e32 v66, v76, v76
	v_cmp_lt_i32_e32 vcc, v63, v62
	v_fmac_f32_e32 v66, v77, v77
	v_mul_f32_e32 v75, v67, v75
	v_cndmask_b32_e32 v63, v249, v63, vcc
	v_fmac_f32_e32 v66, v75, v75
	v_mul_f32_e32 v74, v69, v82
	v_lshlrev_b32_e32 v68, 2, v63
	v_fmac_f32_e32 v66, v74, v74
	v_mov_b32_e32 v67, v66
	s_nop 1
	v_permlane32_swap_b32_e32 v67, v66
	v_xor_b32_e32 v63, 16, v249
	v_cmp_lt_i32_e32 vcc, v63, v62
	v_and_b32_e32 v84, 0x78, v105
	v_readlane_b32 s2, v253, 40
	v_cndmask_b32_e32 v63, v249, v63, vcc
	v_lshlrev_b32_e32 v69, 2, v63
	s_waitcnt lgkmcnt(0)
	v_add_f32_e32 v66, v66, v67
	v_mov_b32_e32 v67, v66
	s_nop 1
	v_permlane16_swap_b32_e32 v67, v66
	v_xor_b32_e32 v63, 8, v249
	v_cmp_lt_i32_e32 vcc, v63, v62
	v_lshlrev_b32_e32 v206, 2, v84
	v_readlane_b32 s45, v251, 17
	v_cndmask_b32_e32 v63, v249, v63, vcc
	v_lshlrev_b32_e32 v70, 2, v63
	s_waitcnt lgkmcnt(0)
	v_add_f32_e32 v66, v66, v67
	s_nop 1
	v_mov_b32_dpp v67, v66 row_ror:8 row_mask:0xf bank_mask:0xf
	v_xor_b32_e32 v63, 4, v249
	v_cmp_lt_i32_e32 vcc, v63, v62
	v_readlane_b32 s46, v251, 18
	v_readlane_b32 s47, v251, 19
	v_cndmask_b32_e32 v63, v249, v63, vcc
	v_lshlrev_b32_e32 v71, 2, v63
	s_waitcnt lgkmcnt(0)
	v_add_f32_e32 v66, v66, v67
	v_xor_b32_e32 v63, 2, v249
	s_nop 1
	v_mov_b32_dpp v67, v66 row_shl:4 row_mask:0xf bank_mask:0x5
	v_mov_b32_dpp v67, v66 row_shr:4 row_mask:0xf bank_mask:0xa
	v_cmp_lt_i32_e32 vcc, v63, v62
	v_readlane_b32 s56, v251, 28
	v_readlane_b32 s57, v251, 29
	v_cndmask_b32_e32 v63, v249, v63, vcc
	v_lshlrev_b32_e32 v72, 2, v63
	v_xor_b32_e32 v63, 1, v249
	v_cmp_lt_i32_e32 vcc, v63, v62
	v_readlane_b32 s58, v251, 30
	v_readlane_b32 s59, v251, 31
	v_cndmask_b32_e32 v62, v249, v63, vcc
	s_waitcnt lgkmcnt(0)
	v_add_f32_e32 v63, v66, v67
	s_nop 1
	v_mov_b32_dpp v67, v63 quad_perm:[2,3,0,1] row_mask:0xf bank_mask:0xf
	v_lshlrev_b32_e32 v73, 2, v62
	v_bfe_u32 v66, v64, 4, 2
	v_cmp_eq_u32_e32 vcc, s2, v66
	s_mov_b64 s[20:21], s[52:53]
	s_waitcnt lgkmcnt(0)
	v_add_f32_e32 v82, v63, v67
	s_nop 1
	v_mov_b32_dpp v83, v82 quad_perm:[1,0,3,2] row_mask:0xf bank_mask:0xf
	v_lshl_add_u32 v67, v103, 5, 0
	v_lshl_add_u64 v[62:63], s[0:1], 0, v[206:207]
	v_mad_u32_u24 v67, v84, s13, v67
	s_mov_b64 s[22:23], s[54:55]
	s_and_saveexec_b64 s[0:1], vcc
	s_cbranch_execz .LBB0_1398
; __device__ __forceinline__ float bflo(unsigned w) { return __uint_as_float(w << 16); }
; __device__ __forceinline__ float bfhi(unsigned w) { return __uint_as_float(w & 0xffff0000u); }
; __device__ __forceinline__ unsigned short f2bf(float f) { return (unsigned short)(cvt_pk_bf16(f, 0.f) & 0xffffu); }
; __device__ __forceinline__ void sgu_unit(const Params& p, int l, int un, LAS unsigned char* lds) {
;     ...
;     for (int qi = 0; qi < 16; ++qi) { const int q = wave * 16 + qi;
;         const u32x4 v = vv[qi]; float f[8] = {bflo(v.x), bfhi(v.x), bflo(v.y), bfhi(v.y), bflo(v.z), bfhi(v.z), bflo(v.w), bfhi(v.w)}; float ss = 0.f;
; #pragma unroll
;         for (int j = 0; j < 8; ++j) { f[j] = gelu_tanh(f[j]); ss += f[j] * f[j]; }
;         ss = wave_sum(ss); const float rinv = rsqrtf(ss * (1.0f / 512.0f) + EPS);
;         if ((lane >> 4) == h) { const int c0 = (lane & 15) * 8; const float* g = p.in[I_SGUNG] + l * 512 + h * 128 + c0;
; #pragma unroll
;             for (int j = 0; j < 8; ++j) Vl[(c0 + j) * 136 + q] = f2bf(f[j] * rinv * g[j]); } }
	s_waitcnt lgkmcnt(0)
	v_add_f32_e32 v82, v82, v83
	v_fmamk_f32 v82, v82, 0x3b000000, v246
	s_mov_b32 s2, 0x800000
	v_cmp_gt_f32_e64 s[2:3], s2, v82
	v_mul_f32_e32 v83, 0x4b800000, v82
	s_nop 0
	v_cndmask_b32_e64 v82, v82, v83, s[2:3]
	v_rsq_f32_e32 v82, v82
	s_nop 0
	v_mul_f32_e32 v83, 0x45800000, v82
	v_cndmask_b32_e64 v90, v82, v83, s[2:3]
	global_load_dwordx4 v[82:85], v[62:63], off offset:16
	global_load_dwordx4 v[86:89], v[62:63], off
	v_mul_f32_e32 v79, v79, v90
	v_mul_f32_e32 v76, v76, v90
	v_mul_f32_e32 v81, v81, v90
	v_mul_f32_e32 v78, v78, v90
	v_mul_f32_e32 v75, v75, v90
	v_mul_f32_e32 v74, v74, v90
	s_waitcnt vmcnt(1)
	v_mul_f32_e32 v76, v76, v82
	s_waitcnt vmcnt(0)
	v_mov_b32_e32 v160, v86
	v_mov_b32_e32 v161, v87
	v_mov_b32_e32 v162, v88
	v_mov_b32_e32 v163, v89
	v_mov_b32_e32 v164, v82
	v_mov_b32_e32 v165, v83
	v_mov_b32_e32 v166, v84
	v_mov_b32_e32 v167, v85
	v_mul_f32_e32 v79, v79, v87
	v_cvt_pk_bf16_f32 v79, v79, s0
	v_cvt_pk_bf16_f32 v76, v76, s0
	ds_write_b16 v67, v79 offset:35088
	v_mul_f32_e32 v79, v80, v90
	ds_write_b16 v67, v76 offset:35904
	v_mul_f32_e32 v76, v77, v90
	v_mul_f32_e32 v81, v81, v86
	v_mul_f32_e32 v79, v79, v88
	v_mul_f32_e32 v78, v78, v89
	v_mul_f32_e32 v76, v76, v83
	v_mul_f32_e32 v75, v75, v84
	v_mul_f32_e32 v74, v74, v85
	v_cvt_pk_bf16_f32 v81, v81, s0
	v_cvt_pk_bf16_f32 v79, v79, s0
	v_cvt_pk_bf16_f32 v78, v78, s0
	v_cvt_pk_bf16_f32 v76, v76, s0
	v_cvt_pk_bf16_f32 v75, v75, s0
	v_cvt_pk_bf16_f32 v74, v74, s0
	ds_write_b16 v67, v81 offset:34816
	ds_write_b16 v67, v79 offset:35360
	ds_write_b16 v67, v78 offset:35632
	ds_write_b16 v67, v76 offset:36176
	ds_write_b16 v67, v75 offset:36448
	ds_write_b16 v67, v74 offset:36720
